# speedup vs baseline: 1.0079x; 1.0079x over previous
_Z10scan_pass1PKDF16_S0_PKfS0_S2_S2_PDF16_PfS4_S2_S3_:
	s_load_dwordx16 s[8:23], s[0:1], 0x0
	s_load_dwordx4 s[24:27], s[0:1], 0x40
	s_load_dwordx2 s[28:29], s[0:1], 0x50
	s_mov_b32 s64, 0x3d800000
	s_mov_b32 s65, 0x3fb8aa3b
	s_mov_b32 s66, 0x3f317218
	s_mov_b32 s84, 0x40800000
	s_mov_b32 s86, 0x41800000
	s_lshl_b32 s5, s4, 11
	s_lshl_b32 s6, s3, 5
	s_add_i32 s5, s5, s6
	s_lshl_b32 s6, s4, 6
	s_add_i32 s6, s6, s3
	v_lshl_or_b32 v1, s2, 8, v0
	v_and_b32_e32 v127, 63, v0
	v_lshlrev_b32_e32 v127, 4, v127
	v_lshrrev_b32_e32 v98, 6, v0
	v_lshl_or_b32 v98, v98, 13, v127
	v_add_u32_e32 v99, 0x1000, v98
	v_lshlrev_b32_e32 v126, 4, v1
	v_lshlrev_b32_e32 v114, 2, v1
	v_lshlrev_b32_e32 v115, 6, v1
	v_lshlrev_b32_e32 v116, 5, v0
	s_waitcnt lgkmcnt(0)
	s_lshl_b32 s7, s5, 7
	s_add_u32 s70, s16, s7
	s_addc_u32 s71, s17, 0
	s_load_dwordx16 s[32:47], s[70:71], 0x0
	s_lshl_b32 s7, s6, 12
	s_add_u32 s74, s8, s7
	s_addc_u32 s75, s9, 0
	global_load_dwordx4 v[82:85], v127, s[74:75]
	global_load_dwordx4 v[86:89], v127, s[74:75] offset:1024
	global_load_dwordx4 v[90:93], v127, s[74:75] offset:2048
	global_load_dwordx4 v[94:97], v127, s[74:75] offset:3072
	s_lshl_b32 s7, s2, 15
	s_add_u32 s74, s10, s7
	s_addc_u32 s75, s11, 0
	global_load_dwordx4 v[18:21], v99, s[74:75]
	global_load_dwordx4 v[22:25], v99, s[74:75] offset:1024
	global_load_dwordx4 v[26:29], v99, s[74:75] offset:2048
	global_load_dwordx4 v[30:33], v99, s[74:75] offset:3072
	global_load_dwordx4 v[102:105], v98, s[74:75] offset:1024
	global_load_dwordx4 v[106:109], v98, s[74:75] offset:2048
	global_load_dwordx4 v[110:113], v98, s[74:75] offset:3072
	global_load_dwordx4 v[98:101], v98, s[74:75]
	global_load_dword v122, v114, s[12:13]
	global_load_dwordx4 v[2:5], v115, s[18:19]
	global_load_dwordx4 v[6:9], v115, s[18:19] offset:16
	global_load_dwordx4 v[10:13], v115, s[18:19] offset:32
	global_load_dwordx4 v[14:17], v115, s[18:19] offset:48
	s_lshr_b32 s7, s5, 3
	s_lshl_b32 s7, s7, 15
	s_add_u32 s74, s14, s7
	s_addc_u32 s75, s15, 0
	global_load_dwordx4 v[66:69], v126, s[74:75]
	s_add_u32 s74, s74, 0x8000
	s_addc_u32 s75, s75, 0
	global_load_dwordx4 v[70:73], v126, s[74:75]
	s_add_u32 s74, s74, 0x8000
	s_addc_u32 s75, s75, 0
	global_load_dwordx4 v[74:77], v126, s[74:75]
	s_add_u32 s74, s74, 0x8000
	s_addc_u32 s75, s75, 0
	global_load_dwordx4 v[78:81], v126, s[74:75]
	s_lshl_b32 s7, s6, 3
	s_add_i32 s7, s7, s2
	s_lshl_b32 s4, s7, 13
	s_add_u32 s74, s26, s4
	s_addc_u32 s75, s27, 0
	s_lshl_b32 s4, s7, 12
	s_add_u32 s80, s28, s4
	s_addc_u32 s81, s29, 0
	global_load_dwordx4 v[118:121], v116, s[74:75] nt
	global_load_dwordx4 v[114:117], v116, s[74:75] offset:16 nt
	s_lshr_b32 s7, s5, 2
	s_lshl_b32 s7, s7, 15
	s_add_u32 s72, s24, s7
	s_addc_u32 s73, s25, 0
	s_lshl_b32 s7, s6, 16
	s_add_u32 s76, s20, s7
	s_addc_u32 s77, s21, 0
	s_lshl_b32 s7, s6, 13
	s_add_u32 s78, s22, s7
	s_addc_u32 s79, s23, 0
	s_waitcnt vmcnt(11)
	v_mfma_f32_32x32x16_f16 v[34:49], v[82:85], v[98:101], 0
	v_mfma_f32_32x32x16_f16 v[50:65], v[82:85], v[18:21], 0
	v_mfma_f32_32x32x16_f16 v[34:49], v[86:89], v[102:105], v[34:49]
	v_mfma_f32_32x32x16_f16 v[50:65], v[86:89], v[22:25], v[50:65]
	v_mfma_f32_32x32x16_f16 v[34:49], v[90:93], v[106:109], v[34:49]
	v_mfma_f32_32x32x16_f16 v[50:65], v[90:93], v[26:29], v[50:65]
	v_mfma_f32_32x32x16_f16 v[34:49], v[94:97], v[110:113], v[34:49]
	v_mfma_f32_32x32x16_f16 v[50:65], v[94:97], v[30:33], v[50:65]
	v_mov_b32_e32 v123, 0
	s_nop 15
	s_nop 3
	v_permlane32_swap_b32_e32 v34, v50
	v_permlane32_swap_b32_e32 v35, v51
	v_permlane32_swap_b32_e32 v36, v52
	v_permlane32_swap_b32_e32 v37, v53
	v_permlane32_swap_b32_e32 v38, v54
	v_permlane32_swap_b32_e32 v39, v55
	v_permlane32_swap_b32_e32 v40, v56
	v_permlane32_swap_b32_e32 v41, v57
	v_permlane32_swap_b32_e32 v42, v58
	v_permlane32_swap_b32_e32 v43, v59
	v_permlane32_swap_b32_e32 v44, v60
	v_permlane32_swap_b32_e32 v45, v61
	v_permlane32_swap_b32_e32 v46, v62
	v_permlane32_swap_b32_e32 v47, v63
	v_permlane32_swap_b32_e32 v48, v64
	v_permlane32_swap_b32_e32 v49, v65
	s_waitcnt vmcnt(5)
	v_fma_f32 v98, v34, s64, v122
	v_mul_f32_e64 v99, -|v98|, s65
	v_cvt_f32_f16_e32 v125, v66
	v_exp_f32_e32 v99, v99
	v_max_f32_e32 v98, 0, v98
	v_add_f32_e32 v99, 1.0, v99
	v_log_f32_e32 v99, v99
	s_nop 0
	v_fma_f32 v82, v99, s66, v98
	v_add_f32_e32 v123, v123, v82
	v_mul_f32_e32 v124, v82, v125
	s_waitcnt lgkmcnt(0)
	s_load_dwordx16 s[48:63], s[70:71], 0x80
	v_fma_f32 v98, v35, s64, v122
	v_mul_f32_e64 v99, -|v98|, s65
	v_cvt_f32_f16_sdwa v125, v66 dst_sel:DWORD dst_unused:UNUSED_PAD src0_sel:WORD_1
	v_exp_f32_e32 v99, v99
	v_max_f32_e32 v98, 0, v98
	v_add_f32_e32 v99, 1.0, v99
	v_log_f32_e32 v99, v99
	v_pk_mul_f32 v[18:19], v[124:125], s[32:33] op_sel_hi:[0,1]
	v_fma_f32 v83, v99, s66, v98
	v_add_f32_e32 v123, v123, v83
	v_pk_mul_f32 v[20:21], v[124:125], s[34:35] op_sel_hi:[0,1]
	v_pk_mul_f32 v[22:23], v[124:125], s[36:37] op_sel_hi:[0,1]
	v_pk_mul_f32 v[24:25], v[124:125], s[38:39] op_sel_hi:[0,1]
	v_pk_mul_f32 v[26:27], v[124:125], s[40:41] op_sel_hi:[0,1]
	v_pk_mul_f32 v[28:29], v[124:125], s[42:43] op_sel_hi:[0,1]
	v_pk_mul_f32 v[30:31], v[124:125], s[44:45] op_sel_hi:[0,1]
	v_pk_mul_f32 v[32:33], v[124:125], s[46:47] op_sel_hi:[0,1]
	v_mul_f32_e32 v124, v83, v125
	s_waitcnt lgkmcnt(0)
	s_load_dwordx16 s[32:47], s[70:71], 0x100
	v_fma_f32 v98, v36, s64, v122
	v_mul_f32_e64 v99, -|v98|, s65
	v_cvt_f32_f16_e32 v125, v67
	v_exp_f32_e32 v99, v99
	v_max_f32_e32 v98, 0, v98
	v_add_f32_e32 v99, 1.0, v99
	v_log_f32_e32 v99, v99
	v_pk_mul_f32 v[90:91], v[82:83], v[2:3] op_sel:[1,0]
	v_fma_f32 v84, v99, s66, v98
	v_add_f32_e32 v123, v123, v84
	v_exp_f32_e32 v90, v90
	v_exp_f32_e32 v91, v91
	v_pk_mul_f32 v[92:93], v[82:83], v[4:5] op_sel:[1,0]
	v_pk_mul_f32 v[90:91], v[18:19], v[90:91]
	v_exp_f32_e32 v92, v92
	v_pk_fma_f32 v[18:19], v[124:125], s[48:49], v[90:91] op_sel_hi:[0,1,1]
	v_exp_f32_e32 v93, v93
	v_pk_mul_f32 v[94:95], v[82:83], v[6:7] op_sel:[1,0]
	v_pk_mul_f32 v[92:93], v[20:21], v[92:93]
	v_exp_f32_e32 v94, v94
	v_pk_fma_f32 v[20:21], v[124:125], s[50:51], v[92:93] op_sel_hi:[0,1,1]
	v_exp_f32_e32 v95, v95
	v_pk_mul_f32 v[96:97], v[82:83], v[8:9] op_sel:[1,0]
	v_pk_mul_f32 v[94:95], v[22:23], v[94:95]
	v_exp_f32_e32 v96, v96
	v_pk_fma_f32 v[22:23], v[124:125], s[52:53], v[94:95] op_sel_hi:[0,1,1]
	v_exp_f32_e32 v97, v97
	v_pk_mul_f32 v[90:91], v[82:83], v[10:11] op_sel:[1,0]
	v_pk_mul_f32 v[96:97], v[24:25], v[96:97]
	v_exp_f32_e32 v90, v90
	v_pk_fma_f32 v[24:25], v[124:125], s[54:55], v[96:97] op_sel_hi:[0,1,1]
	v_exp_f32_e32 v91, v91
	v_pk_mul_f32 v[92:93], v[82:83], v[12:13] op_sel:[1,0]
	v_pk_mul_f32 v[90:91], v[26:27], v[90:91]
	v_exp_f32_e32 v92, v92
	v_pk_fma_f32 v[26:27], v[124:125], s[56:57], v[90:91] op_sel_hi:[0,1,1]
	v_exp_f32_e32 v93, v93
	v_pk_mul_f32 v[94:95], v[82:83], v[14:15] op_sel:[1,0]
	v_pk_mul_f32 v[92:93], v[28:29], v[92:93]
	v_exp_f32_e32 v94, v94
	v_pk_fma_f32 v[28:29], v[124:125], s[58:59], v[92:93] op_sel_hi:[0,1,1]
	v_exp_f32_e32 v95, v95
	v_pk_mul_f32 v[96:97], v[82:83], v[16:17] op_sel:[1,0]
	v_pk_mul_f32 v[94:95], v[30:31], v[94:95]
	v_exp_f32_e32 v96, v96
	v_pk_fma_f32 v[30:31], v[124:125], s[60:61], v[94:95] op_sel_hi:[0,1,1]
	v_exp_f32_e32 v97, v97
	s_nop 0
	v_pk_mul_f32 v[96:97], v[32:33], v[96:97]
	s_nop 0
	v_pk_fma_f32 v[32:33], v[124:125], s[62:63], v[96:97] op_sel_hi:[0,1,1]
	v_mul_f32_e32 v124, v84, v125
	s_waitcnt lgkmcnt(0)
	s_load_dwordx16 s[48:63], s[70:71], 0x180
	v_fma_f32 v98, v37, s64, v122
	v_mul_f32_e64 v99, -|v98|, s65
	v_cvt_f32_f16_sdwa v125, v67 dst_sel:DWORD dst_unused:UNUSED_PAD src0_sel:WORD_1
	v_exp_f32_e32 v99, v99
	v_max_f32_e32 v98, 0, v98
	v_add_f32_e32 v99, 1.0, v99
	v_log_f32_e32 v99, v99
	v_pk_mul_f32 v[90:91], v[84:85], v[2:3] op_sel_hi:[0,1]
	v_fma_f32 v85, v99, s66, v98
	v_add_f32_e32 v123, v123, v85
	v_exp_f32_e32 v90, v90
	v_exp_f32_e32 v91, v91
	v_pk_mul_f32 v[92:93], v[84:85], v[4:5] op_sel_hi:[0,1]
	v_pk_mul_f32 v[90:91], v[18:19], v[90:91]
	v_exp_f32_e32 v92, v92
	v_pk_fma_f32 v[18:19], v[124:125], s[32:33], v[90:91] op_sel_hi:[0,1,1]
	v_exp_f32_e32 v93, v93
	v_pk_mul_f32 v[94:95], v[84:85], v[6:7] op_sel_hi:[0,1]
	v_pk_mul_f32 v[92:93], v[20:21], v[92:93]
	v_exp_f32_e32 v94, v94
	v_pk_fma_f32 v[20:21], v[124:125], s[34:35], v[92:93] op_sel_hi:[0,1,1]
	v_exp_f32_e32 v95, v95
	v_pk_mul_f32 v[96:97], v[84:85], v[8:9] op_sel_hi:[0,1]
	v_pk_mul_f32 v[94:95], v[22:23], v[94:95]
	v_exp_f32_e32 v96, v96
	v_pk_fma_f32 v[22:23], v[124:125], s[36:37], v[94:95] op_sel_hi:[0,1,1]
	v_exp_f32_e32 v97, v97
	v_pk_mul_f32 v[90:91], v[84:85], v[10:11] op_sel_hi:[0,1]
	v_pk_mul_f32 v[96:97], v[24:25], v[96:97]
	v_exp_f32_e32 v90, v90
	v_pk_fma_f32 v[24:25], v[124:125], s[38:39], v[96:97] op_sel_hi:[0,1,1]
	v_exp_f32_e32 v91, v91
	v_pk_mul_f32 v[92:93], v[84:85], v[12:13] op_sel_hi:[0,1]
	v_pk_mul_f32 v[90:91], v[26:27], v[90:91]
	v_exp_f32_e32 v92, v92
	v_pk_fma_f32 v[26:27], v[124:125], s[40:41], v[90:91] op_sel_hi:[0,1,1]
	v_exp_f32_e32 v93, v93
	v_pk_mul_f32 v[94:95], v[84:85], v[14:15] op_sel_hi:[0,1]
	v_pk_mul_f32 v[92:93], v[28:29], v[92:93]
	v_exp_f32_e32 v94, v94
	v_pk_fma_f32 v[28:29], v[124:125], s[42:43], v[92:93] op_sel_hi:[0,1,1]
	v_exp_f32_e32 v95, v95
	v_pk_mul_f32 v[96:97], v[84:85], v[16:17] op_sel_hi:[0,1]
	v_pk_mul_f32 v[94:95], v[30:31], v[94:95]
	v_exp_f32_e32 v96, v96
	v_pk_fma_f32 v[30:31], v[124:125], s[44:45], v[94:95] op_sel_hi:[0,1,1]
	v_exp_f32_e32 v97, v97
	s_nop 0
	v_pk_mul_f32 v[96:97], v[32:33], v[96:97]
	s_nop 0
	v_pk_fma_f32 v[32:33], v[124:125], s[46:47], v[96:97] op_sel_hi:[0,1,1]
	v_mul_f32_e32 v124, v85, v125
	s_waitcnt lgkmcnt(0)
	s_load_dwordx16 s[32:47], s[70:71], 0x200
	v_fma_f32 v98, v50, s64, v122
	v_mul_f32_e64 v99, -|v98|, s65
	v_cvt_f32_f16_e32 v125, v68
	v_exp_f32_e32 v99, v99
	v_max_f32_e32 v98, 0, v98
	v_add_f32_e32 v99, 1.0, v99
	v_log_f32_e32 v99, v99
	v_pk_mul_f32 v[90:91], v[84:85], v[2:3] op_sel:[1,0]
	v_fma_f32 v86, v99, s66, v98
	v_add_f32_e32 v123, v123, v86
	v_exp_f32_e32 v90, v90
	v_exp_f32_e32 v91, v91
	v_pk_mul_f32 v[92:93], v[84:85], v[4:5] op_sel:[1,0]
	v_pk_mul_f32 v[90:91], v[18:19], v[90:91]
	v_exp_f32_e32 v92, v92
	v_pk_fma_f32 v[18:19], v[124:125], s[48:49], v[90:91] op_sel_hi:[0,1,1]
	v_exp_f32_e32 v93, v93
	v_pk_mul_f32 v[94:95], v[84:85], v[6:7] op_sel:[1,0]
	v_pk_mul_f32 v[92:93], v[20:21], v[92:93]
	v_exp_f32_e32 v94, v94
	v_pk_fma_f32 v[20:21], v[124:125], s[50:51], v[92:93] op_sel_hi:[0,1,1]
	v_exp_f32_e32 v95, v95
	v_pk_mul_f32 v[96:97], v[84:85], v[8:9] op_sel:[1,0]
	v_pk_mul_f32 v[94:95], v[22:23], v[94:95]
	v_exp_f32_e32 v96, v96
	v_pk_fma_f32 v[22:23], v[124:125], s[52:53], v[94:95] op_sel_hi:[0,1,1]
	v_exp_f32_e32 v97, v97
	v_pk_mul_f32 v[90:91], v[84:85], v[10:11] op_sel:[1,0]
	v_pk_mul_f32 v[96:97], v[24:25], v[96:97]
	v_exp_f32_e32 v90, v90
	v_pk_fma_f32 v[24:25], v[124:125], s[54:55], v[96:97] op_sel_hi:[0,1,1]
	v_exp_f32_e32 v91, v91
	v_pk_mul_f32 v[92:93], v[84:85], v[12:13] op_sel:[1,0]
	v_pk_mul_f32 v[90:91], v[26:27], v[90:91]
	v_exp_f32_e32 v92, v92
	v_pk_fma_f32 v[26:27], v[124:125], s[56:57], v[90:91] op_sel_hi:[0,1,1]
	v_exp_f32_e32 v93, v93
	v_pk_mul_f32 v[94:95], v[84:85], v[14:15] op_sel:[1,0]
	v_pk_mul_f32 v[92:93], v[28:29], v[92:93]
	v_exp_f32_e32 v94, v94
	v_pk_fma_f32 v[28:29], v[124:125], s[58:59], v[92:93] op_sel_hi:[0,1,1]
	v_exp_f32_e32 v95, v95
	v_pk_mul_f32 v[96:97], v[84:85], v[16:17] op_sel:[1,0]
	v_pk_mul_f32 v[94:95], v[30:31], v[94:95]
	v_exp_f32_e32 v96, v96
	v_pk_fma_f32 v[30:31], v[124:125], s[60:61], v[94:95] op_sel_hi:[0,1,1]
	v_exp_f32_e32 v97, v97
	s_nop 0
	v_pk_mul_f32 v[96:97], v[32:33], v[96:97]
	s_nop 0
	v_pk_fma_f32 v[32:33], v[124:125], s[62:63], v[96:97] op_sel_hi:[0,1,1]
	v_mul_f32_e32 v124, v86, v125
	global_store_dwordx4 v126, v[82:85], s[72:73]
	s_add_u32 s72, s72, 0x8000
	s_addc_u32 s73, s73, 0
	s_waitcnt lgkmcnt(0)
	s_load_dwordx16 s[48:63], s[70:71], 0x280
	v_fma_f32 v98, v51, s64, v122
	v_mul_f32_e64 v99, -|v98|, s65
	v_cvt_f32_f16_sdwa v125, v68 dst_sel:DWORD dst_unused:UNUSED_PAD src0_sel:WORD_1
	v_exp_f32_e32 v99, v99
	v_max_f32_e32 v98, 0, v98
	v_add_f32_e32 v99, 1.0, v99
	v_log_f32_e32 v99, v99
	v_pk_mul_f32 v[90:91], v[86:87], v[2:3] op_sel_hi:[0,1]
	v_fma_f32 v87, v99, s66, v98
	v_add_f32_e32 v123, v123, v87
	v_exp_f32_e32 v90, v90
	v_exp_f32_e32 v91, v91
	v_pk_mul_f32 v[92:93], v[86:87], v[4:5] op_sel_hi:[0,1]
	v_pk_mul_f32 v[90:91], v[18:19], v[90:91]
	v_exp_f32_e32 v92, v92
	v_pk_fma_f32 v[18:19], v[124:125], s[32:33], v[90:91] op_sel_hi:[0,1,1]
	v_exp_f32_e32 v93, v93
	v_pk_mul_f32 v[94:95], v[86:87], v[6:7] op_sel_hi:[0,1]
	v_pk_mul_f32 v[92:93], v[20:21], v[92:93]
	v_exp_f32_e32 v94, v94
	v_pk_fma_f32 v[20:21], v[124:125], s[34:35], v[92:93] op_sel_hi:[0,1,1]
	v_exp_f32_e32 v95, v95
	v_pk_mul_f32 v[96:97], v[86:87], v[8:9] op_sel_hi:[0,1]
	v_pk_mul_f32 v[94:95], v[22:23], v[94:95]
	v_exp_f32_e32 v96, v96
	v_pk_fma_f32 v[22:23], v[124:125], s[36:37], v[94:95] op_sel_hi:[0,1,1]
	v_exp_f32_e32 v97, v97
	v_pk_mul_f32 v[90:91], v[86:87], v[10:11] op_sel_hi:[0,1]
	v_pk_mul_f32 v[96:97], v[24:25], v[96:97]
	v_exp_f32_e32 v90, v90
	v_pk_fma_f32 v[24:25], v[124:125], s[38:39], v[96:97] op_sel_hi:[0,1,1]
	v_exp_f32_e32 v91, v91
	v_pk_mul_f32 v[92:93], v[86:87], v[12:13] op_sel_hi:[0,1]
	v_pk_mul_f32 v[90:91], v[26:27], v[90:91]
	v_exp_f32_e32 v92, v92
	v_pk_fma_f32 v[26:27], v[124:125], s[40:41], v[90:91] op_sel_hi:[0,1,1]
	v_exp_f32_e32 v93, v93
	v_pk_mul_f32 v[94:95], v[86:87], v[14:15] op_sel_hi:[0,1]
	v_pk_mul_f32 v[92:93], v[28:29], v[92:93]
	v_exp_f32_e32 v94, v94
	v_pk_fma_f32 v[28:29], v[124:125], s[42:43], v[92:93] op_sel_hi:[0,1,1]
	v_exp_f32_e32 v95, v95
	v_pk_mul_f32 v[96:97], v[86:87], v[16:17] op_sel_hi:[0,1]
	v_pk_mul_f32 v[94:95], v[30:31], v[94:95]
	v_exp_f32_e32 v96, v96
	v_pk_fma_f32 v[30:31], v[124:125], s[44:45], v[94:95] op_sel_hi:[0,1,1]
	v_exp_f32_e32 v97, v97
	s_nop 0
	v_pk_mul_f32 v[96:97], v[32:33], v[96:97]
	s_nop 0
	v_pk_fma_f32 v[32:33], v[124:125], s[46:47], v[96:97] op_sel_hi:[0,1,1]
	v_mul_f32_e32 v124, v87, v125
	s_waitcnt lgkmcnt(0)
	s_load_dwordx16 s[32:47], s[70:71], 0x300
	v_fma_f32 v98, v52, s64, v122
	v_mul_f32_e64 v99, -|v98|, s65
	v_cvt_f32_f16_e32 v125, v69
	v_exp_f32_e32 v99, v99
	v_max_f32_e32 v98, 0, v98
	v_add_f32_e32 v99, 1.0, v99
	v_log_f32_e32 v99, v99
	v_pk_mul_f32 v[90:91], v[86:87], v[2:3] op_sel:[1,0]
	v_fma_f32 v88, v99, s66, v98
	v_add_f32_e32 v123, v123, v88
	v_exp_f32_e32 v90, v90
	v_exp_f32_e32 v91, v91
	v_pk_mul_f32 v[92:93], v[86:87], v[4:5] op_sel:[1,0]
	v_pk_mul_f32 v[90:91], v[18:19], v[90:91]
	v_exp_f32_e32 v92, v92
	v_pk_fma_f32 v[18:19], v[124:125], s[48:49], v[90:91] op_sel_hi:[0,1,1]
	v_exp_f32_e32 v93, v93
	v_pk_mul_f32 v[94:95], v[86:87], v[6:7] op_sel:[1,0]
	v_pk_mul_f32 v[92:93], v[20:21], v[92:93]
	v_exp_f32_e32 v94, v94
	v_pk_fma_f32 v[20:21], v[124:125], s[50:51], v[92:93] op_sel_hi:[0,1,1]
	v_exp_f32_e32 v95, v95
	v_pk_mul_f32 v[96:97], v[86:87], v[8:9] op_sel:[1,0]
	v_pk_mul_f32 v[94:95], v[22:23], v[94:95]
	v_exp_f32_e32 v96, v96
	v_pk_fma_f32 v[22:23], v[124:125], s[52:53], v[94:95] op_sel_hi:[0,1,1]
	v_exp_f32_e32 v97, v97
	v_pk_mul_f32 v[90:91], v[86:87], v[10:11] op_sel:[1,0]
	v_pk_mul_f32 v[96:97], v[24:25], v[96:97]
	v_exp_f32_e32 v90, v90
	v_pk_fma_f32 v[24:25], v[124:125], s[54:55], v[96:97] op_sel_hi:[0,1,1]
	v_exp_f32_e32 v91, v91
	v_pk_mul_f32 v[92:93], v[86:87], v[12:13] op_sel:[1,0]
	v_pk_mul_f32 v[90:91], v[26:27], v[90:91]
	v_exp_f32_e32 v92, v92
	v_pk_fma_f32 v[26:27], v[124:125], s[56:57], v[90:91] op_sel_hi:[0,1,1]
	v_exp_f32_e32 v93, v93
	v_pk_mul_f32 v[94:95], v[86:87], v[14:15] op_sel:[1,0]
	v_pk_mul_f32 v[92:93], v[28:29], v[92:93]
	v_exp_f32_e32 v94, v94
	v_pk_fma_f32 v[28:29], v[124:125], s[58:59], v[92:93] op_sel_hi:[0,1,1]
	v_exp_f32_e32 v95, v95
	v_pk_mul_f32 v[96:97], v[86:87], v[16:17] op_sel:[1,0]
	v_pk_mul_f32 v[94:95], v[30:31], v[94:95]
	v_exp_f32_e32 v96, v96
	v_pk_fma_f32 v[30:31], v[124:125], s[60:61], v[94:95] op_sel_hi:[0,1,1]
	v_exp_f32_e32 v97, v97
	s_nop 0
	v_pk_mul_f32 v[96:97], v[32:33], v[96:97]
	s_nop 0
	v_pk_fma_f32 v[32:33], v[124:125], s[62:63], v[96:97] op_sel_hi:[0,1,1]
	v_mul_f32_e32 v124, v88, v125
	s_waitcnt lgkmcnt(0)
	s_load_dwordx16 s[48:63], s[70:71], 0x380
	v_fma_f32 v98, v53, s64, v122
	v_mul_f32_e64 v99, -|v98|, s65
	v_cvt_f32_f16_sdwa v125, v69 dst_sel:DWORD dst_unused:UNUSED_PAD src0_sel:WORD_1
	v_exp_f32_e32 v99, v99
	v_max_f32_e32 v98, 0, v98
	v_add_f32_e32 v99, 1.0, v99
	v_log_f32_e32 v99, v99
	v_pk_mul_f32 v[90:91], v[88:89], v[2:3] op_sel_hi:[0,1]
	v_fma_f32 v89, v99, s66, v98
	v_add_f32_e32 v123, v123, v89
	v_exp_f32_e32 v90, v90
	v_exp_f32_e32 v91, v91
	v_pk_mul_f32 v[92:93], v[88:89], v[4:5] op_sel_hi:[0,1]
	v_pk_mul_f32 v[90:91], v[18:19], v[90:91]
	v_exp_f32_e32 v92, v92
	v_pk_fma_f32 v[18:19], v[124:125], s[32:33], v[90:91] op_sel_hi:[0,1,1]
	v_exp_f32_e32 v93, v93
	v_pk_mul_f32 v[94:95], v[88:89], v[6:7] op_sel_hi:[0,1]
	v_pk_mul_f32 v[92:93], v[20:21], v[92:93]
	v_exp_f32_e32 v94, v94
	v_pk_fma_f32 v[20:21], v[124:125], s[34:35], v[92:93] op_sel_hi:[0,1,1]
	v_exp_f32_e32 v95, v95
	v_pk_mul_f32 v[96:97], v[88:89], v[8:9] op_sel_hi:[0,1]
	v_pk_mul_f32 v[94:95], v[22:23], v[94:95]
	v_exp_f32_e32 v96, v96
	v_pk_fma_f32 v[22:23], v[124:125], s[36:37], v[94:95] op_sel_hi:[0,1,1]
	v_exp_f32_e32 v97, v97
	v_pk_mul_f32 v[90:91], v[88:89], v[10:11] op_sel_hi:[0,1]
	v_pk_mul_f32 v[96:97], v[24:25], v[96:97]
	v_exp_f32_e32 v90, v90
	v_pk_fma_f32 v[24:25], v[124:125], s[38:39], v[96:97] op_sel_hi:[0,1,1]
	v_exp_f32_e32 v91, v91
	v_pk_mul_f32 v[92:93], v[88:89], v[12:13] op_sel_hi:[0,1]
	v_pk_mul_f32 v[90:91], v[26:27], v[90:91]
	v_exp_f32_e32 v92, v92
	v_pk_fma_f32 v[26:27], v[124:125], s[40:41], v[90:91] op_sel_hi:[0,1,1]
	v_exp_f32_e32 v93, v93
	v_pk_mul_f32 v[94:95], v[88:89], v[14:15] op_sel_hi:[0,1]
	v_pk_mul_f32 v[92:93], v[28:29], v[92:93]
	v_exp_f32_e32 v94, v94
	v_pk_fma_f32 v[28:29], v[124:125], s[42:43], v[92:93] op_sel_hi:[0,1,1]
	v_exp_f32_e32 v95, v95
	v_pk_mul_f32 v[96:97], v[88:89], v[16:17] op_sel_hi:[0,1]
	v_pk_mul_f32 v[94:95], v[30:31], v[94:95]
	v_exp_f32_e32 v96, v96
	v_pk_fma_f32 v[30:31], v[124:125], s[44:45], v[94:95] op_sel_hi:[0,1,1]
	v_exp_f32_e32 v97, v97
	s_nop 0
	v_pk_mul_f32 v[96:97], v[32:33], v[96:97]
	s_nop 0
	v_pk_fma_f32 v[32:33], v[124:125], s[46:47], v[96:97] op_sel_hi:[0,1,1]
	v_mul_f32_e32 v124, v89, v125
	s_waitcnt vmcnt(5)
	s_waitcnt lgkmcnt(0)
	s_load_dwordx16 s[32:47], s[70:71], 0x400
	v_fma_f32 v98, v38, s64, v122
	v_mul_f32_e64 v99, -|v98|, s65
	v_cvt_f32_f16_e32 v125, v70
	v_exp_f32_e32 v99, v99
	v_max_f32_e32 v98, 0, v98
	v_add_f32_e32 v99, 1.0, v99
	v_log_f32_e32 v99, v99
	v_pk_mul_f32 v[90:91], v[88:89], v[2:3] op_sel:[1,0]
	v_fma_f32 v82, v99, s66, v98
	v_add_f32_e32 v123, v123, v82
	v_exp_f32_e32 v90, v90
	v_exp_f32_e32 v91, v91
	v_pk_mul_f32 v[92:93], v[88:89], v[4:5] op_sel:[1,0]
	v_pk_mul_f32 v[90:91], v[18:19], v[90:91]
	v_exp_f32_e32 v92, v92
	v_pk_fma_f32 v[18:19], v[124:125], s[48:49], v[90:91] op_sel_hi:[0,1,1]
	v_exp_f32_e32 v93, v93
	v_pk_mul_f32 v[94:95], v[88:89], v[6:7] op_sel:[1,0]
	v_pk_mul_f32 v[92:93], v[20:21], v[92:93]
	v_exp_f32_e32 v94, v94
	v_pk_fma_f32 v[20:21], v[124:125], s[50:51], v[92:93] op_sel_hi:[0,1,1]
	v_exp_f32_e32 v95, v95
	v_pk_mul_f32 v[96:97], v[88:89], v[8:9] op_sel:[1,0]
	v_pk_mul_f32 v[94:95], v[22:23], v[94:95]
	v_exp_f32_e32 v96, v96
	v_pk_fma_f32 v[22:23], v[124:125], s[52:53], v[94:95] op_sel_hi:[0,1,1]
	v_exp_f32_e32 v97, v97
	v_pk_mul_f32 v[90:91], v[88:89], v[10:11] op_sel:[1,0]
	v_pk_mul_f32 v[96:97], v[24:25], v[96:97]
	v_exp_f32_e32 v90, v90
	v_pk_fma_f32 v[24:25], v[124:125], s[54:55], v[96:97] op_sel_hi:[0,1,1]
	v_exp_f32_e32 v91, v91
	v_pk_mul_f32 v[92:93], v[88:89], v[12:13] op_sel:[1,0]
	v_pk_mul_f32 v[90:91], v[26:27], v[90:91]
	v_exp_f32_e32 v92, v92
	v_pk_fma_f32 v[26:27], v[124:125], s[56:57], v[90:91] op_sel_hi:[0,1,1]
	v_exp_f32_e32 v93, v93
	v_pk_mul_f32 v[94:95], v[88:89], v[14:15] op_sel:[1,0]
	v_pk_mul_f32 v[92:93], v[28:29], v[92:93]
	v_exp_f32_e32 v94, v94
	v_pk_fma_f32 v[28:29], v[124:125], s[58:59], v[92:93] op_sel_hi:[0,1,1]
	v_exp_f32_e32 v95, v95
	v_pk_mul_f32 v[96:97], v[88:89], v[16:17] op_sel:[1,0]
	v_pk_mul_f32 v[94:95], v[30:31], v[94:95]
	v_exp_f32_e32 v96, v96
	v_pk_fma_f32 v[30:31], v[124:125], s[60:61], v[94:95] op_sel_hi:[0,1,1]
	v_exp_f32_e32 v97, v97
	s_nop 0
	v_pk_mul_f32 v[96:97], v[32:33], v[96:97]
	s_nop 0
	v_pk_fma_f32 v[32:33], v[124:125], s[62:63], v[96:97] op_sel_hi:[0,1,1]
	v_mul_f32_e32 v124, v82, v125
	global_store_dwordx4 v126, v[86:89], s[72:73]
	s_add_u32 s72, s72, 0x8000
	s_addc_u32 s73, s73, 0
	s_waitcnt lgkmcnt(0)
	s_load_dwordx16 s[48:63], s[70:71], 0x480
	v_fma_f32 v98, v39, s64, v122
	v_mul_f32_e64 v99, -|v98|, s65
	v_cvt_f32_f16_sdwa v125, v70 dst_sel:DWORD dst_unused:UNUSED_PAD src0_sel:WORD_1
	v_exp_f32_e32 v99, v99
	v_max_f32_e32 v98, 0, v98
	v_add_f32_e32 v99, 1.0, v99
	v_log_f32_e32 v99, v99
	v_pk_mul_f32 v[90:91], v[82:83], v[2:3] op_sel_hi:[0,1]
	v_fma_f32 v83, v99, s66, v98
	v_add_f32_e32 v123, v123, v83
	v_exp_f32_e32 v90, v90
	v_exp_f32_e32 v91, v91
	v_pk_mul_f32 v[92:93], v[82:83], v[4:5] op_sel_hi:[0,1]
	v_pk_mul_f32 v[90:91], v[18:19], v[90:91]
	v_exp_f32_e32 v92, v92
	v_pk_fma_f32 v[18:19], v[124:125], s[32:33], v[90:91] op_sel_hi:[0,1,1]
	v_exp_f32_e32 v93, v93
	v_pk_mul_f32 v[94:95], v[82:83], v[6:7] op_sel_hi:[0,1]
	v_pk_mul_f32 v[92:93], v[20:21], v[92:93]
	v_exp_f32_e32 v94, v94
	v_pk_fma_f32 v[20:21], v[124:125], s[34:35], v[92:93] op_sel_hi:[0,1,1]
	v_exp_f32_e32 v95, v95
	v_pk_mul_f32 v[96:97], v[82:83], v[8:9] op_sel_hi:[0,1]
	v_pk_mul_f32 v[94:95], v[22:23], v[94:95]
	v_exp_f32_e32 v96, v96
	v_pk_fma_f32 v[22:23], v[124:125], s[36:37], v[94:95] op_sel_hi:[0,1,1]
	v_exp_f32_e32 v97, v97
	v_pk_mul_f32 v[90:91], v[82:83], v[10:11] op_sel_hi:[0,1]
	v_pk_mul_f32 v[96:97], v[24:25], v[96:97]
	v_exp_f32_e32 v90, v90
	v_pk_fma_f32 v[24:25], v[124:125], s[38:39], v[96:97] op_sel_hi:[0,1,1]
	v_exp_f32_e32 v91, v91
	v_pk_mul_f32 v[92:93], v[82:83], v[12:13] op_sel_hi:[0,1]
	v_pk_mul_f32 v[90:91], v[26:27], v[90:91]
	v_exp_f32_e32 v92, v92
	v_pk_fma_f32 v[26:27], v[124:125], s[40:41], v[90:91] op_sel_hi:[0,1,1]
	v_exp_f32_e32 v93, v93
	v_pk_mul_f32 v[94:95], v[82:83], v[14:15] op_sel_hi:[0,1]
	v_pk_mul_f32 v[92:93], v[28:29], v[92:93]
	v_exp_f32_e32 v94, v94
	v_pk_fma_f32 v[28:29], v[124:125], s[42:43], v[92:93] op_sel_hi:[0,1,1]
	v_exp_f32_e32 v95, v95
	v_pk_mul_f32 v[96:97], v[82:83], v[16:17] op_sel_hi:[0,1]
	v_pk_mul_f32 v[94:95], v[30:31], v[94:95]
	v_exp_f32_e32 v96, v96
	v_pk_fma_f32 v[30:31], v[124:125], s[44:45], v[94:95] op_sel_hi:[0,1,1]
	v_exp_f32_e32 v97, v97
	s_nop 0
	v_pk_mul_f32 v[96:97], v[32:33], v[96:97]
	s_nop 0
	v_pk_fma_f32 v[32:33], v[124:125], s[46:47], v[96:97] op_sel_hi:[0,1,1]
	v_mul_f32_e32 v124, v83, v125
	s_waitcnt lgkmcnt(0)
	s_load_dwordx16 s[32:47], s[70:71], 0x500
	v_fma_f32 v98, v40, s64, v122
	v_mul_f32_e64 v99, -|v98|, s65
	v_cvt_f32_f16_e32 v125, v71
	v_exp_f32_e32 v99, v99
	v_max_f32_e32 v98, 0, v98
	v_add_f32_e32 v99, 1.0, v99
	v_log_f32_e32 v99, v99
	v_pk_mul_f32 v[90:91], v[82:83], v[2:3] op_sel:[1,0]
	v_fma_f32 v84, v99, s66, v98
	v_add_f32_e32 v123, v123, v84
	v_exp_f32_e32 v90, v90
	v_exp_f32_e32 v91, v91
	v_pk_mul_f32 v[92:93], v[82:83], v[4:5] op_sel:[1,0]
	v_pk_mul_f32 v[90:91], v[18:19], v[90:91]
	v_exp_f32_e32 v92, v92
	v_pk_fma_f32 v[18:19], v[124:125], s[48:49], v[90:91] op_sel_hi:[0,1,1]
	v_exp_f32_e32 v93, v93
	v_pk_mul_f32 v[94:95], v[82:83], v[6:7] op_sel:[1,0]
	v_pk_mul_f32 v[92:93], v[20:21], v[92:93]
	v_exp_f32_e32 v94, v94
	v_pk_fma_f32 v[20:21], v[124:125], s[50:51], v[92:93] op_sel_hi:[0,1,1]
	v_exp_f32_e32 v95, v95
	v_pk_mul_f32 v[96:97], v[82:83], v[8:9] op_sel:[1,0]
	v_pk_mul_f32 v[94:95], v[22:23], v[94:95]
	v_exp_f32_e32 v96, v96
	v_pk_fma_f32 v[22:23], v[124:125], s[52:53], v[94:95] op_sel_hi:[0,1,1]
	v_exp_f32_e32 v97, v97
	v_pk_mul_f32 v[90:91], v[82:83], v[10:11] op_sel:[1,0]
	v_pk_mul_f32 v[96:97], v[24:25], v[96:97]
	v_exp_f32_e32 v90, v90
	v_pk_fma_f32 v[24:25], v[124:125], s[54:55], v[96:97] op_sel_hi:[0,1,1]
	v_exp_f32_e32 v91, v91
	v_pk_mul_f32 v[92:93], v[82:83], v[12:13] op_sel:[1,0]
	v_pk_mul_f32 v[90:91], v[26:27], v[90:91]
	v_exp_f32_e32 v92, v92
	v_pk_fma_f32 v[26:27], v[124:125], s[56:57], v[90:91] op_sel_hi:[0,1,1]
	v_exp_f32_e32 v93, v93
	v_pk_mul_f32 v[94:95], v[82:83], v[14:15] op_sel:[1,0]
	v_pk_mul_f32 v[92:93], v[28:29], v[92:93]
	v_exp_f32_e32 v94, v94
	v_pk_fma_f32 v[28:29], v[124:125], s[58:59], v[92:93] op_sel_hi:[0,1,1]
	v_exp_f32_e32 v95, v95
	v_pk_mul_f32 v[96:97], v[82:83], v[16:17] op_sel:[1,0]
	v_pk_mul_f32 v[94:95], v[30:31], v[94:95]
	v_exp_f32_e32 v96, v96
	v_pk_fma_f32 v[30:31], v[124:125], s[60:61], v[94:95] op_sel_hi:[0,1,1]
	v_exp_f32_e32 v97, v97
	s_nop 0
	v_pk_mul_f32 v[96:97], v[32:33], v[96:97]
	s_nop 0
	v_pk_fma_f32 v[32:33], v[124:125], s[62:63], v[96:97] op_sel_hi:[0,1,1]
	v_mul_f32_e32 v124, v84, v125
	s_waitcnt lgkmcnt(0)
	s_load_dwordx16 s[48:63], s[70:71], 0x580
	v_fma_f32 v98, v41, s64, v122
	v_mul_f32_e64 v99, -|v98|, s65
	v_cvt_f32_f16_sdwa v125, v71 dst_sel:DWORD dst_unused:UNUSED_PAD src0_sel:WORD_1
	v_exp_f32_e32 v99, v99
	v_max_f32_e32 v98, 0, v98
	v_add_f32_e32 v99, 1.0, v99
	v_log_f32_e32 v99, v99
	v_pk_mul_f32 v[90:91], v[84:85], v[2:3] op_sel_hi:[0,1]
	v_fma_f32 v85, v99, s66, v98
	v_add_f32_e32 v123, v123, v85
	v_exp_f32_e32 v90, v90
	v_exp_f32_e32 v91, v91
	v_pk_mul_f32 v[92:93], v[84:85], v[4:5] op_sel_hi:[0,1]
	v_pk_mul_f32 v[90:91], v[18:19], v[90:91]
	v_exp_f32_e32 v92, v92
	v_pk_fma_f32 v[18:19], v[124:125], s[32:33], v[90:91] op_sel_hi:[0,1,1]
	v_exp_f32_e32 v93, v93
	v_pk_mul_f32 v[94:95], v[84:85], v[6:7] op_sel_hi:[0,1]
	v_pk_mul_f32 v[92:93], v[20:21], v[92:93]
	v_exp_f32_e32 v94, v94
	v_pk_fma_f32 v[20:21], v[124:125], s[34:35], v[92:93] op_sel_hi:[0,1,1]
	v_exp_f32_e32 v95, v95
	v_pk_mul_f32 v[96:97], v[84:85], v[8:9] op_sel_hi:[0,1]
	v_pk_mul_f32 v[94:95], v[22:23], v[94:95]
	v_exp_f32_e32 v96, v96
	v_pk_fma_f32 v[22:23], v[124:125], s[36:37], v[94:95] op_sel_hi:[0,1,1]
	v_exp_f32_e32 v97, v97
	v_pk_mul_f32 v[90:91], v[84:85], v[10:11] op_sel_hi:[0,1]
	v_pk_mul_f32 v[96:97], v[24:25], v[96:97]
	v_exp_f32_e32 v90, v90
	v_pk_fma_f32 v[24:25], v[124:125], s[38:39], v[96:97] op_sel_hi:[0,1,1]
	v_exp_f32_e32 v91, v91
	v_pk_mul_f32 v[92:93], v[84:85], v[12:13] op_sel_hi:[0,1]
	v_pk_mul_f32 v[90:91], v[26:27], v[90:91]
	v_exp_f32_e32 v92, v92
	v_pk_fma_f32 v[26:27], v[124:125], s[40:41], v[90:91] op_sel_hi:[0,1,1]
	v_exp_f32_e32 v93, v93
	v_pk_mul_f32 v[94:95], v[84:85], v[14:15] op_sel_hi:[0,1]
	v_pk_mul_f32 v[92:93], v[28:29], v[92:93]
	v_exp_f32_e32 v94, v94
	v_pk_fma_f32 v[28:29], v[124:125], s[42:43], v[92:93] op_sel_hi:[0,1,1]
	v_exp_f32_e32 v95, v95
	v_pk_mul_f32 v[96:97], v[84:85], v[16:17] op_sel_hi:[0,1]
	v_pk_mul_f32 v[94:95], v[30:31], v[94:95]
	v_exp_f32_e32 v96, v96
	v_pk_fma_f32 v[30:31], v[124:125], s[44:45], v[94:95] op_sel_hi:[0,1,1]
	v_exp_f32_e32 v97, v97
	s_nop 0
	v_pk_mul_f32 v[96:97], v[32:33], v[96:97]
	s_nop 0
	v_pk_fma_f32 v[32:33], v[124:125], s[46:47], v[96:97] op_sel_hi:[0,1,1]
	v_mul_f32_e32 v124, v85, v125
	s_waitcnt lgkmcnt(0)
	s_load_dwordx16 s[32:47], s[70:71], 0x600
	v_fma_f32 v98, v54, s64, v122
	v_mul_f32_e64 v99, -|v98|, s65
	v_cvt_f32_f16_e32 v125, v72
	v_exp_f32_e32 v99, v99
	v_max_f32_e32 v98, 0, v98
	v_add_f32_e32 v99, 1.0, v99
	v_log_f32_e32 v99, v99
	v_pk_mul_f32 v[90:91], v[84:85], v[2:3] op_sel:[1,0]
	v_fma_f32 v86, v99, s66, v98
	v_add_f32_e32 v123, v123, v86
	v_exp_f32_e32 v90, v90
	v_exp_f32_e32 v91, v91
	v_pk_mul_f32 v[92:93], v[84:85], v[4:5] op_sel:[1,0]
	v_pk_mul_f32 v[90:91], v[18:19], v[90:91]
	v_exp_f32_e32 v92, v92
	v_pk_fma_f32 v[18:19], v[124:125], s[48:49], v[90:91] op_sel_hi:[0,1,1]
	v_exp_f32_e32 v93, v93
	v_pk_mul_f32 v[94:95], v[84:85], v[6:7] op_sel:[1,0]
	v_pk_mul_f32 v[92:93], v[20:21], v[92:93]
	v_exp_f32_e32 v94, v94
	v_pk_fma_f32 v[20:21], v[124:125], s[50:51], v[92:93] op_sel_hi:[0,1,1]
	v_exp_f32_e32 v95, v95
	v_pk_mul_f32 v[96:97], v[84:85], v[8:9] op_sel:[1,0]
	v_pk_mul_f32 v[94:95], v[22:23], v[94:95]
	v_exp_f32_e32 v96, v96
	v_pk_fma_f32 v[22:23], v[124:125], s[52:53], v[94:95] op_sel_hi:[0,1,1]
	v_exp_f32_e32 v97, v97
	v_pk_mul_f32 v[90:91], v[84:85], v[10:11] op_sel:[1,0]
	v_pk_mul_f32 v[96:97], v[24:25], v[96:97]
	v_exp_f32_e32 v90, v90
	v_pk_fma_f32 v[24:25], v[124:125], s[54:55], v[96:97] op_sel_hi:[0,1,1]
	v_exp_f32_e32 v91, v91
	v_pk_mul_f32 v[92:93], v[84:85], v[12:13] op_sel:[1,0]
	v_pk_mul_f32 v[90:91], v[26:27], v[90:91]
	v_exp_f32_e32 v92, v92
	v_pk_fma_f32 v[26:27], v[124:125], s[56:57], v[90:91] op_sel_hi:[0,1,1]
	v_exp_f32_e32 v93, v93
	v_pk_mul_f32 v[94:95], v[84:85], v[14:15] op_sel:[1,0]
	v_pk_mul_f32 v[92:93], v[28:29], v[92:93]
	v_exp_f32_e32 v94, v94
	v_pk_fma_f32 v[28:29], v[124:125], s[58:59], v[92:93] op_sel_hi:[0,1,1]
	v_exp_f32_e32 v95, v95
	v_pk_mul_f32 v[96:97], v[84:85], v[16:17] op_sel:[1,0]
	v_pk_mul_f32 v[94:95], v[30:31], v[94:95]
	v_exp_f32_e32 v96, v96
	v_pk_fma_f32 v[30:31], v[124:125], s[60:61], v[94:95] op_sel_hi:[0,1,1]
	v_exp_f32_e32 v97, v97
	s_nop 0
	v_pk_mul_f32 v[96:97], v[32:33], v[96:97]
	s_nop 0
	v_pk_fma_f32 v[32:33], v[124:125], s[62:63], v[96:97] op_sel_hi:[0,1,1]
	v_mul_f32_e32 v124, v86, v125
	global_store_dwordx4 v126, v[82:85], s[72:73]
	s_add_u32 s72, s72, 0x8000
	s_addc_u32 s73, s73, 0
	s_waitcnt lgkmcnt(0)
	s_load_dwordx16 s[48:63], s[70:71], 0x680
	v_fma_f32 v98, v55, s64, v122
	v_mul_f32_e64 v99, -|v98|, s65
	v_cvt_f32_f16_sdwa v125, v72 dst_sel:DWORD dst_unused:UNUSED_PAD src0_sel:WORD_1
	v_exp_f32_e32 v99, v99
	v_max_f32_e32 v98, 0, v98
	v_add_f32_e32 v99, 1.0, v99
	v_log_f32_e32 v99, v99
	v_pk_mul_f32 v[90:91], v[86:87], v[2:3] op_sel_hi:[0,1]
	v_fma_f32 v87, v99, s66, v98
	v_add_f32_e32 v123, v123, v87
	v_exp_f32_e32 v90, v90
	v_exp_f32_e32 v91, v91
	v_pk_mul_f32 v[92:93], v[86:87], v[4:5] op_sel_hi:[0,1]
	v_pk_mul_f32 v[90:91], v[18:19], v[90:91]
	v_exp_f32_e32 v92, v92
	v_pk_fma_f32 v[18:19], v[124:125], s[32:33], v[90:91] op_sel_hi:[0,1,1]
	v_exp_f32_e32 v93, v93
	v_pk_mul_f32 v[94:95], v[86:87], v[6:7] op_sel_hi:[0,1]
	v_pk_mul_f32 v[92:93], v[20:21], v[92:93]
	v_exp_f32_e32 v94, v94
	v_pk_fma_f32 v[20:21], v[124:125], s[34:35], v[92:93] op_sel_hi:[0,1,1]
	v_exp_f32_e32 v95, v95
	v_pk_mul_f32 v[96:97], v[86:87], v[8:9] op_sel_hi:[0,1]
	v_pk_mul_f32 v[94:95], v[22:23], v[94:95]
	v_exp_f32_e32 v96, v96
	v_pk_fma_f32 v[22:23], v[124:125], s[36:37], v[94:95] op_sel_hi:[0,1,1]
	v_exp_f32_e32 v97, v97
	v_pk_mul_f32 v[90:91], v[86:87], v[10:11] op_sel_hi:[0,1]
	v_pk_mul_f32 v[96:97], v[24:25], v[96:97]
	v_exp_f32_e32 v90, v90
	v_pk_fma_f32 v[24:25], v[124:125], s[38:39], v[96:97] op_sel_hi:[0,1,1]
	v_exp_f32_e32 v91, v91
	v_pk_mul_f32 v[92:93], v[86:87], v[12:13] op_sel_hi:[0,1]
	v_pk_mul_f32 v[90:91], v[26:27], v[90:91]
	v_exp_f32_e32 v92, v92
	v_pk_fma_f32 v[26:27], v[124:125], s[40:41], v[90:91] op_sel_hi:[0,1,1]
	v_exp_f32_e32 v93, v93
	v_pk_mul_f32 v[94:95], v[86:87], v[14:15] op_sel_hi:[0,1]
	v_pk_mul_f32 v[92:93], v[28:29], v[92:93]
	v_exp_f32_e32 v94, v94
	v_pk_fma_f32 v[28:29], v[124:125], s[42:43], v[92:93] op_sel_hi:[0,1,1]
	v_exp_f32_e32 v95, v95
	v_pk_mul_f32 v[96:97], v[86:87], v[16:17] op_sel_hi:[0,1]
	v_pk_mul_f32 v[94:95], v[30:31], v[94:95]
	v_exp_f32_e32 v96, v96
	v_pk_fma_f32 v[30:31], v[124:125], s[44:45], v[94:95] op_sel_hi:[0,1,1]
	v_exp_f32_e32 v97, v97
	s_nop 0
	v_pk_mul_f32 v[96:97], v[32:33], v[96:97]
	s_nop 0
	v_pk_fma_f32 v[32:33], v[124:125], s[46:47], v[96:97] op_sel_hi:[0,1,1]
	v_mul_f32_e32 v124, v87, v125
	s_waitcnt lgkmcnt(0)
	s_load_dwordx16 s[32:47], s[70:71], 0x700
	v_fma_f32 v98, v56, s64, v122
	v_mul_f32_e64 v99, -|v98|, s65
	v_cvt_f32_f16_e32 v125, v73
	v_exp_f32_e32 v99, v99
	v_max_f32_e32 v98, 0, v98
	v_add_f32_e32 v99, 1.0, v99
	v_log_f32_e32 v99, v99
	v_pk_mul_f32 v[90:91], v[86:87], v[2:3] op_sel:[1,0]
	v_fma_f32 v88, v99, s66, v98
	v_add_f32_e32 v123, v123, v88
	v_exp_f32_e32 v90, v90
	v_exp_f32_e32 v91, v91
	v_pk_mul_f32 v[92:93], v[86:87], v[4:5] op_sel:[1,0]
	v_pk_mul_f32 v[90:91], v[18:19], v[90:91]
	v_exp_f32_e32 v92, v92
	v_pk_fma_f32 v[18:19], v[124:125], s[48:49], v[90:91] op_sel_hi:[0,1,1]
	v_exp_f32_e32 v93, v93
	v_pk_mul_f32 v[94:95], v[86:87], v[6:7] op_sel:[1,0]
	v_pk_mul_f32 v[92:93], v[20:21], v[92:93]
	v_exp_f32_e32 v94, v94
	v_pk_fma_f32 v[20:21], v[124:125], s[50:51], v[92:93] op_sel_hi:[0,1,1]
	v_exp_f32_e32 v95, v95
	v_pk_mul_f32 v[96:97], v[86:87], v[8:9] op_sel:[1,0]
	v_pk_mul_f32 v[94:95], v[22:23], v[94:95]
	v_exp_f32_e32 v96, v96
	v_pk_fma_f32 v[22:23], v[124:125], s[52:53], v[94:95] op_sel_hi:[0,1,1]
	v_exp_f32_e32 v97, v97
	v_pk_mul_f32 v[90:91], v[86:87], v[10:11] op_sel:[1,0]
	v_pk_mul_f32 v[96:97], v[24:25], v[96:97]
	v_exp_f32_e32 v90, v90
	v_pk_fma_f32 v[24:25], v[124:125], s[54:55], v[96:97] op_sel_hi:[0,1,1]
	v_exp_f32_e32 v91, v91
	v_pk_mul_f32 v[92:93], v[86:87], v[12:13] op_sel:[1,0]
	v_pk_mul_f32 v[90:91], v[26:27], v[90:91]
	v_exp_f32_e32 v92, v92
	v_pk_fma_f32 v[26:27], v[124:125], s[56:57], v[90:91] op_sel_hi:[0,1,1]
	v_exp_f32_e32 v93, v93
	v_pk_mul_f32 v[94:95], v[86:87], v[14:15] op_sel:[1,0]
	v_pk_mul_f32 v[92:93], v[28:29], v[92:93]
	v_exp_f32_e32 v94, v94
	v_pk_fma_f32 v[28:29], v[124:125], s[58:59], v[92:93] op_sel_hi:[0,1,1]
	v_exp_f32_e32 v95, v95
	v_pk_mul_f32 v[96:97], v[86:87], v[16:17] op_sel:[1,0]
	v_pk_mul_f32 v[94:95], v[30:31], v[94:95]
	v_exp_f32_e32 v96, v96
	v_pk_fma_f32 v[30:31], v[124:125], s[60:61], v[94:95] op_sel_hi:[0,1,1]
	v_exp_f32_e32 v97, v97
	s_nop 0
	v_pk_mul_f32 v[96:97], v[32:33], v[96:97]
	s_nop 0
	v_pk_fma_f32 v[32:33], v[124:125], s[62:63], v[96:97] op_sel_hi:[0,1,1]
	v_mul_f32_e32 v124, v88, v125
	s_waitcnt lgkmcnt(0)
	s_load_dwordx16 s[48:63], s[70:71], 0x780
	v_fma_f32 v98, v57, s64, v122
	v_mul_f32_e64 v99, -|v98|, s65
	v_cvt_f32_f16_sdwa v125, v73 dst_sel:DWORD dst_unused:UNUSED_PAD src0_sel:WORD_1
	v_exp_f32_e32 v99, v99
	v_max_f32_e32 v98, 0, v98
	v_add_f32_e32 v99, 1.0, v99
	v_log_f32_e32 v99, v99
	v_pk_mul_f32 v[90:91], v[88:89], v[2:3] op_sel_hi:[0,1]
	v_fma_f32 v89, v99, s66, v98
	v_add_f32_e32 v123, v123, v89
	v_exp_f32_e32 v90, v90
	v_exp_f32_e32 v91, v91
	v_pk_mul_f32 v[92:93], v[88:89], v[4:5] op_sel_hi:[0,1]
	v_pk_mul_f32 v[90:91], v[18:19], v[90:91]
	v_exp_f32_e32 v92, v92
	v_pk_fma_f32 v[18:19], v[124:125], s[32:33], v[90:91] op_sel_hi:[0,1,1]
	v_exp_f32_e32 v93, v93
	v_pk_mul_f32 v[94:95], v[88:89], v[6:7] op_sel_hi:[0,1]
	v_pk_mul_f32 v[92:93], v[20:21], v[92:93]
	v_exp_f32_e32 v94, v94
	v_pk_fma_f32 v[20:21], v[124:125], s[34:35], v[92:93] op_sel_hi:[0,1,1]
	v_exp_f32_e32 v95, v95
	v_pk_mul_f32 v[96:97], v[88:89], v[8:9] op_sel_hi:[0,1]
	v_pk_mul_f32 v[94:95], v[22:23], v[94:95]
	v_exp_f32_e32 v96, v96
	v_pk_fma_f32 v[22:23], v[124:125], s[36:37], v[94:95] op_sel_hi:[0,1,1]
	v_exp_f32_e32 v97, v97
	v_pk_mul_f32 v[90:91], v[88:89], v[10:11] op_sel_hi:[0,1]
	v_pk_mul_f32 v[96:97], v[24:25], v[96:97]
	v_exp_f32_e32 v90, v90
	v_pk_fma_f32 v[24:25], v[124:125], s[38:39], v[96:97] op_sel_hi:[0,1,1]
	v_exp_f32_e32 v91, v91
	v_pk_mul_f32 v[92:93], v[88:89], v[12:13] op_sel_hi:[0,1]
	v_pk_mul_f32 v[90:91], v[26:27], v[90:91]
	v_exp_f32_e32 v92, v92
	v_pk_fma_f32 v[26:27], v[124:125], s[40:41], v[90:91] op_sel_hi:[0,1,1]
	v_exp_f32_e32 v93, v93
	v_pk_mul_f32 v[94:95], v[88:89], v[14:15] op_sel_hi:[0,1]
	v_pk_mul_f32 v[92:93], v[28:29], v[92:93]
	v_exp_f32_e32 v94, v94
	v_pk_fma_f32 v[28:29], v[124:125], s[42:43], v[92:93] op_sel_hi:[0,1,1]
	v_exp_f32_e32 v95, v95
	v_pk_mul_f32 v[96:97], v[88:89], v[16:17] op_sel_hi:[0,1]
	v_pk_mul_f32 v[94:95], v[30:31], v[94:95]
	v_exp_f32_e32 v96, v96
	v_pk_fma_f32 v[30:31], v[124:125], s[44:45], v[94:95] op_sel_hi:[0,1,1]
	v_exp_f32_e32 v97, v97
	s_nop 0
	v_pk_mul_f32 v[96:97], v[32:33], v[96:97]
	s_nop 0
	v_pk_fma_f32 v[32:33], v[124:125], s[46:47], v[96:97] op_sel_hi:[0,1,1]
	v_mul_f32_e32 v124, v89, v125
	s_waitcnt vmcnt(6)
	s_waitcnt lgkmcnt(0)
	s_load_dwordx16 s[32:47], s[70:71], 0x800
	v_fma_f32 v98, v42, s64, v122
	v_mul_f32_e64 v99, -|v98|, s65
	v_cvt_f32_f16_e32 v125, v74
	v_exp_f32_e32 v99, v99
	v_max_f32_e32 v98, 0, v98
	v_add_f32_e32 v99, 1.0, v99
	v_log_f32_e32 v99, v99
	v_pk_mul_f32 v[90:91], v[88:89], v[2:3] op_sel:[1,0]
	v_fma_f32 v82, v99, s66, v98
	v_add_f32_e32 v123, v123, v82
	v_exp_f32_e32 v90, v90
	v_exp_f32_e32 v91, v91
	v_pk_mul_f32 v[92:93], v[88:89], v[4:5] op_sel:[1,0]
	v_pk_mul_f32 v[90:91], v[18:19], v[90:91]
	v_exp_f32_e32 v92, v92
	v_pk_fma_f32 v[18:19], v[124:125], s[48:49], v[90:91] op_sel_hi:[0,1,1]
	v_exp_f32_e32 v93, v93
	v_pk_mul_f32 v[94:95], v[88:89], v[6:7] op_sel:[1,0]
	v_pk_mul_f32 v[92:93], v[20:21], v[92:93]
	v_exp_f32_e32 v94, v94
	v_pk_fma_f32 v[20:21], v[124:125], s[50:51], v[92:93] op_sel_hi:[0,1,1]
	v_exp_f32_e32 v95, v95
	v_pk_mul_f32 v[96:97], v[88:89], v[8:9] op_sel:[1,0]
	v_pk_mul_f32 v[94:95], v[22:23], v[94:95]
	v_exp_f32_e32 v96, v96
	v_pk_fma_f32 v[22:23], v[124:125], s[52:53], v[94:95] op_sel_hi:[0,1,1]
	v_exp_f32_e32 v97, v97
	v_pk_mul_f32 v[90:91], v[88:89], v[10:11] op_sel:[1,0]
	v_pk_mul_f32 v[96:97], v[24:25], v[96:97]
	v_exp_f32_e32 v90, v90
	v_pk_fma_f32 v[24:25], v[124:125], s[54:55], v[96:97] op_sel_hi:[0,1,1]
	v_exp_f32_e32 v91, v91
	v_pk_mul_f32 v[92:93], v[88:89], v[12:13] op_sel:[1,0]
	v_pk_mul_f32 v[90:91], v[26:27], v[90:91]
	v_exp_f32_e32 v92, v92
	v_pk_fma_f32 v[26:27], v[124:125], s[56:57], v[90:91] op_sel_hi:[0,1,1]
	v_exp_f32_e32 v93, v93
	v_pk_mul_f32 v[94:95], v[88:89], v[14:15] op_sel:[1,0]
	v_pk_mul_f32 v[92:93], v[28:29], v[92:93]
	v_exp_f32_e32 v94, v94
	v_pk_fma_f32 v[28:29], v[124:125], s[58:59], v[92:93] op_sel_hi:[0,1,1]
	v_exp_f32_e32 v95, v95
	v_pk_mul_f32 v[96:97], v[88:89], v[16:17] op_sel:[1,0]
	v_pk_mul_f32 v[94:95], v[30:31], v[94:95]
	v_exp_f32_e32 v96, v96
	v_pk_fma_f32 v[30:31], v[124:125], s[60:61], v[94:95] op_sel_hi:[0,1,1]
	v_exp_f32_e32 v97, v97
	s_nop 0
	v_pk_mul_f32 v[96:97], v[32:33], v[96:97]
	s_nop 0
	v_pk_fma_f32 v[32:33], v[124:125], s[62:63], v[96:97] op_sel_hi:[0,1,1]
	v_mul_f32_e32 v124, v82, v125
	global_store_dwordx4 v126, v[86:89], s[72:73]
	s_add_u32 s72, s72, 0x8000
	s_addc_u32 s73, s73, 0
	s_waitcnt lgkmcnt(0)
	s_load_dwordx16 s[48:63], s[70:71], 0x880
	v_fma_f32 v98, v43, s64, v122
	v_mul_f32_e64 v99, -|v98|, s65
	v_cvt_f32_f16_sdwa v125, v74 dst_sel:DWORD dst_unused:UNUSED_PAD src0_sel:WORD_1
	v_exp_f32_e32 v99, v99
	v_max_f32_e32 v98, 0, v98
	v_add_f32_e32 v99, 1.0, v99
	v_log_f32_e32 v99, v99
	v_pk_mul_f32 v[90:91], v[82:83], v[2:3] op_sel_hi:[0,1]
	v_fma_f32 v83, v99, s66, v98
	v_add_f32_e32 v123, v123, v83
	v_exp_f32_e32 v90, v90
	v_exp_f32_e32 v91, v91
	v_pk_mul_f32 v[92:93], v[82:83], v[4:5] op_sel_hi:[0,1]
	v_pk_mul_f32 v[90:91], v[18:19], v[90:91]
	v_exp_f32_e32 v92, v92
	v_pk_fma_f32 v[18:19], v[124:125], s[32:33], v[90:91] op_sel_hi:[0,1,1]
	v_exp_f32_e32 v93, v93
	v_pk_mul_f32 v[94:95], v[82:83], v[6:7] op_sel_hi:[0,1]
	v_pk_mul_f32 v[92:93], v[20:21], v[92:93]
	v_exp_f32_e32 v94, v94
	v_pk_fma_f32 v[20:21], v[124:125], s[34:35], v[92:93] op_sel_hi:[0,1,1]
	v_exp_f32_e32 v95, v95
	v_pk_mul_f32 v[96:97], v[82:83], v[8:9] op_sel_hi:[0,1]
	v_pk_mul_f32 v[94:95], v[22:23], v[94:95]
	v_exp_f32_e32 v96, v96
	v_pk_fma_f32 v[22:23], v[124:125], s[36:37], v[94:95] op_sel_hi:[0,1,1]
	v_exp_f32_e32 v97, v97
	v_pk_mul_f32 v[90:91], v[82:83], v[10:11] op_sel_hi:[0,1]
	v_pk_mul_f32 v[96:97], v[24:25], v[96:97]
	v_exp_f32_e32 v90, v90
	v_pk_fma_f32 v[24:25], v[124:125], s[38:39], v[96:97] op_sel_hi:[0,1,1]
	v_exp_f32_e32 v91, v91
	v_pk_mul_f32 v[92:93], v[82:83], v[12:13] op_sel_hi:[0,1]
	v_pk_mul_f32 v[90:91], v[26:27], v[90:91]
	v_exp_f32_e32 v92, v92
	v_pk_fma_f32 v[26:27], v[124:125], s[40:41], v[90:91] op_sel_hi:[0,1,1]
	v_exp_f32_e32 v93, v93
	v_pk_mul_f32 v[94:95], v[82:83], v[14:15] op_sel_hi:[0,1]
	v_pk_mul_f32 v[92:93], v[28:29], v[92:93]
	v_exp_f32_e32 v94, v94
	v_pk_fma_f32 v[28:29], v[124:125], s[42:43], v[92:93] op_sel_hi:[0,1,1]
	v_exp_f32_e32 v95, v95
	v_pk_mul_f32 v[96:97], v[82:83], v[16:17] op_sel_hi:[0,1]
	v_pk_mul_f32 v[94:95], v[30:31], v[94:95]
	v_exp_f32_e32 v96, v96
	v_pk_fma_f32 v[30:31], v[124:125], s[44:45], v[94:95] op_sel_hi:[0,1,1]
	v_exp_f32_e32 v97, v97
	s_nop 0
	v_pk_mul_f32 v[96:97], v[32:33], v[96:97]
	s_nop 0
	v_pk_fma_f32 v[32:33], v[124:125], s[46:47], v[96:97] op_sel_hi:[0,1,1]
	v_mul_f32_e32 v124, v83, v125
	s_waitcnt lgkmcnt(0)
	s_load_dwordx16 s[32:47], s[70:71], 0x900
	v_fma_f32 v98, v44, s64, v122
	v_mul_f32_e64 v99, -|v98|, s65
	v_cvt_f32_f16_e32 v125, v75
	v_exp_f32_e32 v99, v99
	v_max_f32_e32 v98, 0, v98
	v_add_f32_e32 v99, 1.0, v99
	v_log_f32_e32 v99, v99
	v_pk_mul_f32 v[90:91], v[82:83], v[2:3] op_sel:[1,0]
	v_fma_f32 v84, v99, s66, v98
	v_add_f32_e32 v123, v123, v84
	v_exp_f32_e32 v90, v90
	v_exp_f32_e32 v91, v91
	v_pk_mul_f32 v[92:93], v[82:83], v[4:5] op_sel:[1,0]
	v_pk_mul_f32 v[90:91], v[18:19], v[90:91]
	v_exp_f32_e32 v92, v92
	v_pk_fma_f32 v[18:19], v[124:125], s[48:49], v[90:91] op_sel_hi:[0,1,1]
	v_exp_f32_e32 v93, v93
	v_pk_mul_f32 v[94:95], v[82:83], v[6:7] op_sel:[1,0]
	v_pk_mul_f32 v[92:93], v[20:21], v[92:93]
	v_exp_f32_e32 v94, v94
	v_pk_fma_f32 v[20:21], v[124:125], s[50:51], v[92:93] op_sel_hi:[0,1,1]
	v_exp_f32_e32 v95, v95
	v_pk_mul_f32 v[96:97], v[82:83], v[8:9] op_sel:[1,0]
	v_pk_mul_f32 v[94:95], v[22:23], v[94:95]
	v_exp_f32_e32 v96, v96
	v_pk_fma_f32 v[22:23], v[124:125], s[52:53], v[94:95] op_sel_hi:[0,1,1]
	v_exp_f32_e32 v97, v97
	v_pk_mul_f32 v[90:91], v[82:83], v[10:11] op_sel:[1,0]
	v_pk_mul_f32 v[96:97], v[24:25], v[96:97]
	v_exp_f32_e32 v90, v90
	v_pk_fma_f32 v[24:25], v[124:125], s[54:55], v[96:97] op_sel_hi:[0,1,1]
	v_exp_f32_e32 v91, v91
	v_pk_mul_f32 v[92:93], v[82:83], v[12:13] op_sel:[1,0]
	v_pk_mul_f32 v[90:91], v[26:27], v[90:91]
	v_exp_f32_e32 v92, v92
	v_pk_fma_f32 v[26:27], v[124:125], s[56:57], v[90:91] op_sel_hi:[0,1,1]
	v_exp_f32_e32 v93, v93
	v_pk_mul_f32 v[94:95], v[82:83], v[14:15] op_sel:[1,0]
	v_pk_mul_f32 v[92:93], v[28:29], v[92:93]
	v_exp_f32_e32 v94, v94
	v_pk_fma_f32 v[28:29], v[124:125], s[58:59], v[92:93] op_sel_hi:[0,1,1]
	v_exp_f32_e32 v95, v95
	v_pk_mul_f32 v[96:97], v[82:83], v[16:17] op_sel:[1,0]
	v_pk_mul_f32 v[94:95], v[30:31], v[94:95]
	v_exp_f32_e32 v96, v96
	v_pk_fma_f32 v[30:31], v[124:125], s[60:61], v[94:95] op_sel_hi:[0,1,1]
	v_exp_f32_e32 v97, v97
	s_nop 0
	v_pk_mul_f32 v[96:97], v[32:33], v[96:97]
	s_nop 0
	v_pk_fma_f32 v[32:33], v[124:125], s[62:63], v[96:97] op_sel_hi:[0,1,1]
	v_mul_f32_e32 v124, v84, v125
	s_waitcnt lgkmcnt(0)
	s_load_dwordx16 s[48:63], s[70:71], 0x980
	v_fma_f32 v98, v45, s64, v122
	v_mul_f32_e64 v99, -|v98|, s65
	v_cvt_f32_f16_sdwa v125, v75 dst_sel:DWORD dst_unused:UNUSED_PAD src0_sel:WORD_1
	v_exp_f32_e32 v99, v99
	v_max_f32_e32 v98, 0, v98
	v_add_f32_e32 v99, 1.0, v99
	v_log_f32_e32 v99, v99
	v_pk_mul_f32 v[90:91], v[84:85], v[2:3] op_sel_hi:[0,1]
	v_fma_f32 v85, v99, s66, v98
	v_add_f32_e32 v123, v123, v85
	v_exp_f32_e32 v90, v90
	v_exp_f32_e32 v91, v91
	v_pk_mul_f32 v[92:93], v[84:85], v[4:5] op_sel_hi:[0,1]
	v_pk_mul_f32 v[90:91], v[18:19], v[90:91]
	v_exp_f32_e32 v92, v92
	v_pk_fma_f32 v[18:19], v[124:125], s[32:33], v[90:91] op_sel_hi:[0,1,1]
	v_exp_f32_e32 v93, v93
	v_pk_mul_f32 v[94:95], v[84:85], v[6:7] op_sel_hi:[0,1]
	v_pk_mul_f32 v[92:93], v[20:21], v[92:93]
	v_exp_f32_e32 v94, v94
	v_pk_fma_f32 v[20:21], v[124:125], s[34:35], v[92:93] op_sel_hi:[0,1,1]
	v_exp_f32_e32 v95, v95
	v_pk_mul_f32 v[96:97], v[84:85], v[8:9] op_sel_hi:[0,1]
	v_pk_mul_f32 v[94:95], v[22:23], v[94:95]
	v_exp_f32_e32 v96, v96
	v_pk_fma_f32 v[22:23], v[124:125], s[36:37], v[94:95] op_sel_hi:[0,1,1]
	v_exp_f32_e32 v97, v97
	v_pk_mul_f32 v[90:91], v[84:85], v[10:11] op_sel_hi:[0,1]
	v_pk_mul_f32 v[96:97], v[24:25], v[96:97]
	v_exp_f32_e32 v90, v90
	v_pk_fma_f32 v[24:25], v[124:125], s[38:39], v[96:97] op_sel_hi:[0,1,1]
	v_exp_f32_e32 v91, v91
	v_pk_mul_f32 v[92:93], v[84:85], v[12:13] op_sel_hi:[0,1]
	v_pk_mul_f32 v[90:91], v[26:27], v[90:91]
	v_exp_f32_e32 v92, v92
	v_pk_fma_f32 v[26:27], v[124:125], s[40:41], v[90:91] op_sel_hi:[0,1,1]
	v_exp_f32_e32 v93, v93
	v_pk_mul_f32 v[94:95], v[84:85], v[14:15] op_sel_hi:[0,1]
	v_pk_mul_f32 v[92:93], v[28:29], v[92:93]
	v_exp_f32_e32 v94, v94
	v_pk_fma_f32 v[28:29], v[124:125], s[42:43], v[92:93] op_sel_hi:[0,1,1]
	v_exp_f32_e32 v95, v95
	v_pk_mul_f32 v[96:97], v[84:85], v[16:17] op_sel_hi:[0,1]
	v_pk_mul_f32 v[94:95], v[30:31], v[94:95]
	v_exp_f32_e32 v96, v96
	v_pk_fma_f32 v[30:31], v[124:125], s[44:45], v[94:95] op_sel_hi:[0,1,1]
	v_exp_f32_e32 v97, v97
	s_nop 0
	v_pk_mul_f32 v[96:97], v[32:33], v[96:97]
	s_nop 0
	v_pk_fma_f32 v[32:33], v[124:125], s[46:47], v[96:97] op_sel_hi:[0,1,1]
	v_mul_f32_e32 v124, v85, v125
	s_waitcnt lgkmcnt(0)
	s_load_dwordx16 s[32:47], s[70:71], 0xa00
	v_fma_f32 v98, v58, s64, v122
	v_mul_f32_e64 v99, -|v98|, s65
	v_cvt_f32_f16_e32 v125, v76
	v_exp_f32_e32 v99, v99
	v_max_f32_e32 v98, 0, v98
	v_add_f32_e32 v99, 1.0, v99
	v_log_f32_e32 v99, v99
	v_pk_mul_f32 v[90:91], v[84:85], v[2:3] op_sel:[1,0]
	v_fma_f32 v86, v99, s66, v98
	v_add_f32_e32 v123, v123, v86
	v_exp_f32_e32 v90, v90
	v_exp_f32_e32 v91, v91
	v_pk_mul_f32 v[92:93], v[84:85], v[4:5] op_sel:[1,0]
	v_pk_mul_f32 v[90:91], v[18:19], v[90:91]
	v_exp_f32_e32 v92, v92
	v_pk_fma_f32 v[18:19], v[124:125], s[48:49], v[90:91] op_sel_hi:[0,1,1]
	v_exp_f32_e32 v93, v93
	v_pk_mul_f32 v[94:95], v[84:85], v[6:7] op_sel:[1,0]
	v_pk_mul_f32 v[92:93], v[20:21], v[92:93]
	v_exp_f32_e32 v94, v94
	v_pk_fma_f32 v[20:21], v[124:125], s[50:51], v[92:93] op_sel_hi:[0,1,1]
	v_exp_f32_e32 v95, v95
	v_pk_mul_f32 v[96:97], v[84:85], v[8:9] op_sel:[1,0]
	v_pk_mul_f32 v[94:95], v[22:23], v[94:95]
	v_exp_f32_e32 v96, v96
	v_pk_fma_f32 v[22:23], v[124:125], s[52:53], v[94:95] op_sel_hi:[0,1,1]
	v_exp_f32_e32 v97, v97
	v_pk_mul_f32 v[90:91], v[84:85], v[10:11] op_sel:[1,0]
	v_pk_mul_f32 v[96:97], v[24:25], v[96:97]
	v_exp_f32_e32 v90, v90
	v_pk_fma_f32 v[24:25], v[124:125], s[54:55], v[96:97] op_sel_hi:[0,1,1]
	v_exp_f32_e32 v91, v91
	v_pk_mul_f32 v[92:93], v[84:85], v[12:13] op_sel:[1,0]
	v_pk_mul_f32 v[90:91], v[26:27], v[90:91]
	v_exp_f32_e32 v92, v92
	v_pk_fma_f32 v[26:27], v[124:125], s[56:57], v[90:91] op_sel_hi:[0,1,1]
	v_exp_f32_e32 v93, v93
	v_pk_mul_f32 v[94:95], v[84:85], v[14:15] op_sel:[1,0]
	v_pk_mul_f32 v[92:93], v[28:29], v[92:93]
	v_exp_f32_e32 v94, v94
	v_pk_fma_f32 v[28:29], v[124:125], s[58:59], v[92:93] op_sel_hi:[0,1,1]
	v_exp_f32_e32 v95, v95
	v_pk_mul_f32 v[96:97], v[84:85], v[16:17] op_sel:[1,0]
	v_pk_mul_f32 v[94:95], v[30:31], v[94:95]
	v_exp_f32_e32 v96, v96
	v_pk_fma_f32 v[30:31], v[124:125], s[60:61], v[94:95] op_sel_hi:[0,1,1]
	v_exp_f32_e32 v97, v97
	s_nop 0
	v_pk_mul_f32 v[96:97], v[32:33], v[96:97]
	s_nop 0
	v_pk_fma_f32 v[32:33], v[124:125], s[62:63], v[96:97] op_sel_hi:[0,1,1]
	v_mul_f32_e32 v124, v86, v125
	global_store_dwordx4 v126, v[82:85], s[72:73]
	s_add_u32 s72, s72, 0x8000
	s_addc_u32 s73, s73, 0
	s_waitcnt lgkmcnt(0)
	s_load_dwordx16 s[48:63], s[70:71], 0xa80
	v_fma_f32 v98, v59, s64, v122
	v_mul_f32_e64 v99, -|v98|, s65
	v_cvt_f32_f16_sdwa v125, v76 dst_sel:DWORD dst_unused:UNUSED_PAD src0_sel:WORD_1
	v_exp_f32_e32 v99, v99
	v_max_f32_e32 v98, 0, v98
	v_add_f32_e32 v99, 1.0, v99
	v_log_f32_e32 v99, v99
	v_pk_mul_f32 v[90:91], v[86:87], v[2:3] op_sel_hi:[0,1]
	v_fma_f32 v87, v99, s66, v98
	v_add_f32_e32 v123, v123, v87
	v_exp_f32_e32 v90, v90
	v_exp_f32_e32 v91, v91
	v_pk_mul_f32 v[92:93], v[86:87], v[4:5] op_sel_hi:[0,1]
	v_pk_mul_f32 v[90:91], v[18:19], v[90:91]
	v_exp_f32_e32 v92, v92
	v_pk_fma_f32 v[18:19], v[124:125], s[32:33], v[90:91] op_sel_hi:[0,1,1]
	v_exp_f32_e32 v93, v93
	v_pk_mul_f32 v[94:95], v[86:87], v[6:7] op_sel_hi:[0,1]
	v_pk_mul_f32 v[92:93], v[20:21], v[92:93]
	v_exp_f32_e32 v94, v94
	v_pk_fma_f32 v[20:21], v[124:125], s[34:35], v[92:93] op_sel_hi:[0,1,1]
	v_exp_f32_e32 v95, v95
	v_pk_mul_f32 v[96:97], v[86:87], v[8:9] op_sel_hi:[0,1]
	v_pk_mul_f32 v[94:95], v[22:23], v[94:95]
	v_exp_f32_e32 v96, v96
	v_pk_fma_f32 v[22:23], v[124:125], s[36:37], v[94:95] op_sel_hi:[0,1,1]
	v_exp_f32_e32 v97, v97
	v_pk_mul_f32 v[90:91], v[86:87], v[10:11] op_sel_hi:[0,1]
	v_pk_mul_f32 v[96:97], v[24:25], v[96:97]
	v_exp_f32_e32 v90, v90
	v_pk_fma_f32 v[24:25], v[124:125], s[38:39], v[96:97] op_sel_hi:[0,1,1]
	v_exp_f32_e32 v91, v91
	v_pk_mul_f32 v[92:93], v[86:87], v[12:13] op_sel_hi:[0,1]
	v_pk_mul_f32 v[90:91], v[26:27], v[90:91]
	v_exp_f32_e32 v92, v92
	v_pk_fma_f32 v[26:27], v[124:125], s[40:41], v[90:91] op_sel_hi:[0,1,1]
	v_exp_f32_e32 v93, v93
	v_pk_mul_f32 v[94:95], v[86:87], v[14:15] op_sel_hi:[0,1]
	v_pk_mul_f32 v[92:93], v[28:29], v[92:93]
	v_exp_f32_e32 v94, v94
	v_pk_fma_f32 v[28:29], v[124:125], s[42:43], v[92:93] op_sel_hi:[0,1,1]
	v_exp_f32_e32 v95, v95
	v_pk_mul_f32 v[96:97], v[86:87], v[16:17] op_sel_hi:[0,1]
	v_pk_mul_f32 v[94:95], v[30:31], v[94:95]
	v_exp_f32_e32 v96, v96
	v_pk_fma_f32 v[30:31], v[124:125], s[44:45], v[94:95] op_sel_hi:[0,1,1]
	v_exp_f32_e32 v97, v97
	s_nop 0
	v_pk_mul_f32 v[96:97], v[32:33], v[96:97]
	s_nop 0
	v_pk_fma_f32 v[32:33], v[124:125], s[46:47], v[96:97] op_sel_hi:[0,1,1]
	v_mul_f32_e32 v124, v87, v125
	s_waitcnt lgkmcnt(0)
	s_load_dwordx16 s[32:47], s[70:71], 0xb00
	v_fma_f32 v98, v60, s64, v122
	v_mul_f32_e64 v99, -|v98|, s65
	v_cvt_f32_f16_e32 v125, v77
	v_exp_f32_e32 v99, v99
	v_max_f32_e32 v98, 0, v98
	v_add_f32_e32 v99, 1.0, v99
	v_log_f32_e32 v99, v99
	v_pk_mul_f32 v[90:91], v[86:87], v[2:3] op_sel:[1,0]
	v_fma_f32 v88, v99, s66, v98
	v_add_f32_e32 v123, v123, v88
	v_exp_f32_e32 v90, v90
	v_exp_f32_e32 v91, v91
	v_pk_mul_f32 v[92:93], v[86:87], v[4:5] op_sel:[1,0]
	v_pk_mul_f32 v[90:91], v[18:19], v[90:91]
	v_exp_f32_e32 v92, v92
	v_pk_fma_f32 v[18:19], v[124:125], s[48:49], v[90:91] op_sel_hi:[0,1,1]
	v_exp_f32_e32 v93, v93
	v_pk_mul_f32 v[94:95], v[86:87], v[6:7] op_sel:[1,0]
	v_pk_mul_f32 v[92:93], v[20:21], v[92:93]
	v_exp_f32_e32 v94, v94
	v_pk_fma_f32 v[20:21], v[124:125], s[50:51], v[92:93] op_sel_hi:[0,1,1]
	v_exp_f32_e32 v95, v95
	v_pk_mul_f32 v[96:97], v[86:87], v[8:9] op_sel:[1,0]
	v_pk_mul_f32 v[94:95], v[22:23], v[94:95]
	v_exp_f32_e32 v96, v96
	v_pk_fma_f32 v[22:23], v[124:125], s[52:53], v[94:95] op_sel_hi:[0,1,1]
	v_exp_f32_e32 v97, v97
	v_pk_mul_f32 v[90:91], v[86:87], v[10:11] op_sel:[1,0]
	v_pk_mul_f32 v[96:97], v[24:25], v[96:97]
	v_exp_f32_e32 v90, v90
	v_pk_fma_f32 v[24:25], v[124:125], s[54:55], v[96:97] op_sel_hi:[0,1,1]
	v_exp_f32_e32 v91, v91
	v_pk_mul_f32 v[92:93], v[86:87], v[12:13] op_sel:[1,0]
	v_pk_mul_f32 v[90:91], v[26:27], v[90:91]
	v_exp_f32_e32 v92, v92
	v_pk_fma_f32 v[26:27], v[124:125], s[56:57], v[90:91] op_sel_hi:[0,1,1]
	v_exp_f32_e32 v93, v93
	v_pk_mul_f32 v[94:95], v[86:87], v[14:15] op_sel:[1,0]
	v_pk_mul_f32 v[92:93], v[28:29], v[92:93]
	v_exp_f32_e32 v94, v94
	v_pk_fma_f32 v[28:29], v[124:125], s[58:59], v[92:93] op_sel_hi:[0,1,1]
	v_exp_f32_e32 v95, v95
	v_pk_mul_f32 v[96:97], v[86:87], v[16:17] op_sel:[1,0]
	v_pk_mul_f32 v[94:95], v[30:31], v[94:95]
	v_exp_f32_e32 v96, v96
	v_pk_fma_f32 v[30:31], v[124:125], s[60:61], v[94:95] op_sel_hi:[0,1,1]
	v_exp_f32_e32 v97, v97
	s_nop 0
	v_pk_mul_f32 v[96:97], v[32:33], v[96:97]
	s_nop 0
	v_pk_fma_f32 v[32:33], v[124:125], s[62:63], v[96:97] op_sel_hi:[0,1,1]
	v_mul_f32_e32 v124, v88, v125
	s_waitcnt lgkmcnt(0)
	s_load_dwordx16 s[48:63], s[70:71], 0xb80
	v_fma_f32 v98, v61, s64, v122
	v_mul_f32_e64 v99, -|v98|, s65
	v_cvt_f32_f16_sdwa v125, v77 dst_sel:DWORD dst_unused:UNUSED_PAD src0_sel:WORD_1
	v_exp_f32_e32 v99, v99
	v_max_f32_e32 v98, 0, v98
	v_add_f32_e32 v99, 1.0, v99
	v_log_f32_e32 v99, v99
	v_pk_mul_f32 v[90:91], v[88:89], v[2:3] op_sel_hi:[0,1]
	v_fma_f32 v89, v99, s66, v98
	v_add_f32_e32 v123, v123, v89
	v_exp_f32_e32 v90, v90
	v_exp_f32_e32 v91, v91
	v_pk_mul_f32 v[92:93], v[88:89], v[4:5] op_sel_hi:[0,1]
	v_pk_mul_f32 v[90:91], v[18:19], v[90:91]
	v_exp_f32_e32 v92, v92
	v_pk_fma_f32 v[18:19], v[124:125], s[32:33], v[90:91] op_sel_hi:[0,1,1]
	v_exp_f32_e32 v93, v93
	v_pk_mul_f32 v[94:95], v[88:89], v[6:7] op_sel_hi:[0,1]
	v_pk_mul_f32 v[92:93], v[20:21], v[92:93]
	v_exp_f32_e32 v94, v94
	v_pk_fma_f32 v[20:21], v[124:125], s[34:35], v[92:93] op_sel_hi:[0,1,1]
	v_exp_f32_e32 v95, v95
	v_pk_mul_f32 v[96:97], v[88:89], v[8:9] op_sel_hi:[0,1]
	v_pk_mul_f32 v[94:95], v[22:23], v[94:95]
	v_exp_f32_e32 v96, v96
	v_pk_fma_f32 v[22:23], v[124:125], s[36:37], v[94:95] op_sel_hi:[0,1,1]
	v_exp_f32_e32 v97, v97
	v_pk_mul_f32 v[90:91], v[88:89], v[10:11] op_sel_hi:[0,1]
	v_pk_mul_f32 v[96:97], v[24:25], v[96:97]
	v_exp_f32_e32 v90, v90
	v_pk_fma_f32 v[24:25], v[124:125], s[38:39], v[96:97] op_sel_hi:[0,1,1]
	v_exp_f32_e32 v91, v91
	v_pk_mul_f32 v[92:93], v[88:89], v[12:13] op_sel_hi:[0,1]
	v_pk_mul_f32 v[90:91], v[26:27], v[90:91]
	v_exp_f32_e32 v92, v92
	v_pk_fma_f32 v[26:27], v[124:125], s[40:41], v[90:91] op_sel_hi:[0,1,1]
	v_exp_f32_e32 v93, v93
	v_pk_mul_f32 v[94:95], v[88:89], v[14:15] op_sel_hi:[0,1]
	v_pk_mul_f32 v[92:93], v[28:29], v[92:93]
	v_exp_f32_e32 v94, v94
	v_pk_fma_f32 v[28:29], v[124:125], s[42:43], v[92:93] op_sel_hi:[0,1,1]
	v_exp_f32_e32 v95, v95
	v_pk_mul_f32 v[96:97], v[88:89], v[16:17] op_sel_hi:[0,1]
	v_pk_mul_f32 v[94:95], v[30:31], v[94:95]
	v_exp_f32_e32 v96, v96
	v_pk_fma_f32 v[30:31], v[124:125], s[44:45], v[94:95] op_sel_hi:[0,1,1]
	v_exp_f32_e32 v97, v97
	s_nop 0
	v_pk_mul_f32 v[96:97], v[32:33], v[96:97]
	s_nop 0
	v_pk_fma_f32 v[32:33], v[124:125], s[46:47], v[96:97] op_sel_hi:[0,1,1]
	v_mul_f32_e32 v124, v89, v125
	s_waitcnt vmcnt(7)
	s_waitcnt lgkmcnt(0)
	s_load_dwordx16 s[32:47], s[70:71], 0xc00
	v_fma_f32 v98, v46, s64, v122
	v_mul_f32_e64 v99, -|v98|, s65
	v_cvt_f32_f16_e32 v125, v78
	v_exp_f32_e32 v99, v99
	v_max_f32_e32 v98, 0, v98
	v_add_f32_e32 v99, 1.0, v99
	v_log_f32_e32 v99, v99
	v_pk_mul_f32 v[90:91], v[88:89], v[2:3] op_sel:[1,0]
	v_fma_f32 v82, v99, s66, v98
	v_add_f32_e32 v123, v123, v82
	v_exp_f32_e32 v90, v90
	v_exp_f32_e32 v91, v91
	v_pk_mul_f32 v[92:93], v[88:89], v[4:5] op_sel:[1,0]
	v_pk_mul_f32 v[90:91], v[18:19], v[90:91]
	v_exp_f32_e32 v92, v92
	v_pk_fma_f32 v[18:19], v[124:125], s[48:49], v[90:91] op_sel_hi:[0,1,1]
	v_exp_f32_e32 v93, v93
	v_pk_mul_f32 v[94:95], v[88:89], v[6:7] op_sel:[1,0]
	v_pk_mul_f32 v[92:93], v[20:21], v[92:93]
	v_exp_f32_e32 v94, v94
	v_pk_fma_f32 v[20:21], v[124:125], s[50:51], v[92:93] op_sel_hi:[0,1,1]
	v_exp_f32_e32 v95, v95
	v_pk_mul_f32 v[96:97], v[88:89], v[8:9] op_sel:[1,0]
	v_pk_mul_f32 v[94:95], v[22:23], v[94:95]
	v_exp_f32_e32 v96, v96
	v_pk_fma_f32 v[22:23], v[124:125], s[52:53], v[94:95] op_sel_hi:[0,1,1]
	v_exp_f32_e32 v97, v97
	v_pk_mul_f32 v[90:91], v[88:89], v[10:11] op_sel:[1,0]
	v_pk_mul_f32 v[96:97], v[24:25], v[96:97]
	v_exp_f32_e32 v90, v90
	v_pk_fma_f32 v[24:25], v[124:125], s[54:55], v[96:97] op_sel_hi:[0,1,1]
	v_exp_f32_e32 v91, v91
	v_pk_mul_f32 v[92:93], v[88:89], v[12:13] op_sel:[1,0]
	v_pk_mul_f32 v[90:91], v[26:27], v[90:91]
	v_exp_f32_e32 v92, v92
	v_pk_fma_f32 v[26:27], v[124:125], s[56:57], v[90:91] op_sel_hi:[0,1,1]
	v_exp_f32_e32 v93, v93
	v_pk_mul_f32 v[94:95], v[88:89], v[14:15] op_sel:[1,0]
	v_pk_mul_f32 v[92:93], v[28:29], v[92:93]
	v_exp_f32_e32 v94, v94
	v_pk_fma_f32 v[28:29], v[124:125], s[58:59], v[92:93] op_sel_hi:[0,1,1]
	v_exp_f32_e32 v95, v95
	v_pk_mul_f32 v[96:97], v[88:89], v[16:17] op_sel:[1,0]
	v_pk_mul_f32 v[94:95], v[30:31], v[94:95]
	v_exp_f32_e32 v96, v96
	v_pk_fma_f32 v[30:31], v[124:125], s[60:61], v[94:95] op_sel_hi:[0,1,1]
	v_exp_f32_e32 v97, v97
	s_nop 0
	v_pk_mul_f32 v[96:97], v[32:33], v[96:97]
	s_nop 0
	v_pk_fma_f32 v[32:33], v[124:125], s[62:63], v[96:97] op_sel_hi:[0,1,1]
	v_mul_f32_e32 v124, v82, v125
	global_store_dwordx4 v126, v[86:89], s[72:73]
	s_add_u32 s72, s72, 0x8000
	s_addc_u32 s73, s73, 0
	s_waitcnt lgkmcnt(0)
	s_load_dwordx16 s[48:63], s[70:71], 0xc80
	v_fma_f32 v98, v47, s64, v122
	v_mul_f32_e64 v99, -|v98|, s65
	v_cvt_f32_f16_sdwa v125, v78 dst_sel:DWORD dst_unused:UNUSED_PAD src0_sel:WORD_1
	v_exp_f32_e32 v99, v99
	v_max_f32_e32 v98, 0, v98
	v_add_f32_e32 v99, 1.0, v99
	v_log_f32_e32 v99, v99
	v_pk_mul_f32 v[90:91], v[82:83], v[2:3] op_sel_hi:[0,1]
	v_fma_f32 v83, v99, s66, v98
	v_add_f32_e32 v123, v123, v83
	v_exp_f32_e32 v90, v90
	v_exp_f32_e32 v91, v91
	v_pk_mul_f32 v[92:93], v[82:83], v[4:5] op_sel_hi:[0,1]
	v_pk_mul_f32 v[90:91], v[18:19], v[90:91]
	v_exp_f32_e32 v92, v92
	v_pk_fma_f32 v[18:19], v[124:125], s[32:33], v[90:91] op_sel_hi:[0,1,1]
	v_exp_f32_e32 v93, v93
	v_pk_mul_f32 v[94:95], v[82:83], v[6:7] op_sel_hi:[0,1]
	v_pk_mul_f32 v[92:93], v[20:21], v[92:93]
	v_exp_f32_e32 v94, v94
	v_pk_fma_f32 v[20:21], v[124:125], s[34:35], v[92:93] op_sel_hi:[0,1,1]
	v_exp_f32_e32 v95, v95
	v_pk_mul_f32 v[96:97], v[82:83], v[8:9] op_sel_hi:[0,1]
	v_pk_mul_f32 v[94:95], v[22:23], v[94:95]
	v_exp_f32_e32 v96, v96
	v_pk_fma_f32 v[22:23], v[124:125], s[36:37], v[94:95] op_sel_hi:[0,1,1]
	v_exp_f32_e32 v97, v97
	v_pk_mul_f32 v[90:91], v[82:83], v[10:11] op_sel_hi:[0,1]
	v_pk_mul_f32 v[96:97], v[24:25], v[96:97]
	v_exp_f32_e32 v90, v90
	v_pk_fma_f32 v[24:25], v[124:125], s[38:39], v[96:97] op_sel_hi:[0,1,1]
	v_exp_f32_e32 v91, v91
	v_pk_mul_f32 v[92:93], v[82:83], v[12:13] op_sel_hi:[0,1]
	v_pk_mul_f32 v[90:91], v[26:27], v[90:91]
	v_exp_f32_e32 v92, v92
	v_pk_fma_f32 v[26:27], v[124:125], s[40:41], v[90:91] op_sel_hi:[0,1,1]
	v_exp_f32_e32 v93, v93
	v_pk_mul_f32 v[94:95], v[82:83], v[14:15] op_sel_hi:[0,1]
	v_pk_mul_f32 v[92:93], v[28:29], v[92:93]
	v_exp_f32_e32 v94, v94
	v_pk_fma_f32 v[28:29], v[124:125], s[42:43], v[92:93] op_sel_hi:[0,1,1]
	v_exp_f32_e32 v95, v95
	v_pk_mul_f32 v[96:97], v[82:83], v[16:17] op_sel_hi:[0,1]
	v_pk_mul_f32 v[94:95], v[30:31], v[94:95]
	v_exp_f32_e32 v96, v96
	v_pk_fma_f32 v[30:31], v[124:125], s[44:45], v[94:95] op_sel_hi:[0,1,1]
	v_exp_f32_e32 v97, v97
	s_nop 0
	v_pk_mul_f32 v[96:97], v[32:33], v[96:97]
	s_nop 0
	v_pk_fma_f32 v[32:33], v[124:125], s[46:47], v[96:97] op_sel_hi:[0,1,1]
	v_mul_f32_e32 v124, v83, v125
	s_waitcnt lgkmcnt(0)
	s_load_dwordx16 s[32:47], s[70:71], 0xd00
	v_fma_f32 v98, v48, s64, v122
	v_mul_f32_e64 v99, -|v98|, s65
	v_cvt_f32_f16_e32 v125, v79
	v_exp_f32_e32 v99, v99
	v_max_f32_e32 v98, 0, v98
	v_add_f32_e32 v99, 1.0, v99
	v_log_f32_e32 v99, v99
	v_pk_mul_f32 v[90:91], v[82:83], v[2:3] op_sel:[1,0]
	v_fma_f32 v84, v99, s66, v98
	v_add_f32_e32 v123, v123, v84
	v_exp_f32_e32 v90, v90
	v_exp_f32_e32 v91, v91
	v_pk_mul_f32 v[92:93], v[82:83], v[4:5] op_sel:[1,0]
	v_pk_mul_f32 v[90:91], v[18:19], v[90:91]
	v_exp_f32_e32 v92, v92
	v_pk_fma_f32 v[18:19], v[124:125], s[48:49], v[90:91] op_sel_hi:[0,1,1]
	v_exp_f32_e32 v93, v93
	v_pk_mul_f32 v[94:95], v[82:83], v[6:7] op_sel:[1,0]
	v_pk_mul_f32 v[92:93], v[20:21], v[92:93]
	v_exp_f32_e32 v94, v94
	v_pk_fma_f32 v[20:21], v[124:125], s[50:51], v[92:93] op_sel_hi:[0,1,1]
	v_exp_f32_e32 v95, v95
	v_pk_mul_f32 v[96:97], v[82:83], v[8:9] op_sel:[1,0]
	v_pk_mul_f32 v[94:95], v[22:23], v[94:95]
	v_exp_f32_e32 v96, v96
	v_pk_fma_f32 v[22:23], v[124:125], s[52:53], v[94:95] op_sel_hi:[0,1,1]
	v_exp_f32_e32 v97, v97
	v_pk_mul_f32 v[90:91], v[82:83], v[10:11] op_sel:[1,0]
	v_pk_mul_f32 v[96:97], v[24:25], v[96:97]
	v_exp_f32_e32 v90, v90
	v_pk_fma_f32 v[24:25], v[124:125], s[54:55], v[96:97] op_sel_hi:[0,1,1]
	v_exp_f32_e32 v91, v91
	v_pk_mul_f32 v[92:93], v[82:83], v[12:13] op_sel:[1,0]
	v_pk_mul_f32 v[90:91], v[26:27], v[90:91]
	v_exp_f32_e32 v92, v92
	v_pk_fma_f32 v[26:27], v[124:125], s[56:57], v[90:91] op_sel_hi:[0,1,1]
	v_exp_f32_e32 v93, v93
	v_pk_mul_f32 v[94:95], v[82:83], v[14:15] op_sel:[1,0]
	v_pk_mul_f32 v[92:93], v[28:29], v[92:93]
	v_exp_f32_e32 v94, v94
	v_pk_fma_f32 v[28:29], v[124:125], s[58:59], v[92:93] op_sel_hi:[0,1,1]
	v_exp_f32_e32 v95, v95
	v_pk_mul_f32 v[96:97], v[82:83], v[16:17] op_sel:[1,0]
	v_pk_mul_f32 v[94:95], v[30:31], v[94:95]
	v_exp_f32_e32 v96, v96
	v_pk_fma_f32 v[30:31], v[124:125], s[60:61], v[94:95] op_sel_hi:[0,1,1]
	v_exp_f32_e32 v97, v97
	s_nop 0
	v_pk_mul_f32 v[96:97], v[32:33], v[96:97]
	s_nop 0
	v_pk_fma_f32 v[32:33], v[124:125], s[62:63], v[96:97] op_sel_hi:[0,1,1]
	v_mul_f32_e32 v124, v84, v125
	s_waitcnt lgkmcnt(0)
	s_load_dwordx16 s[48:63], s[70:71], 0xd80
	v_fma_f32 v98, v49, s64, v122
	v_mul_f32_e64 v99, -|v98|, s65
	v_cvt_f32_f16_sdwa v125, v79 dst_sel:DWORD dst_unused:UNUSED_PAD src0_sel:WORD_1
	v_exp_f32_e32 v99, v99
	v_max_f32_e32 v98, 0, v98
	v_add_f32_e32 v99, 1.0, v99
	v_log_f32_e32 v99, v99
	v_pk_mul_f32 v[90:91], v[84:85], v[2:3] op_sel_hi:[0,1]
	v_fma_f32 v85, v99, s66, v98
	v_add_f32_e32 v123, v123, v85
	v_exp_f32_e32 v90, v90
	v_exp_f32_e32 v91, v91
	v_pk_mul_f32 v[92:93], v[84:85], v[4:5] op_sel_hi:[0,1]
	v_pk_mul_f32 v[90:91], v[18:19], v[90:91]
	v_exp_f32_e32 v92, v92
	v_pk_fma_f32 v[18:19], v[124:125], s[32:33], v[90:91] op_sel_hi:[0,1,1]
	v_exp_f32_e32 v93, v93
	v_pk_mul_f32 v[94:95], v[84:85], v[6:7] op_sel_hi:[0,1]
	v_pk_mul_f32 v[92:93], v[20:21], v[92:93]
	v_exp_f32_e32 v94, v94
	v_pk_fma_f32 v[20:21], v[124:125], s[34:35], v[92:93] op_sel_hi:[0,1,1]
	v_exp_f32_e32 v95, v95
	v_pk_mul_f32 v[96:97], v[84:85], v[8:9] op_sel_hi:[0,1]
	v_pk_mul_f32 v[94:95], v[22:23], v[94:95]
	v_exp_f32_e32 v96, v96
	v_pk_fma_f32 v[22:23], v[124:125], s[36:37], v[94:95] op_sel_hi:[0,1,1]
	v_exp_f32_e32 v97, v97
	v_pk_mul_f32 v[90:91], v[84:85], v[10:11] op_sel_hi:[0,1]
	v_pk_mul_f32 v[96:97], v[24:25], v[96:97]
	v_exp_f32_e32 v90, v90
	v_pk_fma_f32 v[24:25], v[124:125], s[38:39], v[96:97] op_sel_hi:[0,1,1]
	v_exp_f32_e32 v91, v91
	v_pk_mul_f32 v[92:93], v[84:85], v[12:13] op_sel_hi:[0,1]
	v_pk_mul_f32 v[90:91], v[26:27], v[90:91]
	v_exp_f32_e32 v92, v92
	v_pk_fma_f32 v[26:27], v[124:125], s[40:41], v[90:91] op_sel_hi:[0,1,1]
	v_exp_f32_e32 v93, v93
	v_pk_mul_f32 v[94:95], v[84:85], v[14:15] op_sel_hi:[0,1]
	v_pk_mul_f32 v[92:93], v[28:29], v[92:93]
	v_exp_f32_e32 v94, v94
	v_pk_fma_f32 v[28:29], v[124:125], s[42:43], v[92:93] op_sel_hi:[0,1,1]
	v_exp_f32_e32 v95, v95
	v_pk_mul_f32 v[96:97], v[84:85], v[16:17] op_sel_hi:[0,1]
	v_pk_mul_f32 v[94:95], v[30:31], v[94:95]
	v_exp_f32_e32 v96, v96
	v_pk_fma_f32 v[30:31], v[124:125], s[44:45], v[94:95] op_sel_hi:[0,1,1]
	v_exp_f32_e32 v97, v97
	s_nop 0
	v_pk_mul_f32 v[96:97], v[32:33], v[96:97]
	s_nop 0
	v_pk_fma_f32 v[32:33], v[124:125], s[46:47], v[96:97] op_sel_hi:[0,1,1]
	v_mul_f32_e32 v124, v85, v125
	s_waitcnt lgkmcnt(0)
	s_load_dwordx16 s[32:47], s[70:71], 0xe00
	v_fma_f32 v98, v62, s64, v122
	v_mul_f32_e64 v99, -|v98|, s65
	v_cvt_f32_f16_e32 v125, v80
	v_exp_f32_e32 v99, v99
	v_max_f32_e32 v98, 0, v98
	v_add_f32_e32 v99, 1.0, v99
	v_log_f32_e32 v99, v99
	v_pk_mul_f32 v[90:91], v[84:85], v[2:3] op_sel:[1,0]
	v_fma_f32 v86, v99, s66, v98
	v_add_f32_e32 v123, v123, v86
	v_exp_f32_e32 v90, v90
	v_exp_f32_e32 v91, v91
	v_pk_mul_f32 v[92:93], v[84:85], v[4:5] op_sel:[1,0]
	v_pk_mul_f32 v[90:91], v[18:19], v[90:91]
	v_exp_f32_e32 v92, v92
	v_pk_fma_f32 v[18:19], v[124:125], s[48:49], v[90:91] op_sel_hi:[0,1,1]
	v_exp_f32_e32 v93, v93
	v_pk_mul_f32 v[94:95], v[84:85], v[6:7] op_sel:[1,0]
	v_pk_mul_f32 v[92:93], v[20:21], v[92:93]
	v_exp_f32_e32 v94, v94
	v_pk_fma_f32 v[20:21], v[124:125], s[50:51], v[92:93] op_sel_hi:[0,1,1]
	v_exp_f32_e32 v95, v95
	v_pk_mul_f32 v[96:97], v[84:85], v[8:9] op_sel:[1,0]
	v_pk_mul_f32 v[94:95], v[22:23], v[94:95]
	v_exp_f32_e32 v96, v96
	v_pk_fma_f32 v[22:23], v[124:125], s[52:53], v[94:95] op_sel_hi:[0,1,1]
	v_exp_f32_e32 v97, v97
	v_pk_mul_f32 v[90:91], v[84:85], v[10:11] op_sel:[1,0]
	v_pk_mul_f32 v[96:97], v[24:25], v[96:97]
	v_exp_f32_e32 v90, v90
	v_pk_fma_f32 v[24:25], v[124:125], s[54:55], v[96:97] op_sel_hi:[0,1,1]
	v_exp_f32_e32 v91, v91
	v_pk_mul_f32 v[92:93], v[84:85], v[12:13] op_sel:[1,0]
	v_pk_mul_f32 v[90:91], v[26:27], v[90:91]
	v_exp_f32_e32 v92, v92
	v_pk_fma_f32 v[26:27], v[124:125], s[56:57], v[90:91] op_sel_hi:[0,1,1]
	v_exp_f32_e32 v93, v93
	v_pk_mul_f32 v[94:95], v[84:85], v[14:15] op_sel:[1,0]
	v_pk_mul_f32 v[92:93], v[28:29], v[92:93]
	v_exp_f32_e32 v94, v94
	v_pk_fma_f32 v[28:29], v[124:125], s[58:59], v[92:93] op_sel_hi:[0,1,1]
	v_exp_f32_e32 v95, v95
	v_pk_mul_f32 v[96:97], v[84:85], v[16:17] op_sel:[1,0]
	v_pk_mul_f32 v[94:95], v[30:31], v[94:95]
	v_exp_f32_e32 v96, v96
	v_pk_fma_f32 v[30:31], v[124:125], s[60:61], v[94:95] op_sel_hi:[0,1,1]
	v_exp_f32_e32 v97, v97
	s_nop 0
	v_pk_mul_f32 v[96:97], v[32:33], v[96:97]
	s_nop 0
	v_pk_fma_f32 v[32:33], v[124:125], s[62:63], v[96:97] op_sel_hi:[0,1,1]
	v_mul_f32_e32 v124, v86, v125
	global_store_dwordx4 v126, v[82:85], s[72:73]
	s_add_u32 s72, s72, 0x8000
	s_addc_u32 s73, s73, 0
	s_waitcnt lgkmcnt(0)
	s_load_dwordx16 s[48:63], s[70:71], 0xe80
	v_fma_f32 v98, v63, s64, v122
	v_mul_f32_e64 v99, -|v98|, s65
	v_cvt_f32_f16_sdwa v125, v80 dst_sel:DWORD dst_unused:UNUSED_PAD src0_sel:WORD_1
	v_exp_f32_e32 v99, v99
	v_max_f32_e32 v98, 0, v98
	v_add_f32_e32 v99, 1.0, v99
	v_log_f32_e32 v99, v99
	v_pk_mul_f32 v[90:91], v[86:87], v[2:3] op_sel_hi:[0,1]
	v_fma_f32 v87, v99, s66, v98
	v_add_f32_e32 v123, v123, v87
	v_exp_f32_e32 v90, v90
	v_exp_f32_e32 v91, v91
	v_pk_mul_f32 v[92:93], v[86:87], v[4:5] op_sel_hi:[0,1]
	v_pk_mul_f32 v[90:91], v[18:19], v[90:91]
	v_exp_f32_e32 v92, v92
	v_pk_fma_f32 v[18:19], v[124:125], s[32:33], v[90:91] op_sel_hi:[0,1,1]
	v_exp_f32_e32 v93, v93
	v_pk_mul_f32 v[94:95], v[86:87], v[6:7] op_sel_hi:[0,1]
	v_pk_mul_f32 v[92:93], v[20:21], v[92:93]
	v_exp_f32_e32 v94, v94
	v_pk_fma_f32 v[20:21], v[124:125], s[34:35], v[92:93] op_sel_hi:[0,1,1]
	v_exp_f32_e32 v95, v95
	v_pk_mul_f32 v[96:97], v[86:87], v[8:9] op_sel_hi:[0,1]
	v_pk_mul_f32 v[94:95], v[22:23], v[94:95]
	v_exp_f32_e32 v96, v96
	v_pk_fma_f32 v[22:23], v[124:125], s[36:37], v[94:95] op_sel_hi:[0,1,1]
	v_exp_f32_e32 v97, v97
	v_pk_mul_f32 v[90:91], v[86:87], v[10:11] op_sel_hi:[0,1]
	v_pk_mul_f32 v[96:97], v[24:25], v[96:97]
	v_exp_f32_e32 v90, v90
	v_pk_fma_f32 v[24:25], v[124:125], s[38:39], v[96:97] op_sel_hi:[0,1,1]
	v_exp_f32_e32 v91, v91
	v_pk_mul_f32 v[92:93], v[86:87], v[12:13] op_sel_hi:[0,1]
	v_pk_mul_f32 v[90:91], v[26:27], v[90:91]
	v_exp_f32_e32 v92, v92
	v_pk_fma_f32 v[26:27], v[124:125], s[40:41], v[90:91] op_sel_hi:[0,1,1]
	v_exp_f32_e32 v93, v93
	v_pk_mul_f32 v[94:95], v[86:87], v[14:15] op_sel_hi:[0,1]
	v_pk_mul_f32 v[92:93], v[28:29], v[92:93]
	v_exp_f32_e32 v94, v94
	v_pk_fma_f32 v[28:29], v[124:125], s[42:43], v[92:93] op_sel_hi:[0,1,1]
	v_exp_f32_e32 v95, v95
	v_pk_mul_f32 v[96:97], v[86:87], v[16:17] op_sel_hi:[0,1]
	v_pk_mul_f32 v[94:95], v[30:31], v[94:95]
	v_exp_f32_e32 v96, v96
	v_pk_fma_f32 v[30:31], v[124:125], s[44:45], v[94:95] op_sel_hi:[0,1,1]
	v_exp_f32_e32 v97, v97
	s_nop 0
	v_pk_mul_f32 v[96:97], v[32:33], v[96:97]
	s_nop 0
	v_pk_fma_f32 v[32:33], v[124:125], s[46:47], v[96:97] op_sel_hi:[0,1,1]
	v_mul_f32_e32 v124, v87, v125
	s_waitcnt lgkmcnt(0)
	s_load_dwordx16 s[32:47], s[70:71], 0xf00
	v_fma_f32 v98, v64, s64, v122
	v_mul_f32_e64 v99, -|v98|, s65
	v_cvt_f32_f16_e32 v125, v81
	v_exp_f32_e32 v99, v99
	v_max_f32_e32 v98, 0, v98
	v_add_f32_e32 v99, 1.0, v99
	v_log_f32_e32 v99, v99
	v_pk_mul_f32 v[90:91], v[86:87], v[2:3] op_sel:[1,0]
	v_fma_f32 v88, v99, s66, v98
	v_add_f32_e32 v123, v123, v88
	v_exp_f32_e32 v90, v90
	v_exp_f32_e32 v91, v91
	v_pk_mul_f32 v[92:93], v[86:87], v[4:5] op_sel:[1,0]
	v_pk_mul_f32 v[90:91], v[18:19], v[90:91]
	v_exp_f32_e32 v92, v92
	v_pk_fma_f32 v[18:19], v[124:125], s[48:49], v[90:91] op_sel_hi:[0,1,1]
	v_exp_f32_e32 v93, v93
	v_pk_mul_f32 v[94:95], v[86:87], v[6:7] op_sel:[1,0]
	v_pk_mul_f32 v[92:93], v[20:21], v[92:93]
	v_exp_f32_e32 v94, v94
	v_pk_fma_f32 v[20:21], v[124:125], s[50:51], v[92:93] op_sel_hi:[0,1,1]
	v_exp_f32_e32 v95, v95
	v_pk_mul_f32 v[96:97], v[86:87], v[8:9] op_sel:[1,0]
	v_pk_mul_f32 v[94:95], v[22:23], v[94:95]
	v_exp_f32_e32 v96, v96
	v_pk_fma_f32 v[22:23], v[124:125], s[52:53], v[94:95] op_sel_hi:[0,1,1]
	v_exp_f32_e32 v97, v97
	v_pk_mul_f32 v[90:91], v[86:87], v[10:11] op_sel:[1,0]
	v_pk_mul_f32 v[96:97], v[24:25], v[96:97]
	v_exp_f32_e32 v90, v90
	v_pk_fma_f32 v[24:25], v[124:125], s[54:55], v[96:97] op_sel_hi:[0,1,1]
	v_exp_f32_e32 v91, v91
	v_pk_mul_f32 v[92:93], v[86:87], v[12:13] op_sel:[1,0]
	v_pk_mul_f32 v[90:91], v[26:27], v[90:91]
	v_exp_f32_e32 v92, v92
	v_pk_fma_f32 v[26:27], v[124:125], s[56:57], v[90:91] op_sel_hi:[0,1,1]
	v_exp_f32_e32 v93, v93
	v_pk_mul_f32 v[94:95], v[86:87], v[14:15] op_sel:[1,0]
	v_pk_mul_f32 v[92:93], v[28:29], v[92:93]
	v_exp_f32_e32 v94, v94
	v_pk_fma_f32 v[28:29], v[124:125], s[58:59], v[92:93] op_sel_hi:[0,1,1]
	v_exp_f32_e32 v95, v95
	v_pk_mul_f32 v[96:97], v[86:87], v[16:17] op_sel:[1,0]
	v_pk_mul_f32 v[94:95], v[30:31], v[94:95]
	v_exp_f32_e32 v96, v96
	v_pk_fma_f32 v[30:31], v[124:125], s[60:61], v[94:95] op_sel_hi:[0,1,1]
	v_exp_f32_e32 v97, v97
	s_nop 0
	v_pk_mul_f32 v[96:97], v[32:33], v[96:97]
	s_nop 0
	v_pk_fma_f32 v[32:33], v[124:125], s[62:63], v[96:97] op_sel_hi:[0,1,1]
	v_mul_f32_e32 v124, v88, v125
	s_waitcnt lgkmcnt(0)
	s_load_dwordx16 s[48:63], s[70:71], 0xf80
	v_fma_f32 v98, v65, s64, v122
	v_mul_f32_e64 v99, -|v98|, s65
	v_cvt_f32_f16_sdwa v125, v81 dst_sel:DWORD dst_unused:UNUSED_PAD src0_sel:WORD_1
	v_exp_f32_e32 v99, v99
	v_max_f32_e32 v98, 0, v98
	v_add_f32_e32 v99, 1.0, v99
	v_log_f32_e32 v99, v99
	v_pk_mul_f32 v[90:91], v[88:89], v[2:3] op_sel_hi:[0,1]
	v_fma_f32 v89, v99, s66, v98
	v_add_f32_e32 v123, v123, v89
	v_exp_f32_e32 v90, v90
	v_exp_f32_e32 v91, v91
	v_pk_mul_f32 v[92:93], v[88:89], v[4:5] op_sel_hi:[0,1]
	v_pk_mul_f32 v[90:91], v[18:19], v[90:91]
	v_exp_f32_e32 v92, v92
	v_pk_fma_f32 v[18:19], v[124:125], s[32:33], v[90:91] op_sel_hi:[0,1,1]
	v_exp_f32_e32 v93, v93
	v_pk_mul_f32 v[94:95], v[88:89], v[6:7] op_sel_hi:[0,1]
	v_pk_mul_f32 v[92:93], v[20:21], v[92:93]
	v_exp_f32_e32 v94, v94
	v_pk_fma_f32 v[20:21], v[124:125], s[34:35], v[92:93] op_sel_hi:[0,1,1]
	v_exp_f32_e32 v95, v95
	v_pk_mul_f32 v[96:97], v[88:89], v[8:9] op_sel_hi:[0,1]
	v_pk_mul_f32 v[94:95], v[22:23], v[94:95]
	v_exp_f32_e32 v96, v96
	v_pk_fma_f32 v[22:23], v[124:125], s[36:37], v[94:95] op_sel_hi:[0,1,1]
	v_exp_f32_e32 v97, v97
	v_pk_mul_f32 v[90:91], v[88:89], v[10:11] op_sel_hi:[0,1]
	v_pk_mul_f32 v[96:97], v[24:25], v[96:97]
	v_exp_f32_e32 v90, v90
	v_pk_fma_f32 v[24:25], v[124:125], s[38:39], v[96:97] op_sel_hi:[0,1,1]
	v_exp_f32_e32 v91, v91
	v_pk_mul_f32 v[92:93], v[88:89], v[12:13] op_sel_hi:[0,1]
	v_pk_mul_f32 v[90:91], v[26:27], v[90:91]
	v_exp_f32_e32 v92, v92
	v_pk_fma_f32 v[26:27], v[124:125], s[40:41], v[90:91] op_sel_hi:[0,1,1]
	v_exp_f32_e32 v93, v93
	v_pk_mul_f32 v[94:95], v[88:89], v[14:15] op_sel_hi:[0,1]
	v_pk_mul_f32 v[92:93], v[28:29], v[92:93]
	v_exp_f32_e32 v94, v94
	v_pk_fma_f32 v[28:29], v[124:125], s[42:43], v[92:93] op_sel_hi:[0,1,1]
	v_exp_f32_e32 v95, v95
	v_pk_mul_f32 v[96:97], v[88:89], v[16:17] op_sel_hi:[0,1]
	v_pk_mul_f32 v[94:95], v[30:31], v[94:95]
	v_exp_f32_e32 v96, v96
	v_pk_fma_f32 v[30:31], v[124:125], s[44:45], v[94:95] op_sel_hi:[0,1,1]
	v_exp_f32_e32 v97, v97
	s_nop 0
	v_pk_mul_f32 v[96:97], v[32:33], v[96:97]
	s_nop 0
	v_pk_fma_f32 v[32:33], v[124:125], s[46:47], v[96:97] op_sel_hi:[0,1,1]
	v_mul_f32_e32 v124, v89, v125
	s_waitcnt lgkmcnt(0)
	v_pk_mul_f32 v[90:91], v[88:89], v[2:3] op_sel:[1,0]
	v_pk_mul_f32 v[92:93], v[88:89], v[4:5] op_sel:[1,0]
	v_exp_f32_e32 v90, v90
	v_exp_f32_e32 v91, v91
	v_exp_f32_e32 v92, v92
	v_pk_mul_f32 v[90:91], v[18:19], v[90:91]
	v_exp_f32_e32 v93, v93
	v_pk_fma_f32 v[18:19], v[124:125], s[48:49], v[90:91] op_sel_hi:[0,1,1]
	v_pk_mul_f32 v[92:93], v[20:21], v[92:93]
	v_pk_mul_f32 v[94:95], v[88:89], v[6:7] op_sel:[1,0]
	v_pk_fma_f32 v[20:21], v[124:125], s[50:51], v[92:93] op_sel_hi:[0,1,1]
	v_exp_f32_e32 v94, v94
	v_exp_f32_e32 v95, v95
	v_pk_mul_f32 v[96:97], v[88:89], v[8:9] op_sel:[1,0]
	v_pk_mul_f32 v[94:95], v[22:23], v[94:95]
	v_exp_f32_e32 v96, v96
	v_pk_fma_f32 v[22:23], v[124:125], s[52:53], v[94:95] op_sel_hi:[0,1,1]
	v_exp_f32_e32 v97, v97
	v_pk_mul_f32 v[90:91], v[88:89], v[10:11] op_sel:[1,0]
	v_pk_mul_f32 v[96:97], v[24:25], v[96:97]
	v_exp_f32_e32 v90, v90
	v_pk_fma_f32 v[24:25], v[124:125], s[54:55], v[96:97] op_sel_hi:[0,1,1]
	v_exp_f32_e32 v91, v91
	v_pk_mul_f32 v[92:93], v[88:89], v[12:13] op_sel:[1,0]
	v_pk_mul_f32 v[90:91], v[26:27], v[90:91]
	v_exp_f32_e32 v92, v92
	v_pk_fma_f32 v[26:27], v[124:125], s[56:57], v[90:91] op_sel_hi:[0,1,1]
	v_exp_f32_e32 v93, v93
	v_pk_mul_f32 v[94:95], v[88:89], v[14:15] op_sel:[1,0]
	v_pk_mul_f32 v[92:93], v[28:29], v[92:93]
	v_exp_f32_e32 v94, v94
	v_pk_fma_f32 v[28:29], v[124:125], s[58:59], v[92:93] op_sel_hi:[0,1,1]
	v_exp_f32_e32 v95, v95
	v_pk_mul_f32 v[96:97], v[88:89], v[16:17] op_sel:[1,0]
	v_pk_mul_f32 v[94:95], v[30:31], v[94:95]
	v_exp_f32_e32 v96, v96
	v_pk_fma_f32 v[30:31], v[124:125], s[60:61], v[94:95] op_sel_hi:[0,1,1]
	v_exp_f32_e32 v97, v97
	s_nop 0
	v_pk_mul_f32 v[96:97], v[32:33], v[96:97]
	s_nop 0
	v_pk_fma_f32 v[32:33], v[124:125], s[62:63], v[96:97] op_sel_hi:[0,1,1]
	global_store_dwordx4 v126, v[86:89], s[72:73]
	s_waitcnt vmcnt(8)
	v_pk_mul_f32 v[114:115], v[114:115], s[86:87] op_sel_hi:[1,0]
	v_pk_mul_f32 v[116:117], v[116:117], s[86:87] op_sel_hi:[1,0]
	v_pk_mul_f32 v[118:119], v[118:119], s[86:87] op_sel_hi:[1,0]
	v_pk_mul_f32 v[120:121], v[120:121], s[86:87] op_sel_hi:[1,0]
	v_cvt_pk_f16_f32 v90, v118, v119
	v_cvt_pk_f16_f32 v91, v120, v121
	v_cvt_pk_f16_f32 v92, v114, v115
	v_cvt_pk_f16_f32 v93, v116, v117
	v_lshlrev_b32_e32 v127, 4, v0
	global_store_dwordx4 v127, v[90:93], s[80:81]
	v_lshlrev_b32_e32 v127, 2, v1
	v_pk_mul_f32 v[18:19], v[18:19], s[84:85] op_sel_hi:[1,0]
	v_pk_mul_f32 v[20:21], v[20:21], s[84:85] op_sel_hi:[1,0]
	v_pk_mul_f32 v[22:23], v[22:23], s[84:85] op_sel_hi:[1,0]
	v_pk_mul_f32 v[24:25], v[24:25], s[84:85] op_sel_hi:[1,0]
	v_pk_mul_f32 v[26:27], v[26:27], s[84:85] op_sel_hi:[1,0]
	v_pk_mul_f32 v[28:29], v[28:29], s[84:85] op_sel_hi:[1,0]
	v_pk_mul_f32 v[30:31], v[30:31], s[84:85] op_sel_hi:[1,0]
	v_pk_mul_f32 v[32:33], v[32:33], s[84:85] op_sel_hi:[1,0]
	v_cvt_pk_f16_f32 v98, v18, v19
	v_cvt_pk_f16_f32 v99, v20, v21
	v_cvt_pk_f16_f32 v100, v22, v23
	v_cvt_pk_f16_f32 v101, v24, v25
	v_cvt_pk_f16_f32 v102, v26, v27
	v_cvt_pk_f16_f32 v103, v28, v29
	v_cvt_pk_f16_f32 v104, v30, v31
	v_cvt_pk_f16_f32 v105, v32, v33
	global_store_dword v127, v98, s[76:77]
	s_add_u32 s76, s76, 0x2000
	s_addc_u32 s77, s77, 0
	global_store_dword v127, v99, s[76:77]
	s_add_u32 s76, s76, 0x2000
	s_addc_u32 s77, s77, 0
	global_store_dword v127, v100, s[76:77]
	s_add_u32 s76, s76, 0x2000
	s_addc_u32 s77, s77, 0
	global_store_dword v127, v101, s[76:77]
	s_add_u32 s76, s76, 0x2000
	s_addc_u32 s77, s77, 0
	global_store_dword v127, v102, s[76:77]
	s_add_u32 s76, s76, 0x2000
	s_addc_u32 s77, s77, 0
	global_store_dword v127, v103, s[76:77]
	s_add_u32 s76, s76, 0x2000
	s_addc_u32 s77, s77, 0
	global_store_dword v127, v104, s[76:77]
	s_add_u32 s76, s76, 0x2000
	s_addc_u32 s77, s77, 0
	global_store_dword v127, v105, s[76:77]
	global_store_dword v127, v123, s[78:79]
	s_endpgm
	.p2alignl 8, 3212836864

	.amdhsa_kernel _Z10scan_pass1PKDF16_S0_PKfS0_S2_S2_PDF16_PfS4_S2_S3_
		.amdhsa_group_segment_fixed_size 4096
		.amdhsa_private_segment_fixed_size 0
		.amdhsa_kernarg_size 88
		.amdhsa_user_sgpr_count 2
		.amdhsa_user_sgpr_dispatch_ptr 0
		.amdhsa_user_sgpr_queue_ptr 0
		.amdhsa_user_sgpr_kernarg_segment_ptr 1
		.amdhsa_user_sgpr_dispatch_id 0
		.amdhsa_user_sgpr_kernarg_preload_length 0
		.amdhsa_user_sgpr_kernarg_preload_offset 0
		.amdhsa_user_sgpr_private_segment_size 0
		.amdhsa_uses_dynamic_stack 0
		.amdhsa_enable_private_segment 0
		.amdhsa_system_sgpr_workgroup_id_x 1
		.amdhsa_system_sgpr_workgroup_id_y 1
		.amdhsa_system_sgpr_workgroup_id_z 1
		.amdhsa_system_sgpr_workgroup_info 0
		.amdhsa_system_vgpr_workitem_id 0
		.amdhsa_next_free_vgpr 128
		.amdhsa_next_free_sgpr 88
		.amdhsa_accum_offset 128
		.amdhsa_reserve_vcc 1
		.amdhsa_float_round_mode_32 0
		.amdhsa_float_round_mode_16_64 0
		.amdhsa_float_denorm_mode_32 3
		.amdhsa_float_denorm_mode_16_64 3
		.amdhsa_dx10_clamp 1
		.amdhsa_ieee_mode 1
		.amdhsa_fp16_overflow 0
		.amdhsa_tg_split 0
		.amdhsa_exception_fp_ieee_invalid_op 0
		.amdhsa_exception_fp_denorm_src 0
		.amdhsa_exception_fp_ieee_div_zero 0
		.amdhsa_exception_fp_ieee_overflow 0
		.amdhsa_exception_fp_ieee_underflow 0
		.amdhsa_exception_fp_ieee_inexact 0
		.amdhsa_exception_int_div_zero 0
	.end_amdhsa_kernel

_Z10scan_pass2PKDF16_PKfS2_S0_S2_S0_PDF16_S2_:
	s_load_dwordx16 s[8:23], s[0:1], 0x0
	s_mov_b32 s28, 0x3e800000
	s_mov_b32 s29, 0x3c800000
	s_mov_b32 s30, 0x40800000
	s_lshl_b32 s5, s4, 11
	s_lshl_b32 s6, s3, 5
	s_add_i32 s5, s5, s6
	s_lshl_b32 s6, s4, 6
	s_add_i32 s6, s6, s3
	v_lshl_or_b32 v1, s2, 8, v0
	v_lshlrev_b32_e32 v99, 1, v1
	v_lshlrev_b32_e32 v100, 6, v1
	v_lshlrev_b32_e32 v101, 2, v1
	v_lshlrev_b32_e32 v102, 4, v1
	v_lshlrev_b32_e32 v103, 3, v1
	s_waitcnt lgkmcnt(0)
	s_lshl_b32 s7, s5, 7
	s_add_u32 s24, s10, s7
	s_addc_u32 s25, s11, 0
	s_load_dwordx16 s[32:47], s[24:25], 0x0
	s_load_dwordx16 s[48:63], s[24:25], 0x40
	global_load_dwordx4 v[2:5], v100, s[12:13]
	global_load_dwordx4 v[6:9], v100, s[12:13] offset:16
	global_load_dwordx4 v[10:13], v100, s[12:13] offset:32
	global_load_dwordx4 v[14:17], v100, s[12:13] offset:48
	s_lshl_b32 s7, s6, 16
	s_add_u32 s96, s14, s7
	s_addc_u32 s97, s15, 0
	global_load_dword v104, v101, s[96:97]
	s_add_u32 s96, s96, 0x2000
	s_addc_u32 s97, s97, 0
	global_load_dword v105, v101, s[96:97]
	s_add_u32 s96, s96, 0x2000
	s_addc_u32 s97, s97, 0
	global_load_dword v106, v101, s[96:97]
	s_add_u32 s96, s96, 0x2000
	s_addc_u32 s97, s97, 0
	global_load_dword v107, v101, s[96:97]
	s_add_u32 s96, s96, 0x2000
	s_addc_u32 s97, s97, 0
	global_load_dword v108, v101, s[96:97]
	s_add_u32 s96, s96, 0x2000
	s_addc_u32 s97, s97, 0
	global_load_dword v109, v101, s[96:97]
	s_add_u32 s96, s96, 0x2000
	s_addc_u32 s97, s97, 0
	global_load_dword v110, v101, s[96:97]
	s_add_u32 s96, s96, 0x2000
	s_addc_u32 s97, s97, 0
	global_load_dword v111, v101, s[96:97]
	s_lshr_b32 s7, s5, 2
	s_lshl_b32 s7, s7, 15
	s_add_u32 s0, s22, s7
	s_addc_u32 s1, s23, 0
	s_add_u32 s2, s18, s7
	s_addc_u32 s3, s19, 0
	s_add_u32 s2, s2, 0x4000
	s_addc_u32 s3, s3, 0
	s_lshr_b32 s7, s5, 3
	s_lshl_b32 s7, s7, 15
	s_add_u32 s8, s8, s7
	s_addc_u32 s9, s9, 0
	s_lshl_b32 s7, s5, 12
	s_add_u32 s26, s20, s7
	s_addc_u32 s27, s21, 0
	global_load_dwordx4 v[34:37], v102, s[0:1]
	s_add_u32 s0, s0, 0x8000
	s_addc_u32 s1, s1, 0
	global_load_dwordx4 v[42:45], v102, s[8:9]
	s_add_u32 s8, s8, 0x8000
	s_addc_u32 s9, s9, 0
	global_load_dwordx2 v[46:47], v103, s[2:3]
	s_add_u32 s2, s2, 0x8000
	s_addc_u32 s3, s3, 0
	global_load_dwordx4 v[38:41], v102, s[0:1]
	s_add_u32 s0, s0, 0x8000
	s_addc_u32 s1, s1, 0
	global_load_dwordx2 v[48:49], v103, s[2:3]
	s_add_u32 s2, s2, 0x8000
	s_addc_u32 s3, s3, 0
	global_load_dword v98, v101, s[16:17]
	global_load_dwordx4 v[50:53], v102, s[0:1]
	s_add_u32 s0, s0, 0x8000
	s_addc_u32 s1, s1, 0
	global_load_dwordx4 v[58:61], v102, s[8:9]
	s_add_u32 s8, s8, 0x8000
	s_addc_u32 s9, s9, 0
	global_load_dwordx2 v[62:63], v103, s[2:3]
	s_add_u32 s2, s2, 0x8000
	s_addc_u32 s3, s3, 0
	global_load_dwordx4 v[54:57], v102, s[0:1]
	s_add_u32 s0, s0, 0x8000
	s_addc_u32 s1, s1, 0
	global_load_dwordx2 v[64:65], v103, s[2:3]
	s_add_u32 s2, s2, 0x8000
	s_addc_u32 s3, s3, 0
	s_waitcnt vmcnt(11)
	v_cvt_f32_f16_e32 v18, v104
	v_cvt_f32_f16_sdwa v19, v104 dst_sel:DWORD dst_unused:UNUSED_PAD src0_sel:WORD_1
	v_cvt_f32_f16_e32 v20, v105
	v_cvt_f32_f16_sdwa v21, v105 dst_sel:DWORD dst_unused:UNUSED_PAD src0_sel:WORD_1
	v_cvt_f32_f16_e32 v22, v106
	v_cvt_f32_f16_sdwa v23, v106 dst_sel:DWORD dst_unused:UNUSED_PAD src0_sel:WORD_1
	v_cvt_f32_f16_e32 v24, v107
	v_cvt_f32_f16_sdwa v25, v107 dst_sel:DWORD dst_unused:UNUSED_PAD src0_sel:WORD_1
	v_cvt_f32_f16_e32 v26, v108
	v_cvt_f32_f16_sdwa v27, v108 dst_sel:DWORD dst_unused:UNUSED_PAD src0_sel:WORD_1
	v_cvt_f32_f16_e32 v28, v109
	v_cvt_f32_f16_sdwa v29, v109 dst_sel:DWORD dst_unused:UNUSED_PAD src0_sel:WORD_1
	v_cvt_f32_f16_e32 v30, v110
	v_cvt_f32_f16_sdwa v31, v110 dst_sel:DWORD dst_unused:UNUSED_PAD src0_sel:WORD_1
	v_cvt_f32_f16_e32 v32, v111
	v_cvt_f32_f16_sdwa v33, v111 dst_sel:DWORD dst_unused:UNUSED_PAD src0_sel:WORD_1
	v_pk_mul_f32 v[18:19], v[18:19], s[28:29] op_sel_hi:[1,0]
	v_pk_mul_f32 v[20:21], v[20:21], s[28:29] op_sel_hi:[1,0]
	v_pk_mul_f32 v[22:23], v[22:23], s[28:29] op_sel_hi:[1,0]
	v_pk_mul_f32 v[24:25], v[24:25], s[28:29] op_sel_hi:[1,0]
	v_pk_mul_f32 v[26:27], v[26:27], s[28:29] op_sel_hi:[1,0]
	v_pk_mul_f32 v[28:29], v[28:29], s[28:29] op_sel_hi:[1,0]
	v_pk_mul_f32 v[30:31], v[30:31], s[28:29] op_sel_hi:[1,0]
	v_pk_mul_f32 v[32:33], v[32:33], s[28:29] op_sel_hi:[1,0]
	s_waitcnt vmcnt(5)
	global_load_dwordx4 v[66:69], v102, s[0:1]
	s_add_u32 s0, s0, 0x8000
	s_addc_u32 s1, s1, 0
	global_load_dwordx4 v[74:77], v102, s[8:9]
	s_add_u32 s8, s8, 0x8000
	s_addc_u32 s9, s9, 0
	global_load_dwordx2 v[78:79], v103, s[2:3]
	s_add_u32 s2, s2, 0x8000
	s_addc_u32 s3, s3, 0
	global_load_dwordx4 v[70:73], v102, s[0:1]
	s_add_u32 s0, s0, 0x8000
	s_addc_u32 s1, s1, 0
	global_load_dwordx2 v[80:81], v103, s[2:3]
	s_add_u32 s2, s2, 0x8000
	s_addc_u32 s3, s3, 0
	s_waitcnt lgkmcnt(0)
	s_load_dwordx16 s[64:79], s[24:25], 0x80
	s_load_dwordx16 s[80:95], s[24:25], 0xc0
	v_cvt_f32_f16_e32 v113, v42
	v_mul_f32_e32 v112, v34, v113
	v_pk_mul_f32 v[104:105], v[34:35], v[2:3] op_sel_hi:[0,1]
	v_pk_mul_f32 v[106:107], v[34:35], v[4:5] op_sel_hi:[0,1]
	v_exp_f32_e32 v104, v104
	v_exp_f32_e32 v105, v105
	v_exp_f32_e32 v106, v106
	v_pk_mul_f32 v[104:105], v[18:19], v[104:105]
	v_exp_f32_e32 v107, v107
	v_pk_fma_f32 v[18:19], v[112:113], s[32:33], v[104:105] op_sel_hi:[0,1,1]
	v_pk_mul_f32 v[106:107], v[20:21], v[106:107]
	v_pk_fma_f32 v[114:115], s[48:49], v[18:19], 0 op_sel_hi:[1,1,0]
	v_pk_fma_f32 v[20:21], v[112:113], s[34:35], v[106:107] op_sel_hi:[0,1,1]
	v_pk_mul_f32 v[108:109], v[34:35], v[6:7] op_sel_hi:[0,1]
	v_pk_fma_f32 v[114:115], s[50:51], v[20:21], v[114:115]
	v_exp_f32_e32 v108, v108
	v_exp_f32_e32 v109, v109
	v_pk_mul_f32 v[110:111], v[34:35], v[8:9] op_sel_hi:[0,1]
	v_pk_mul_f32 v[108:109], v[22:23], v[108:109]
	v_exp_f32_e32 v110, v110
	v_pk_fma_f32 v[22:23], v[112:113], s[36:37], v[108:109] op_sel_hi:[0,1,1]
	v_exp_f32_e32 v111, v111
	v_pk_fma_f32 v[114:115], s[52:53], v[22:23], v[114:115]
	v_pk_mul_f32 v[110:111], v[24:25], v[110:111]
	v_pk_mul_f32 v[104:105], v[34:35], v[10:11] op_sel_hi:[0,1]
	v_pk_fma_f32 v[24:25], v[112:113], s[38:39], v[110:111] op_sel_hi:[0,1,1]
	v_exp_f32_e32 v104, v104
	v_pk_fma_f32 v[114:115], s[54:55], v[24:25], v[114:115]
	v_exp_f32_e32 v105, v105
	v_pk_mul_f32 v[106:107], v[34:35], v[12:13] op_sel_hi:[0,1]
	v_pk_mul_f32 v[104:105], v[26:27], v[104:105]
	v_exp_f32_e32 v106, v106
	v_pk_fma_f32 v[26:27], v[112:113], s[40:41], v[104:105] op_sel_hi:[0,1,1]
	v_exp_f32_e32 v107, v107
	v_pk_fma_f32 v[114:115], s[56:57], v[26:27], v[114:115]
	v_pk_mul_f32 v[106:107], v[28:29], v[106:107]
	v_pk_mul_f32 v[108:109], v[34:35], v[14:15] op_sel_hi:[0,1]
	v_pk_fma_f32 v[28:29], v[112:113], s[42:43], v[106:107] op_sel_hi:[0,1,1]
	v_exp_f32_e32 v108, v108
	v_pk_fma_f32 v[114:115], s[58:59], v[28:29], v[114:115]
	v_exp_f32_e32 v109, v109
	v_pk_mul_f32 v[110:111], v[34:35], v[16:17] op_sel_hi:[0,1]
	v_pk_mul_f32 v[108:109], v[30:31], v[108:109]
	v_exp_f32_e32 v110, v110
	v_pk_fma_f32 v[30:31], v[112:113], s[44:45], v[108:109] op_sel_hi:[0,1,1]
	v_exp_f32_e32 v111, v111
	v_pk_fma_f32 v[114:115], s[60:61], v[30:31], v[114:115]
	v_pk_mul_f32 v[110:111], v[32:33], v[110:111]
	v_cvt_f32_f16_e32 v117, v46
	v_pk_fma_f32 v[32:33], v[112:113], s[46:47], v[110:111] op_sel_hi:[0,1,1]
	s_nop 0
	v_pk_fma_f32 v[114:115], s[62:63], v[32:33], v[114:115]
	s_nop 0
	v_add_f32_e32 v116, v114, v115
	v_fmac_f32_e32 v116, v98, v113
	v_mul_f32_e32 v116, v116, v117
	v_fma_mixlo_f16 v116, v116, s30, 0
	global_store_short v99, v116, s[26:27]
	s_add_u32 s26, s26, 0x1000
	s_addc_u32 s27, s27, 0
	s_waitcnt lgkmcnt(0)
	s_load_dwordx16 s[32:47], s[24:25], 0x100
	s_load_dwordx16 s[48:63], s[24:25], 0x140
	v_cvt_f32_f16_sdwa v113, v42 dst_sel:DWORD dst_unused:UNUSED_PAD src0_sel:WORD_1
	v_pk_mul_f32 v[104:105], v[34:35], v[2:3] op_sel:[1,0]
	v_mul_f32_e32 v112, v35, v113
	v_exp_f32_e32 v104, v104
	v_exp_f32_e32 v105, v105
	v_pk_mul_f32 v[106:107], v[34:35], v[4:5] op_sel:[1,0]
	v_pk_mul_f32 v[104:105], v[18:19], v[104:105]
	v_exp_f32_e32 v106, v106
	v_pk_fma_f32 v[18:19], v[112:113], s[64:65], v[104:105] op_sel_hi:[0,1,1]
	v_exp_f32_e32 v107, v107
	v_pk_fma_f32 v[114:115], s[80:81], v[18:19], 0 op_sel_hi:[1,1,0]
	v_pk_mul_f32 v[106:107], v[20:21], v[106:107]
	v_pk_mul_f32 v[108:109], v[34:35], v[6:7] op_sel:[1,0]
	v_pk_fma_f32 v[20:21], v[112:113], s[66:67], v[106:107] op_sel_hi:[0,1,1]
	v_exp_f32_e32 v108, v108
	v_pk_fma_f32 v[114:115], s[82:83], v[20:21], v[114:115]
	v_exp_f32_e32 v109, v109
	v_pk_mul_f32 v[110:111], v[34:35], v[8:9] op_sel:[1,0]
	v_pk_mul_f32 v[108:109], v[22:23], v[108:109]
	v_exp_f32_e32 v110, v110
	v_pk_fma_f32 v[22:23], v[112:113], s[68:69], v[108:109] op_sel_hi:[0,1,1]
	v_exp_f32_e32 v111, v111
	v_pk_fma_f32 v[114:115], s[84:85], v[22:23], v[114:115]
	v_pk_mul_f32 v[110:111], v[24:25], v[110:111]
	v_pk_mul_f32 v[104:105], v[34:35], v[10:11] op_sel:[1,0]
	v_pk_fma_f32 v[24:25], v[112:113], s[70:71], v[110:111] op_sel_hi:[0,1,1]
	v_exp_f32_e32 v104, v104
	v_pk_fma_f32 v[114:115], s[86:87], v[24:25], v[114:115]
	v_exp_f32_e32 v105, v105
	v_pk_mul_f32 v[106:107], v[34:35], v[12:13] op_sel:[1,0]
	v_pk_mul_f32 v[104:105], v[26:27], v[104:105]
	v_exp_f32_e32 v106, v106
	v_pk_fma_f32 v[26:27], v[112:113], s[72:73], v[104:105] op_sel_hi:[0,1,1]
	v_exp_f32_e32 v107, v107
	v_pk_fma_f32 v[114:115], s[88:89], v[26:27], v[114:115]
	v_pk_mul_f32 v[106:107], v[28:29], v[106:107]
	v_pk_mul_f32 v[108:109], v[34:35], v[14:15] op_sel:[1,0]
	v_pk_fma_f32 v[28:29], v[112:113], s[74:75], v[106:107] op_sel_hi:[0,1,1]
	v_exp_f32_e32 v108, v108
	v_pk_fma_f32 v[114:115], s[90:91], v[28:29], v[114:115]
	v_exp_f32_e32 v109, v109
	v_pk_mul_f32 v[110:111], v[34:35], v[16:17] op_sel:[1,0]
	v_pk_mul_f32 v[108:109], v[30:31], v[108:109]
	v_exp_f32_e32 v110, v110
	v_pk_fma_f32 v[30:31], v[112:113], s[76:77], v[108:109] op_sel_hi:[0,1,1]
	v_exp_f32_e32 v111, v111
	v_pk_fma_f32 v[114:115], s[92:93], v[30:31], v[114:115]
	v_pk_mul_f32 v[110:111], v[32:33], v[110:111]
	v_cvt_f32_f16_sdwa v117, v46 dst_sel:DWORD dst_unused:UNUSED_PAD src0_sel:WORD_1
	v_pk_fma_f32 v[32:33], v[112:113], s[78:79], v[110:111] op_sel_hi:[0,1,1]
	s_nop 0
	v_pk_fma_f32 v[114:115], s[94:95], v[32:33], v[114:115]
	s_nop 0
	v_add_f32_e32 v116, v114, v115
	v_fmac_f32_e32 v116, v98, v113
	v_mul_f32_e32 v116, v116, v117
	v_fma_mixlo_f16 v116, v116, s30, 0
	global_store_short v99, v116, s[26:27]
	s_add_u32 s26, s26, 0x1000
	s_addc_u32 s27, s27, 0
	s_waitcnt lgkmcnt(0)
	s_load_dwordx16 s[64:79], s[24:25], 0x180
	s_load_dwordx16 s[80:95], s[24:25], 0x1c0
	v_cvt_f32_f16_e32 v113, v43
	v_mul_f32_e32 v112, v36, v113
	v_pk_mul_f32 v[104:105], v[36:37], v[2:3] op_sel_hi:[0,1]
	v_pk_mul_f32 v[106:107], v[36:37], v[4:5] op_sel_hi:[0,1]
	v_exp_f32_e32 v104, v104
	v_exp_f32_e32 v105, v105
	v_exp_f32_e32 v106, v106
	v_pk_mul_f32 v[104:105], v[18:19], v[104:105]
	v_exp_f32_e32 v107, v107
	v_pk_fma_f32 v[18:19], v[112:113], s[32:33], v[104:105] op_sel_hi:[0,1,1]
	v_pk_mul_f32 v[106:107], v[20:21], v[106:107]
	v_pk_fma_f32 v[114:115], s[48:49], v[18:19], 0 op_sel_hi:[1,1,0]
	v_pk_fma_f32 v[20:21], v[112:113], s[34:35], v[106:107] op_sel_hi:[0,1,1]
	v_pk_mul_f32 v[108:109], v[36:37], v[6:7] op_sel_hi:[0,1]
	v_pk_fma_f32 v[114:115], s[50:51], v[20:21], v[114:115]
	v_exp_f32_e32 v108, v108
	v_exp_f32_e32 v109, v109
	v_pk_mul_f32 v[110:111], v[36:37], v[8:9] op_sel_hi:[0,1]
	v_pk_mul_f32 v[108:109], v[22:23], v[108:109]
	v_exp_f32_e32 v110, v110
	v_pk_fma_f32 v[22:23], v[112:113], s[36:37], v[108:109] op_sel_hi:[0,1,1]
	v_exp_f32_e32 v111, v111
	v_pk_fma_f32 v[114:115], s[52:53], v[22:23], v[114:115]
	v_pk_mul_f32 v[110:111], v[24:25], v[110:111]
	v_pk_mul_f32 v[104:105], v[36:37], v[10:11] op_sel_hi:[0,1]
	v_pk_fma_f32 v[24:25], v[112:113], s[38:39], v[110:111] op_sel_hi:[0,1,1]
	v_exp_f32_e32 v104, v104
	v_pk_fma_f32 v[114:115], s[54:55], v[24:25], v[114:115]
	v_exp_f32_e32 v105, v105
	v_pk_mul_f32 v[106:107], v[36:37], v[12:13] op_sel_hi:[0,1]
	v_pk_mul_f32 v[104:105], v[26:27], v[104:105]
	v_exp_f32_e32 v106, v106
	v_pk_fma_f32 v[26:27], v[112:113], s[40:41], v[104:105] op_sel_hi:[0,1,1]
	v_exp_f32_e32 v107, v107
	v_pk_fma_f32 v[114:115], s[56:57], v[26:27], v[114:115]
	v_pk_mul_f32 v[106:107], v[28:29], v[106:107]
	v_pk_mul_f32 v[108:109], v[36:37], v[14:15] op_sel_hi:[0,1]
	v_pk_fma_f32 v[28:29], v[112:113], s[42:43], v[106:107] op_sel_hi:[0,1,1]
	v_exp_f32_e32 v108, v108
	v_pk_fma_f32 v[114:115], s[58:59], v[28:29], v[114:115]
	v_exp_f32_e32 v109, v109
	v_pk_mul_f32 v[110:111], v[36:37], v[16:17] op_sel_hi:[0,1]
	v_pk_mul_f32 v[108:109], v[30:31], v[108:109]
	v_exp_f32_e32 v110, v110
	v_pk_fma_f32 v[30:31], v[112:113], s[44:45], v[108:109] op_sel_hi:[0,1,1]
	v_exp_f32_e32 v111, v111
	v_pk_fma_f32 v[114:115], s[60:61], v[30:31], v[114:115]
	v_pk_mul_f32 v[110:111], v[32:33], v[110:111]
	v_cvt_f32_f16_e32 v117, v47
	v_pk_fma_f32 v[32:33], v[112:113], s[46:47], v[110:111] op_sel_hi:[0,1,1]
	s_nop 0
	v_pk_fma_f32 v[114:115], s[62:63], v[32:33], v[114:115]
	s_nop 0
	v_add_f32_e32 v116, v114, v115
	v_fmac_f32_e32 v116, v98, v113
	v_mul_f32_e32 v116, v116, v117
	v_fma_mixlo_f16 v116, v116, s30, 0
	global_store_short v99, v116, s[26:27]
	s_add_u32 s26, s26, 0x1000
	s_addc_u32 s27, s27, 0
	s_waitcnt lgkmcnt(0)
	s_load_dwordx16 s[32:47], s[24:25], 0x200
	s_load_dwordx16 s[48:63], s[24:25], 0x240
	v_cvt_f32_f16_sdwa v113, v43 dst_sel:DWORD dst_unused:UNUSED_PAD src0_sel:WORD_1
	v_pk_mul_f32 v[104:105], v[36:37], v[2:3] op_sel:[1,0]
	v_mul_f32_e32 v112, v37, v113
	v_exp_f32_e32 v104, v104
	v_exp_f32_e32 v105, v105
	v_pk_mul_f32 v[106:107], v[36:37], v[4:5] op_sel:[1,0]
	v_pk_mul_f32 v[104:105], v[18:19], v[104:105]
	v_exp_f32_e32 v106, v106
	v_pk_fma_f32 v[18:19], v[112:113], s[64:65], v[104:105] op_sel_hi:[0,1,1]
	v_exp_f32_e32 v107, v107
	v_pk_fma_f32 v[114:115], s[80:81], v[18:19], 0 op_sel_hi:[1,1,0]
	v_pk_mul_f32 v[106:107], v[20:21], v[106:107]
	v_pk_mul_f32 v[108:109], v[36:37], v[6:7] op_sel:[1,0]
	v_pk_fma_f32 v[20:21], v[112:113], s[66:67], v[106:107] op_sel_hi:[0,1,1]
	v_exp_f32_e32 v108, v108
	v_pk_fma_f32 v[114:115], s[82:83], v[20:21], v[114:115]
	v_exp_f32_e32 v109, v109
	v_pk_mul_f32 v[110:111], v[36:37], v[8:9] op_sel:[1,0]
	v_pk_mul_f32 v[108:109], v[22:23], v[108:109]
	v_exp_f32_e32 v110, v110
	v_pk_fma_f32 v[22:23], v[112:113], s[68:69], v[108:109] op_sel_hi:[0,1,1]
	v_exp_f32_e32 v111, v111
	v_pk_fma_f32 v[114:115], s[84:85], v[22:23], v[114:115]
	v_pk_mul_f32 v[110:111], v[24:25], v[110:111]
	v_pk_mul_f32 v[104:105], v[36:37], v[10:11] op_sel:[1,0]
	v_pk_fma_f32 v[24:25], v[112:113], s[70:71], v[110:111] op_sel_hi:[0,1,1]
	v_exp_f32_e32 v104, v104
	v_pk_fma_f32 v[114:115], s[86:87], v[24:25], v[114:115]
	v_exp_f32_e32 v105, v105
	v_pk_mul_f32 v[106:107], v[36:37], v[12:13] op_sel:[1,0]
	v_pk_mul_f32 v[104:105], v[26:27], v[104:105]
	v_exp_f32_e32 v106, v106
	v_pk_fma_f32 v[26:27], v[112:113], s[72:73], v[104:105] op_sel_hi:[0,1,1]
	v_exp_f32_e32 v107, v107
	v_pk_fma_f32 v[114:115], s[88:89], v[26:27], v[114:115]
	v_pk_mul_f32 v[106:107], v[28:29], v[106:107]
	v_pk_mul_f32 v[108:109], v[36:37], v[14:15] op_sel:[1,0]
	v_pk_fma_f32 v[28:29], v[112:113], s[74:75], v[106:107] op_sel_hi:[0,1,1]
	v_exp_f32_e32 v108, v108
	v_pk_fma_f32 v[114:115], s[90:91], v[28:29], v[114:115]
	v_exp_f32_e32 v109, v109
	v_pk_mul_f32 v[110:111], v[36:37], v[16:17] op_sel:[1,0]
	v_pk_mul_f32 v[108:109], v[30:31], v[108:109]
	v_exp_f32_e32 v110, v110
	v_pk_fma_f32 v[30:31], v[112:113], s[76:77], v[108:109] op_sel_hi:[0,1,1]
	v_exp_f32_e32 v111, v111
	v_pk_fma_f32 v[114:115], s[92:93], v[30:31], v[114:115]
	v_pk_mul_f32 v[110:111], v[32:33], v[110:111]
	v_cvt_f32_f16_sdwa v117, v47 dst_sel:DWORD dst_unused:UNUSED_PAD src0_sel:WORD_1
	v_pk_fma_f32 v[32:33], v[112:113], s[78:79], v[110:111] op_sel_hi:[0,1,1]
	s_nop 0
	v_pk_fma_f32 v[114:115], s[94:95], v[32:33], v[114:115]
	s_nop 0
	v_add_f32_e32 v116, v114, v115
	v_fmac_f32_e32 v116, v98, v113
	v_mul_f32_e32 v116, v116, v117
	v_fma_mixlo_f16 v116, v116, s30, 0
	global_store_short v99, v116, s[26:27]
	s_add_u32 s26, s26, 0x1000
	s_addc_u32 s27, s27, 0
	s_waitcnt lgkmcnt(0)
	s_load_dwordx16 s[64:79], s[24:25], 0x280
	s_load_dwordx16 s[80:95], s[24:25], 0x2c0
	v_cvt_f32_f16_e32 v113, v44
	v_mul_f32_e32 v112, v38, v113
	v_pk_mul_f32 v[104:105], v[38:39], v[2:3] op_sel_hi:[0,1]
	v_pk_mul_f32 v[106:107], v[38:39], v[4:5] op_sel_hi:[0,1]
	v_exp_f32_e32 v104, v104
	v_exp_f32_e32 v105, v105
	v_exp_f32_e32 v106, v106
	v_pk_mul_f32 v[104:105], v[18:19], v[104:105]
	v_exp_f32_e32 v107, v107
	v_pk_fma_f32 v[18:19], v[112:113], s[32:33], v[104:105] op_sel_hi:[0,1,1]
	v_pk_mul_f32 v[106:107], v[20:21], v[106:107]
	v_pk_fma_f32 v[114:115], s[48:49], v[18:19], 0 op_sel_hi:[1,1,0]
	v_pk_fma_f32 v[20:21], v[112:113], s[34:35], v[106:107] op_sel_hi:[0,1,1]
	v_pk_mul_f32 v[108:109], v[38:39], v[6:7] op_sel_hi:[0,1]
	v_pk_fma_f32 v[114:115], s[50:51], v[20:21], v[114:115]
	v_exp_f32_e32 v108, v108
	v_exp_f32_e32 v109, v109
	v_pk_mul_f32 v[110:111], v[38:39], v[8:9] op_sel_hi:[0,1]
	v_pk_mul_f32 v[108:109], v[22:23], v[108:109]
	v_exp_f32_e32 v110, v110
	v_pk_fma_f32 v[22:23], v[112:113], s[36:37], v[108:109] op_sel_hi:[0,1,1]
	v_exp_f32_e32 v111, v111
	v_pk_fma_f32 v[114:115], s[52:53], v[22:23], v[114:115]
	v_pk_mul_f32 v[110:111], v[24:25], v[110:111]
	v_pk_mul_f32 v[104:105], v[38:39], v[10:11] op_sel_hi:[0,1]
	v_pk_fma_f32 v[24:25], v[112:113], s[38:39], v[110:111] op_sel_hi:[0,1,1]
	v_exp_f32_e32 v104, v104
	v_pk_fma_f32 v[114:115], s[54:55], v[24:25], v[114:115]
	v_exp_f32_e32 v105, v105
	v_pk_mul_f32 v[106:107], v[38:39], v[12:13] op_sel_hi:[0,1]
	v_pk_mul_f32 v[104:105], v[26:27], v[104:105]
	v_exp_f32_e32 v106, v106
	v_pk_fma_f32 v[26:27], v[112:113], s[40:41], v[104:105] op_sel_hi:[0,1,1]
	v_exp_f32_e32 v107, v107
	v_pk_fma_f32 v[114:115], s[56:57], v[26:27], v[114:115]
	v_pk_mul_f32 v[106:107], v[28:29], v[106:107]
	v_pk_mul_f32 v[108:109], v[38:39], v[14:15] op_sel_hi:[0,1]
	v_pk_fma_f32 v[28:29], v[112:113], s[42:43], v[106:107] op_sel_hi:[0,1,1]
	v_exp_f32_e32 v108, v108
	v_pk_fma_f32 v[114:115], s[58:59], v[28:29], v[114:115]
	v_exp_f32_e32 v109, v109
	v_pk_mul_f32 v[110:111], v[38:39], v[16:17] op_sel_hi:[0,1]
	v_pk_mul_f32 v[108:109], v[30:31], v[108:109]
	v_exp_f32_e32 v110, v110
	v_pk_fma_f32 v[30:31], v[112:113], s[44:45], v[108:109] op_sel_hi:[0,1,1]
	v_exp_f32_e32 v111, v111
	v_pk_fma_f32 v[114:115], s[60:61], v[30:31], v[114:115]
	v_pk_mul_f32 v[110:111], v[32:33], v[110:111]
	v_cvt_f32_f16_e32 v117, v48
	v_pk_fma_f32 v[32:33], v[112:113], s[46:47], v[110:111] op_sel_hi:[0,1,1]
	s_nop 0
	v_pk_fma_f32 v[114:115], s[62:63], v[32:33], v[114:115]
	s_nop 0
	v_add_f32_e32 v116, v114, v115
	v_fmac_f32_e32 v116, v98, v113
	v_mul_f32_e32 v116, v116, v117
	v_fma_mixlo_f16 v116, v116, s30, 0
	global_store_short v99, v116, s[26:27]
	s_add_u32 s26, s26, 0x1000
	s_addc_u32 s27, s27, 0
	s_waitcnt lgkmcnt(0)
	s_load_dwordx16 s[32:47], s[24:25], 0x300
	s_load_dwordx16 s[48:63], s[24:25], 0x340
	v_cvt_f32_f16_sdwa v113, v44 dst_sel:DWORD dst_unused:UNUSED_PAD src0_sel:WORD_1
	v_pk_mul_f32 v[104:105], v[38:39], v[2:3] op_sel:[1,0]
	v_mul_f32_e32 v112, v39, v113
	v_exp_f32_e32 v104, v104
	v_exp_f32_e32 v105, v105
	v_pk_mul_f32 v[106:107], v[38:39], v[4:5] op_sel:[1,0]
	v_pk_mul_f32 v[104:105], v[18:19], v[104:105]
	v_exp_f32_e32 v106, v106
	v_pk_fma_f32 v[18:19], v[112:113], s[64:65], v[104:105] op_sel_hi:[0,1,1]
	v_exp_f32_e32 v107, v107
	v_pk_fma_f32 v[114:115], s[80:81], v[18:19], 0 op_sel_hi:[1,1,0]
	v_pk_mul_f32 v[106:107], v[20:21], v[106:107]
	v_pk_mul_f32 v[108:109], v[38:39], v[6:7] op_sel:[1,0]
	v_pk_fma_f32 v[20:21], v[112:113], s[66:67], v[106:107] op_sel_hi:[0,1,1]
	v_exp_f32_e32 v108, v108
	v_pk_fma_f32 v[114:115], s[82:83], v[20:21], v[114:115]
	v_exp_f32_e32 v109, v109
	v_pk_mul_f32 v[110:111], v[38:39], v[8:9] op_sel:[1,0]
	v_pk_mul_f32 v[108:109], v[22:23], v[108:109]
	v_exp_f32_e32 v110, v110
	v_pk_fma_f32 v[22:23], v[112:113], s[68:69], v[108:109] op_sel_hi:[0,1,1]
	v_exp_f32_e32 v111, v111
	v_pk_fma_f32 v[114:115], s[84:85], v[22:23], v[114:115]
	v_pk_mul_f32 v[110:111], v[24:25], v[110:111]
	v_pk_mul_f32 v[104:105], v[38:39], v[10:11] op_sel:[1,0]
	v_pk_fma_f32 v[24:25], v[112:113], s[70:71], v[110:111] op_sel_hi:[0,1,1]
	v_exp_f32_e32 v104, v104
	v_pk_fma_f32 v[114:115], s[86:87], v[24:25], v[114:115]
	v_exp_f32_e32 v105, v105
	v_pk_mul_f32 v[106:107], v[38:39], v[12:13] op_sel:[1,0]
	v_pk_mul_f32 v[104:105], v[26:27], v[104:105]
	v_exp_f32_e32 v106, v106
	v_pk_fma_f32 v[26:27], v[112:113], s[72:73], v[104:105] op_sel_hi:[0,1,1]
	v_exp_f32_e32 v107, v107
	v_pk_fma_f32 v[114:115], s[88:89], v[26:27], v[114:115]
	v_pk_mul_f32 v[106:107], v[28:29], v[106:107]
	v_pk_mul_f32 v[108:109], v[38:39], v[14:15] op_sel:[1,0]
	v_pk_fma_f32 v[28:29], v[112:113], s[74:75], v[106:107] op_sel_hi:[0,1,1]
	v_exp_f32_e32 v108, v108
	v_pk_fma_f32 v[114:115], s[90:91], v[28:29], v[114:115]
	v_exp_f32_e32 v109, v109
	v_pk_mul_f32 v[110:111], v[38:39], v[16:17] op_sel:[1,0]
	v_pk_mul_f32 v[108:109], v[30:31], v[108:109]
	v_exp_f32_e32 v110, v110
	v_pk_fma_f32 v[30:31], v[112:113], s[76:77], v[108:109] op_sel_hi:[0,1,1]
	v_exp_f32_e32 v111, v111
	v_pk_fma_f32 v[114:115], s[92:93], v[30:31], v[114:115]
	v_pk_mul_f32 v[110:111], v[32:33], v[110:111]
	v_cvt_f32_f16_sdwa v117, v48 dst_sel:DWORD dst_unused:UNUSED_PAD src0_sel:WORD_1
	v_pk_fma_f32 v[32:33], v[112:113], s[78:79], v[110:111] op_sel_hi:[0,1,1]
	s_nop 0
	v_pk_fma_f32 v[114:115], s[94:95], v[32:33], v[114:115]
	s_nop 0
	v_add_f32_e32 v116, v114, v115
	v_fmac_f32_e32 v116, v98, v113
	v_mul_f32_e32 v116, v116, v117
	v_fma_mixlo_f16 v116, v116, s30, 0
	global_store_short v99, v116, s[26:27]
	s_add_u32 s26, s26, 0x1000
	s_addc_u32 s27, s27, 0
	s_waitcnt lgkmcnt(0)
	s_load_dwordx16 s[64:79], s[24:25], 0x380
	s_load_dwordx16 s[80:95], s[24:25], 0x3c0
	v_cvt_f32_f16_e32 v113, v45
	v_mul_f32_e32 v112, v40, v113
	v_pk_mul_f32 v[104:105], v[40:41], v[2:3] op_sel_hi:[0,1]
	v_pk_mul_f32 v[106:107], v[40:41], v[4:5] op_sel_hi:[0,1]
	v_exp_f32_e32 v104, v104
	v_exp_f32_e32 v105, v105
	v_exp_f32_e32 v106, v106
	v_pk_mul_f32 v[104:105], v[18:19], v[104:105]
	v_exp_f32_e32 v107, v107
	v_pk_fma_f32 v[18:19], v[112:113], s[32:33], v[104:105] op_sel_hi:[0,1,1]
	v_pk_mul_f32 v[106:107], v[20:21], v[106:107]
	v_pk_fma_f32 v[114:115], s[48:49], v[18:19], 0 op_sel_hi:[1,1,0]
	v_pk_fma_f32 v[20:21], v[112:113], s[34:35], v[106:107] op_sel_hi:[0,1,1]
	v_pk_mul_f32 v[108:109], v[40:41], v[6:7] op_sel_hi:[0,1]
	v_pk_fma_f32 v[114:115], s[50:51], v[20:21], v[114:115]
	v_exp_f32_e32 v108, v108
	v_exp_f32_e32 v109, v109
	v_pk_mul_f32 v[110:111], v[40:41], v[8:9] op_sel_hi:[0,1]
	v_pk_mul_f32 v[108:109], v[22:23], v[108:109]
	v_exp_f32_e32 v110, v110
	v_pk_fma_f32 v[22:23], v[112:113], s[36:37], v[108:109] op_sel_hi:[0,1,1]
	v_exp_f32_e32 v111, v111
	v_pk_fma_f32 v[114:115], s[52:53], v[22:23], v[114:115]
	v_pk_mul_f32 v[110:111], v[24:25], v[110:111]
	v_pk_mul_f32 v[104:105], v[40:41], v[10:11] op_sel_hi:[0,1]
	v_pk_fma_f32 v[24:25], v[112:113], s[38:39], v[110:111] op_sel_hi:[0,1,1]
	v_exp_f32_e32 v104, v104
	v_pk_fma_f32 v[114:115], s[54:55], v[24:25], v[114:115]
	v_exp_f32_e32 v105, v105
	v_pk_mul_f32 v[106:107], v[40:41], v[12:13] op_sel_hi:[0,1]
	v_pk_mul_f32 v[104:105], v[26:27], v[104:105]
	v_exp_f32_e32 v106, v106
	v_pk_fma_f32 v[26:27], v[112:113], s[40:41], v[104:105] op_sel_hi:[0,1,1]
	v_exp_f32_e32 v107, v107
	v_pk_fma_f32 v[114:115], s[56:57], v[26:27], v[114:115]
	v_pk_mul_f32 v[106:107], v[28:29], v[106:107]
	v_pk_mul_f32 v[108:109], v[40:41], v[14:15] op_sel_hi:[0,1]
	v_pk_fma_f32 v[28:29], v[112:113], s[42:43], v[106:107] op_sel_hi:[0,1,1]
	v_exp_f32_e32 v108, v108
	v_pk_fma_f32 v[114:115], s[58:59], v[28:29], v[114:115]
	v_exp_f32_e32 v109, v109
	v_pk_mul_f32 v[110:111], v[40:41], v[16:17] op_sel_hi:[0,1]
	v_pk_mul_f32 v[108:109], v[30:31], v[108:109]
	v_exp_f32_e32 v110, v110
	v_pk_fma_f32 v[30:31], v[112:113], s[44:45], v[108:109] op_sel_hi:[0,1,1]
	v_exp_f32_e32 v111, v111
	v_pk_fma_f32 v[114:115], s[60:61], v[30:31], v[114:115]
	v_pk_mul_f32 v[110:111], v[32:33], v[110:111]
	v_cvt_f32_f16_e32 v117, v49
	v_pk_fma_f32 v[32:33], v[112:113], s[46:47], v[110:111] op_sel_hi:[0,1,1]
	s_nop 0
	v_pk_fma_f32 v[114:115], s[62:63], v[32:33], v[114:115]
	s_nop 0
	v_add_f32_e32 v116, v114, v115
	v_fmac_f32_e32 v116, v98, v113
	v_mul_f32_e32 v116, v116, v117
	v_fma_mixlo_f16 v116, v116, s30, 0
	global_store_short v99, v116, s[26:27]
	s_add_u32 s26, s26, 0x1000
	s_addc_u32 s27, s27, 0
	s_waitcnt lgkmcnt(0)
	s_load_dwordx16 s[32:47], s[24:25], 0x400
	s_load_dwordx16 s[48:63], s[24:25], 0x440
	v_cvt_f32_f16_sdwa v113, v45 dst_sel:DWORD dst_unused:UNUSED_PAD src0_sel:WORD_1
	v_pk_mul_f32 v[104:105], v[40:41], v[2:3] op_sel:[1,0]
	v_mul_f32_e32 v112, v41, v113
	v_exp_f32_e32 v104, v104
	v_exp_f32_e32 v105, v105
	v_pk_mul_f32 v[106:107], v[40:41], v[4:5] op_sel:[1,0]
	v_pk_mul_f32 v[104:105], v[18:19], v[104:105]
	v_exp_f32_e32 v106, v106
	v_pk_fma_f32 v[18:19], v[112:113], s[64:65], v[104:105] op_sel_hi:[0,1,1]
	v_exp_f32_e32 v107, v107
	v_pk_fma_f32 v[114:115], s[80:81], v[18:19], 0 op_sel_hi:[1,1,0]
	v_pk_mul_f32 v[106:107], v[20:21], v[106:107]
	v_pk_mul_f32 v[108:109], v[40:41], v[6:7] op_sel:[1,0]
	v_pk_fma_f32 v[20:21], v[112:113], s[66:67], v[106:107] op_sel_hi:[0,1,1]
	v_exp_f32_e32 v108, v108
	v_pk_fma_f32 v[114:115], s[82:83], v[20:21], v[114:115]
	v_exp_f32_e32 v109, v109
	v_pk_mul_f32 v[110:111], v[40:41], v[8:9] op_sel:[1,0]
	v_pk_mul_f32 v[108:109], v[22:23], v[108:109]
	v_exp_f32_e32 v110, v110
	v_pk_fma_f32 v[22:23], v[112:113], s[68:69], v[108:109] op_sel_hi:[0,1,1]
	v_exp_f32_e32 v111, v111
	v_pk_fma_f32 v[114:115], s[84:85], v[22:23], v[114:115]
	v_pk_mul_f32 v[110:111], v[24:25], v[110:111]
	v_pk_mul_f32 v[104:105], v[40:41], v[10:11] op_sel:[1,0]
	v_pk_fma_f32 v[24:25], v[112:113], s[70:71], v[110:111] op_sel_hi:[0,1,1]
	v_exp_f32_e32 v104, v104
	v_pk_fma_f32 v[114:115], s[86:87], v[24:25], v[114:115]
	v_exp_f32_e32 v105, v105
	v_pk_mul_f32 v[106:107], v[40:41], v[12:13] op_sel:[1,0]
	v_pk_mul_f32 v[104:105], v[26:27], v[104:105]
	v_exp_f32_e32 v106, v106
	v_pk_fma_f32 v[26:27], v[112:113], s[72:73], v[104:105] op_sel_hi:[0,1,1]
	v_exp_f32_e32 v107, v107
	v_pk_fma_f32 v[114:115], s[88:89], v[26:27], v[114:115]
	v_pk_mul_f32 v[106:107], v[28:29], v[106:107]
	v_pk_mul_f32 v[108:109], v[40:41], v[14:15] op_sel:[1,0]
	v_pk_fma_f32 v[28:29], v[112:113], s[74:75], v[106:107] op_sel_hi:[0,1,1]
	v_exp_f32_e32 v108, v108
	v_pk_fma_f32 v[114:115], s[90:91], v[28:29], v[114:115]
	v_exp_f32_e32 v109, v109
	v_pk_mul_f32 v[110:111], v[40:41], v[16:17] op_sel:[1,0]
	v_pk_mul_f32 v[108:109], v[30:31], v[108:109]
	v_exp_f32_e32 v110, v110
	v_pk_fma_f32 v[30:31], v[112:113], s[76:77], v[108:109] op_sel_hi:[0,1,1]
	v_exp_f32_e32 v111, v111
	v_pk_fma_f32 v[114:115], s[92:93], v[30:31], v[114:115]
	v_pk_mul_f32 v[110:111], v[32:33], v[110:111]
	v_cvt_f32_f16_sdwa v117, v49 dst_sel:DWORD dst_unused:UNUSED_PAD src0_sel:WORD_1
	v_pk_fma_f32 v[32:33], v[112:113], s[78:79], v[110:111] op_sel_hi:[0,1,1]
	s_nop 0
	v_pk_fma_f32 v[114:115], s[94:95], v[32:33], v[114:115]
	s_nop 0
	v_add_f32_e32 v116, v114, v115
	v_fmac_f32_e32 v116, v98, v113
	v_mul_f32_e32 v116, v116, v117
	v_fma_mixlo_f16 v116, v116, s30, 0
	global_store_short v99, v116, s[26:27]
	s_add_u32 s26, s26, 0x1000
	s_addc_u32 s27, s27, 0
	s_waitcnt vmcnt(13)
	global_load_dwordx4 v[82:85], v102, s[0:1]
	s_add_u32 s0, s0, 0x8000
	s_addc_u32 s1, s1, 0
	global_load_dwordx4 v[90:93], v102, s[8:9]
	s_add_u32 s8, s8, 0x8000
	s_addc_u32 s9, s9, 0
	global_load_dwordx2 v[94:95], v103, s[2:3]
	s_add_u32 s2, s2, 0x8000
	s_addc_u32 s3, s3, 0
	global_load_dwordx4 v[86:89], v102, s[0:1]
	s_add_u32 s0, s0, 0x8000
	s_addc_u32 s1, s1, 0
	global_load_dwordx2 v[96:97], v103, s[2:3]
	s_add_u32 s2, s2, 0x8000
	s_addc_u32 s3, s3, 0
	s_waitcnt lgkmcnt(0)
	s_load_dwordx16 s[64:79], s[24:25], 0x480
	s_load_dwordx16 s[80:95], s[24:25], 0x4c0
	v_cvt_f32_f16_e32 v113, v58
	v_mul_f32_e32 v112, v50, v113
	v_pk_mul_f32 v[104:105], v[50:51], v[2:3] op_sel_hi:[0,1]
	v_pk_mul_f32 v[106:107], v[50:51], v[4:5] op_sel_hi:[0,1]
	v_exp_f32_e32 v104, v104
	v_exp_f32_e32 v105, v105
	v_exp_f32_e32 v106, v106
	v_pk_mul_f32 v[104:105], v[18:19], v[104:105]
	v_exp_f32_e32 v107, v107
	v_pk_fma_f32 v[18:19], v[112:113], s[32:33], v[104:105] op_sel_hi:[0,1,1]
	v_pk_mul_f32 v[106:107], v[20:21], v[106:107]
	v_pk_fma_f32 v[114:115], s[48:49], v[18:19], 0 op_sel_hi:[1,1,0]
	v_pk_fma_f32 v[20:21], v[112:113], s[34:35], v[106:107] op_sel_hi:[0,1,1]
	v_pk_mul_f32 v[108:109], v[50:51], v[6:7] op_sel_hi:[0,1]
	v_pk_fma_f32 v[114:115], s[50:51], v[20:21], v[114:115]
	v_exp_f32_e32 v108, v108
	v_exp_f32_e32 v109, v109
	v_pk_mul_f32 v[110:111], v[50:51], v[8:9] op_sel_hi:[0,1]
	v_pk_mul_f32 v[108:109], v[22:23], v[108:109]
	v_exp_f32_e32 v110, v110
	v_pk_fma_f32 v[22:23], v[112:113], s[36:37], v[108:109] op_sel_hi:[0,1,1]
	v_exp_f32_e32 v111, v111
	v_pk_fma_f32 v[114:115], s[52:53], v[22:23], v[114:115]
	v_pk_mul_f32 v[110:111], v[24:25], v[110:111]
	v_pk_mul_f32 v[104:105], v[50:51], v[10:11] op_sel_hi:[0,1]
	v_pk_fma_f32 v[24:25], v[112:113], s[38:39], v[110:111] op_sel_hi:[0,1,1]
	v_exp_f32_e32 v104, v104
	v_pk_fma_f32 v[114:115], s[54:55], v[24:25], v[114:115]
	v_exp_f32_e32 v105, v105
	v_pk_mul_f32 v[106:107], v[50:51], v[12:13] op_sel_hi:[0,1]
	v_pk_mul_f32 v[104:105], v[26:27], v[104:105]
	v_exp_f32_e32 v106, v106
	v_pk_fma_f32 v[26:27], v[112:113], s[40:41], v[104:105] op_sel_hi:[0,1,1]
	v_exp_f32_e32 v107, v107
	v_pk_fma_f32 v[114:115], s[56:57], v[26:27], v[114:115]
	v_pk_mul_f32 v[106:107], v[28:29], v[106:107]
	v_pk_mul_f32 v[108:109], v[50:51], v[14:15] op_sel_hi:[0,1]
	v_pk_fma_f32 v[28:29], v[112:113], s[42:43], v[106:107] op_sel_hi:[0,1,1]
	v_exp_f32_e32 v108, v108
	v_pk_fma_f32 v[114:115], s[58:59], v[28:29], v[114:115]
	v_exp_f32_e32 v109, v109
	v_pk_mul_f32 v[110:111], v[50:51], v[16:17] op_sel_hi:[0,1]
	v_pk_mul_f32 v[108:109], v[30:31], v[108:109]
	v_exp_f32_e32 v110, v110
	v_pk_fma_f32 v[30:31], v[112:113], s[44:45], v[108:109] op_sel_hi:[0,1,1]
	v_exp_f32_e32 v111, v111
	v_pk_fma_f32 v[114:115], s[60:61], v[30:31], v[114:115]
	v_pk_mul_f32 v[110:111], v[32:33], v[110:111]
	v_cvt_f32_f16_e32 v117, v62
	v_pk_fma_f32 v[32:33], v[112:113], s[46:47], v[110:111] op_sel_hi:[0,1,1]
	s_nop 0
	v_pk_fma_f32 v[114:115], s[62:63], v[32:33], v[114:115]
	s_nop 0
	v_add_f32_e32 v116, v114, v115
	v_fmac_f32_e32 v116, v98, v113
	v_mul_f32_e32 v116, v116, v117
	v_fma_mixlo_f16 v116, v116, s30, 0
	global_store_short v99, v116, s[26:27]
	s_add_u32 s26, s26, 0x1000
	s_addc_u32 s27, s27, 0
	s_waitcnt lgkmcnt(0)
	s_load_dwordx16 s[32:47], s[24:25], 0x500
	s_load_dwordx16 s[48:63], s[24:25], 0x540
	v_cvt_f32_f16_sdwa v113, v58 dst_sel:DWORD dst_unused:UNUSED_PAD src0_sel:WORD_1
	v_pk_mul_f32 v[104:105], v[50:51], v[2:3] op_sel:[1,0]
	v_mul_f32_e32 v112, v51, v113
	v_exp_f32_e32 v104, v104
	v_exp_f32_e32 v105, v105
	v_pk_mul_f32 v[106:107], v[50:51], v[4:5] op_sel:[1,0]
	v_pk_mul_f32 v[104:105], v[18:19], v[104:105]
	v_exp_f32_e32 v106, v106
	v_pk_fma_f32 v[18:19], v[112:113], s[64:65], v[104:105] op_sel_hi:[0,1,1]
	v_exp_f32_e32 v107, v107
	v_pk_fma_f32 v[114:115], s[80:81], v[18:19], 0 op_sel_hi:[1,1,0]
	v_pk_mul_f32 v[106:107], v[20:21], v[106:107]
	v_pk_mul_f32 v[108:109], v[50:51], v[6:7] op_sel:[1,0]
	v_pk_fma_f32 v[20:21], v[112:113], s[66:67], v[106:107] op_sel_hi:[0,1,1]
	v_exp_f32_e32 v108, v108
	v_pk_fma_f32 v[114:115], s[82:83], v[20:21], v[114:115]
	v_exp_f32_e32 v109, v109
	v_pk_mul_f32 v[110:111], v[50:51], v[8:9] op_sel:[1,0]
	v_pk_mul_f32 v[108:109], v[22:23], v[108:109]
	v_exp_f32_e32 v110, v110
	v_pk_fma_f32 v[22:23], v[112:113], s[68:69], v[108:109] op_sel_hi:[0,1,1]
	v_exp_f32_e32 v111, v111
	v_pk_fma_f32 v[114:115], s[84:85], v[22:23], v[114:115]
	v_pk_mul_f32 v[110:111], v[24:25], v[110:111]
	v_pk_mul_f32 v[104:105], v[50:51], v[10:11] op_sel:[1,0]
	v_pk_fma_f32 v[24:25], v[112:113], s[70:71], v[110:111] op_sel_hi:[0,1,1]
	v_exp_f32_e32 v104, v104
	v_pk_fma_f32 v[114:115], s[86:87], v[24:25], v[114:115]
	v_exp_f32_e32 v105, v105
	v_pk_mul_f32 v[106:107], v[50:51], v[12:13] op_sel:[1,0]
	v_pk_mul_f32 v[104:105], v[26:27], v[104:105]
	v_exp_f32_e32 v106, v106
	v_pk_fma_f32 v[26:27], v[112:113], s[72:73], v[104:105] op_sel_hi:[0,1,1]
	v_exp_f32_e32 v107, v107
	v_pk_fma_f32 v[114:115], s[88:89], v[26:27], v[114:115]
	v_pk_mul_f32 v[106:107], v[28:29], v[106:107]
	v_pk_mul_f32 v[108:109], v[50:51], v[14:15] op_sel:[1,0]
	v_pk_fma_f32 v[28:29], v[112:113], s[74:75], v[106:107] op_sel_hi:[0,1,1]
	v_exp_f32_e32 v108, v108
	v_pk_fma_f32 v[114:115], s[90:91], v[28:29], v[114:115]
	v_exp_f32_e32 v109, v109
	v_pk_mul_f32 v[110:111], v[50:51], v[16:17] op_sel:[1,0]
	v_pk_mul_f32 v[108:109], v[30:31], v[108:109]
	v_exp_f32_e32 v110, v110
	v_pk_fma_f32 v[30:31], v[112:113], s[76:77], v[108:109] op_sel_hi:[0,1,1]
	v_exp_f32_e32 v111, v111
	v_pk_fma_f32 v[114:115], s[92:93], v[30:31], v[114:115]
	v_pk_mul_f32 v[110:111], v[32:33], v[110:111]
	v_cvt_f32_f16_sdwa v117, v62 dst_sel:DWORD dst_unused:UNUSED_PAD src0_sel:WORD_1
	v_pk_fma_f32 v[32:33], v[112:113], s[78:79], v[110:111] op_sel_hi:[0,1,1]
	s_nop 0
	v_pk_fma_f32 v[114:115], s[94:95], v[32:33], v[114:115]
	s_nop 0
	v_add_f32_e32 v116, v114, v115
	v_fmac_f32_e32 v116, v98, v113
	v_mul_f32_e32 v116, v116, v117
	v_fma_mixlo_f16 v116, v116, s30, 0
	global_store_short v99, v116, s[26:27]
	s_add_u32 s26, s26, 0x1000
	s_addc_u32 s27, s27, 0
	s_waitcnt lgkmcnt(0)
	s_load_dwordx16 s[64:79], s[24:25], 0x580
	s_load_dwordx16 s[80:95], s[24:25], 0x5c0
	v_cvt_f32_f16_e32 v113, v59
	v_mul_f32_e32 v112, v52, v113
	v_pk_mul_f32 v[104:105], v[52:53], v[2:3] op_sel_hi:[0,1]
	v_pk_mul_f32 v[106:107], v[52:53], v[4:5] op_sel_hi:[0,1]
	v_exp_f32_e32 v104, v104
	v_exp_f32_e32 v105, v105
	v_exp_f32_e32 v106, v106
	v_pk_mul_f32 v[104:105], v[18:19], v[104:105]
	v_exp_f32_e32 v107, v107
	v_pk_fma_f32 v[18:19], v[112:113], s[32:33], v[104:105] op_sel_hi:[0,1,1]
	v_pk_mul_f32 v[106:107], v[20:21], v[106:107]
	v_pk_fma_f32 v[114:115], s[48:49], v[18:19], 0 op_sel_hi:[1,1,0]
	v_pk_fma_f32 v[20:21], v[112:113], s[34:35], v[106:107] op_sel_hi:[0,1,1]
	v_pk_mul_f32 v[108:109], v[52:53], v[6:7] op_sel_hi:[0,1]
	v_pk_fma_f32 v[114:115], s[50:51], v[20:21], v[114:115]
	v_exp_f32_e32 v108, v108
	v_exp_f32_e32 v109, v109
	v_pk_mul_f32 v[110:111], v[52:53], v[8:9] op_sel_hi:[0,1]
	v_pk_mul_f32 v[108:109], v[22:23], v[108:109]
	v_exp_f32_e32 v110, v110
	v_pk_fma_f32 v[22:23], v[112:113], s[36:37], v[108:109] op_sel_hi:[0,1,1]
	v_exp_f32_e32 v111, v111
	v_pk_fma_f32 v[114:115], s[52:53], v[22:23], v[114:115]
	v_pk_mul_f32 v[110:111], v[24:25], v[110:111]
	v_pk_mul_f32 v[104:105], v[52:53], v[10:11] op_sel_hi:[0,1]
	v_pk_fma_f32 v[24:25], v[112:113], s[38:39], v[110:111] op_sel_hi:[0,1,1]
	v_exp_f32_e32 v104, v104
	v_pk_fma_f32 v[114:115], s[54:55], v[24:25], v[114:115]
	v_exp_f32_e32 v105, v105
	v_pk_mul_f32 v[106:107], v[52:53], v[12:13] op_sel_hi:[0,1]
	v_pk_mul_f32 v[104:105], v[26:27], v[104:105]
	v_exp_f32_e32 v106, v106
	v_pk_fma_f32 v[26:27], v[112:113], s[40:41], v[104:105] op_sel_hi:[0,1,1]
	v_exp_f32_e32 v107, v107
	v_pk_fma_f32 v[114:115], s[56:57], v[26:27], v[114:115]
	v_pk_mul_f32 v[106:107], v[28:29], v[106:107]
	v_pk_mul_f32 v[108:109], v[52:53], v[14:15] op_sel_hi:[0,1]
	v_pk_fma_f32 v[28:29], v[112:113], s[42:43], v[106:107] op_sel_hi:[0,1,1]
	v_exp_f32_e32 v108, v108
	v_pk_fma_f32 v[114:115], s[58:59], v[28:29], v[114:115]
	v_exp_f32_e32 v109, v109
	v_pk_mul_f32 v[110:111], v[52:53], v[16:17] op_sel_hi:[0,1]
	v_pk_mul_f32 v[108:109], v[30:31], v[108:109]
	v_exp_f32_e32 v110, v110
	v_pk_fma_f32 v[30:31], v[112:113], s[44:45], v[108:109] op_sel_hi:[0,1,1]
	v_exp_f32_e32 v111, v111
	v_pk_fma_f32 v[114:115], s[60:61], v[30:31], v[114:115]
	v_pk_mul_f32 v[110:111], v[32:33], v[110:111]
	v_cvt_f32_f16_e32 v117, v63
	v_pk_fma_f32 v[32:33], v[112:113], s[46:47], v[110:111] op_sel_hi:[0,1,1]
	s_nop 0
	v_pk_fma_f32 v[114:115], s[62:63], v[32:33], v[114:115]
	s_nop 0
	v_add_f32_e32 v116, v114, v115
	v_fmac_f32_e32 v116, v98, v113
	v_mul_f32_e32 v116, v116, v117
	v_fma_mixlo_f16 v116, v116, s30, 0
	global_store_short v99, v116, s[26:27]
	s_add_u32 s26, s26, 0x1000
	s_addc_u32 s27, s27, 0
	s_waitcnt lgkmcnt(0)
	s_load_dwordx16 s[32:47], s[24:25], 0x600
	s_load_dwordx16 s[48:63], s[24:25], 0x640
	v_cvt_f32_f16_sdwa v113, v59 dst_sel:DWORD dst_unused:UNUSED_PAD src0_sel:WORD_1
	v_pk_mul_f32 v[104:105], v[52:53], v[2:3] op_sel:[1,0]
	v_mul_f32_e32 v112, v53, v113
	v_exp_f32_e32 v104, v104
	v_exp_f32_e32 v105, v105
	v_pk_mul_f32 v[106:107], v[52:53], v[4:5] op_sel:[1,0]
	v_pk_mul_f32 v[104:105], v[18:19], v[104:105]
	v_exp_f32_e32 v106, v106
	v_pk_fma_f32 v[18:19], v[112:113], s[64:65], v[104:105] op_sel_hi:[0,1,1]
	v_exp_f32_e32 v107, v107
	v_pk_fma_f32 v[114:115], s[80:81], v[18:19], 0 op_sel_hi:[1,1,0]
	v_pk_mul_f32 v[106:107], v[20:21], v[106:107]
	v_pk_mul_f32 v[108:109], v[52:53], v[6:7] op_sel:[1,0]
	v_pk_fma_f32 v[20:21], v[112:113], s[66:67], v[106:107] op_sel_hi:[0,1,1]
	v_exp_f32_e32 v108, v108
	v_pk_fma_f32 v[114:115], s[82:83], v[20:21], v[114:115]
	v_exp_f32_e32 v109, v109
	v_pk_mul_f32 v[110:111], v[52:53], v[8:9] op_sel:[1,0]
	v_pk_mul_f32 v[108:109], v[22:23], v[108:109]
	v_exp_f32_e32 v110, v110
	v_pk_fma_f32 v[22:23], v[112:113], s[68:69], v[108:109] op_sel_hi:[0,1,1]
	v_exp_f32_e32 v111, v111
	v_pk_fma_f32 v[114:115], s[84:85], v[22:23], v[114:115]
	v_pk_mul_f32 v[110:111], v[24:25], v[110:111]
	v_pk_mul_f32 v[104:105], v[52:53], v[10:11] op_sel:[1,0]
	v_pk_fma_f32 v[24:25], v[112:113], s[70:71], v[110:111] op_sel_hi:[0,1,1]
	v_exp_f32_e32 v104, v104
	v_pk_fma_f32 v[114:115], s[86:87], v[24:25], v[114:115]
	v_exp_f32_e32 v105, v105
	v_pk_mul_f32 v[106:107], v[52:53], v[12:13] op_sel:[1,0]
	v_pk_mul_f32 v[104:105], v[26:27], v[104:105]
	v_exp_f32_e32 v106, v106
	v_pk_fma_f32 v[26:27], v[112:113], s[72:73], v[104:105] op_sel_hi:[0,1,1]
	v_exp_f32_e32 v107, v107
	v_pk_fma_f32 v[114:115], s[88:89], v[26:27], v[114:115]
	v_pk_mul_f32 v[106:107], v[28:29], v[106:107]
	v_pk_mul_f32 v[108:109], v[52:53], v[14:15] op_sel:[1,0]
	v_pk_fma_f32 v[28:29], v[112:113], s[74:75], v[106:107] op_sel_hi:[0,1,1]
	v_exp_f32_e32 v108, v108
	v_pk_fma_f32 v[114:115], s[90:91], v[28:29], v[114:115]
	v_exp_f32_e32 v109, v109
	v_pk_mul_f32 v[110:111], v[52:53], v[16:17] op_sel:[1,0]
	v_pk_mul_f32 v[108:109], v[30:31], v[108:109]
	v_exp_f32_e32 v110, v110
	v_pk_fma_f32 v[30:31], v[112:113], s[76:77], v[108:109] op_sel_hi:[0,1,1]
	v_exp_f32_e32 v111, v111
	v_pk_fma_f32 v[114:115], s[92:93], v[30:31], v[114:115]
	v_pk_mul_f32 v[110:111], v[32:33], v[110:111]
	v_cvt_f32_f16_sdwa v117, v63 dst_sel:DWORD dst_unused:UNUSED_PAD src0_sel:WORD_1
	v_pk_fma_f32 v[32:33], v[112:113], s[78:79], v[110:111] op_sel_hi:[0,1,1]
	s_nop 0
	v_pk_fma_f32 v[114:115], s[94:95], v[32:33], v[114:115]
	s_nop 0
	v_add_f32_e32 v116, v114, v115
	v_fmac_f32_e32 v116, v98, v113
	v_mul_f32_e32 v116, v116, v117
	v_fma_mixlo_f16 v116, v116, s30, 0
	global_store_short v99, v116, s[26:27]
	s_add_u32 s26, s26, 0x1000
	s_addc_u32 s27, s27, 0
	s_waitcnt lgkmcnt(0)
	s_load_dwordx16 s[64:79], s[24:25], 0x680
	s_load_dwordx16 s[80:95], s[24:25], 0x6c0
	v_cvt_f32_f16_e32 v113, v60
	v_mul_f32_e32 v112, v54, v113
	v_pk_mul_f32 v[104:105], v[54:55], v[2:3] op_sel_hi:[0,1]
	v_pk_mul_f32 v[106:107], v[54:55], v[4:5] op_sel_hi:[0,1]
	v_exp_f32_e32 v104, v104
	v_exp_f32_e32 v105, v105
	v_exp_f32_e32 v106, v106
	v_pk_mul_f32 v[104:105], v[18:19], v[104:105]
	v_exp_f32_e32 v107, v107
	v_pk_fma_f32 v[18:19], v[112:113], s[32:33], v[104:105] op_sel_hi:[0,1,1]
	v_pk_mul_f32 v[106:107], v[20:21], v[106:107]
	v_pk_fma_f32 v[114:115], s[48:49], v[18:19], 0 op_sel_hi:[1,1,0]
	v_pk_fma_f32 v[20:21], v[112:113], s[34:35], v[106:107] op_sel_hi:[0,1,1]
	v_pk_mul_f32 v[108:109], v[54:55], v[6:7] op_sel_hi:[0,1]
	v_pk_fma_f32 v[114:115], s[50:51], v[20:21], v[114:115]
	v_exp_f32_e32 v108, v108
	v_exp_f32_e32 v109, v109
	v_pk_mul_f32 v[110:111], v[54:55], v[8:9] op_sel_hi:[0,1]
	v_pk_mul_f32 v[108:109], v[22:23], v[108:109]
	v_exp_f32_e32 v110, v110
	v_pk_fma_f32 v[22:23], v[112:113], s[36:37], v[108:109] op_sel_hi:[0,1,1]
	v_exp_f32_e32 v111, v111
	v_pk_fma_f32 v[114:115], s[52:53], v[22:23], v[114:115]
	v_pk_mul_f32 v[110:111], v[24:25], v[110:111]
	v_pk_mul_f32 v[104:105], v[54:55], v[10:11] op_sel_hi:[0,1]
	v_pk_fma_f32 v[24:25], v[112:113], s[38:39], v[110:111] op_sel_hi:[0,1,1]
	v_exp_f32_e32 v104, v104
	v_pk_fma_f32 v[114:115], s[54:55], v[24:25], v[114:115]
	v_exp_f32_e32 v105, v105
	v_pk_mul_f32 v[106:107], v[54:55], v[12:13] op_sel_hi:[0,1]
	v_pk_mul_f32 v[104:105], v[26:27], v[104:105]
	v_exp_f32_e32 v106, v106
	v_pk_fma_f32 v[26:27], v[112:113], s[40:41], v[104:105] op_sel_hi:[0,1,1]
	v_exp_f32_e32 v107, v107
	v_pk_fma_f32 v[114:115], s[56:57], v[26:27], v[114:115]
	v_pk_mul_f32 v[106:107], v[28:29], v[106:107]
	v_pk_mul_f32 v[108:109], v[54:55], v[14:15] op_sel_hi:[0,1]
	v_pk_fma_f32 v[28:29], v[112:113], s[42:43], v[106:107] op_sel_hi:[0,1,1]
	v_exp_f32_e32 v108, v108
	v_pk_fma_f32 v[114:115], s[58:59], v[28:29], v[114:115]
	v_exp_f32_e32 v109, v109
	v_pk_mul_f32 v[110:111], v[54:55], v[16:17] op_sel_hi:[0,1]
	v_pk_mul_f32 v[108:109], v[30:31], v[108:109]
	v_exp_f32_e32 v110, v110
	v_pk_fma_f32 v[30:31], v[112:113], s[44:45], v[108:109] op_sel_hi:[0,1,1]
	v_exp_f32_e32 v111, v111
	v_pk_fma_f32 v[114:115], s[60:61], v[30:31], v[114:115]
	v_pk_mul_f32 v[110:111], v[32:33], v[110:111]
	v_cvt_f32_f16_e32 v117, v64
	v_pk_fma_f32 v[32:33], v[112:113], s[46:47], v[110:111] op_sel_hi:[0,1,1]
	s_nop 0
	v_pk_fma_f32 v[114:115], s[62:63], v[32:33], v[114:115]
	s_nop 0
	v_add_f32_e32 v116, v114, v115
	v_fmac_f32_e32 v116, v98, v113
	v_mul_f32_e32 v116, v116, v117
	v_fma_mixlo_f16 v116, v116, s30, 0
	global_store_short v99, v116, s[26:27]
	s_add_u32 s26, s26, 0x1000
	s_addc_u32 s27, s27, 0
	s_waitcnt lgkmcnt(0)
	s_load_dwordx16 s[32:47], s[24:25], 0x700
	s_load_dwordx16 s[48:63], s[24:25], 0x740
	v_cvt_f32_f16_sdwa v113, v60 dst_sel:DWORD dst_unused:UNUSED_PAD src0_sel:WORD_1
	v_pk_mul_f32 v[104:105], v[54:55], v[2:3] op_sel:[1,0]
	v_mul_f32_e32 v112, v55, v113
	v_exp_f32_e32 v104, v104
	v_exp_f32_e32 v105, v105
	v_pk_mul_f32 v[106:107], v[54:55], v[4:5] op_sel:[1,0]
	v_pk_mul_f32 v[104:105], v[18:19], v[104:105]
	v_exp_f32_e32 v106, v106
	v_pk_fma_f32 v[18:19], v[112:113], s[64:65], v[104:105] op_sel_hi:[0,1,1]
	v_exp_f32_e32 v107, v107
	v_pk_fma_f32 v[114:115], s[80:81], v[18:19], 0 op_sel_hi:[1,1,0]
	v_pk_mul_f32 v[106:107], v[20:21], v[106:107]
	v_pk_mul_f32 v[108:109], v[54:55], v[6:7] op_sel:[1,0]
	v_pk_fma_f32 v[20:21], v[112:113], s[66:67], v[106:107] op_sel_hi:[0,1,1]
	v_exp_f32_e32 v108, v108
	v_pk_fma_f32 v[114:115], s[82:83], v[20:21], v[114:115]
	v_exp_f32_e32 v109, v109
	v_pk_mul_f32 v[110:111], v[54:55], v[8:9] op_sel:[1,0]
	v_pk_mul_f32 v[108:109], v[22:23], v[108:109]
	v_exp_f32_e32 v110, v110
	v_pk_fma_f32 v[22:23], v[112:113], s[68:69], v[108:109] op_sel_hi:[0,1,1]
	v_exp_f32_e32 v111, v111
	v_pk_fma_f32 v[114:115], s[84:85], v[22:23], v[114:115]
	v_pk_mul_f32 v[110:111], v[24:25], v[110:111]
	v_pk_mul_f32 v[104:105], v[54:55], v[10:11] op_sel:[1,0]
	v_pk_fma_f32 v[24:25], v[112:113], s[70:71], v[110:111] op_sel_hi:[0,1,1]
	v_exp_f32_e32 v104, v104
	v_pk_fma_f32 v[114:115], s[86:87], v[24:25], v[114:115]
	v_exp_f32_e32 v105, v105
	v_pk_mul_f32 v[106:107], v[54:55], v[12:13] op_sel:[1,0]
	v_pk_mul_f32 v[104:105], v[26:27], v[104:105]
	v_exp_f32_e32 v106, v106
	v_pk_fma_f32 v[26:27], v[112:113], s[72:73], v[104:105] op_sel_hi:[0,1,1]
	v_exp_f32_e32 v107, v107
	v_pk_fma_f32 v[114:115], s[88:89], v[26:27], v[114:115]
	v_pk_mul_f32 v[106:107], v[28:29], v[106:107]
	v_pk_mul_f32 v[108:109], v[54:55], v[14:15] op_sel:[1,0]
	v_pk_fma_f32 v[28:29], v[112:113], s[74:75], v[106:107] op_sel_hi:[0,1,1]
	v_exp_f32_e32 v108, v108
	v_pk_fma_f32 v[114:115], s[90:91], v[28:29], v[114:115]
	v_exp_f32_e32 v109, v109
	v_pk_mul_f32 v[110:111], v[54:55], v[16:17] op_sel:[1,0]
	v_pk_mul_f32 v[108:109], v[30:31], v[108:109]
	v_exp_f32_e32 v110, v110
	v_pk_fma_f32 v[30:31], v[112:113], s[76:77], v[108:109] op_sel_hi:[0,1,1]
	v_exp_f32_e32 v111, v111
	v_pk_fma_f32 v[114:115], s[92:93], v[30:31], v[114:115]
	v_pk_mul_f32 v[110:111], v[32:33], v[110:111]
	v_cvt_f32_f16_sdwa v117, v64 dst_sel:DWORD dst_unused:UNUSED_PAD src0_sel:WORD_1
	v_pk_fma_f32 v[32:33], v[112:113], s[78:79], v[110:111] op_sel_hi:[0,1,1]
	s_nop 0
	v_pk_fma_f32 v[114:115], s[94:95], v[32:33], v[114:115]
	s_nop 0
	v_add_f32_e32 v116, v114, v115
	v_fmac_f32_e32 v116, v98, v113
	v_mul_f32_e32 v116, v116, v117
	v_fma_mixlo_f16 v116, v116, s30, 0
	global_store_short v99, v116, s[26:27]
	s_add_u32 s26, s26, 0x1000
	s_addc_u32 s27, s27, 0
	s_waitcnt lgkmcnt(0)
	s_load_dwordx16 s[64:79], s[24:25], 0x780
	s_load_dwordx16 s[80:95], s[24:25], 0x7c0
	v_cvt_f32_f16_e32 v113, v61
	v_mul_f32_e32 v112, v56, v113
	v_pk_mul_f32 v[104:105], v[56:57], v[2:3] op_sel_hi:[0,1]
	v_pk_mul_f32 v[106:107], v[56:57], v[4:5] op_sel_hi:[0,1]
	v_exp_f32_e32 v104, v104
	v_exp_f32_e32 v105, v105
	v_exp_f32_e32 v106, v106
	v_pk_mul_f32 v[104:105], v[18:19], v[104:105]
	v_exp_f32_e32 v107, v107
	v_pk_fma_f32 v[18:19], v[112:113], s[32:33], v[104:105] op_sel_hi:[0,1,1]
	v_pk_mul_f32 v[106:107], v[20:21], v[106:107]
	v_pk_fma_f32 v[114:115], s[48:49], v[18:19], 0 op_sel_hi:[1,1,0]
	v_pk_fma_f32 v[20:21], v[112:113], s[34:35], v[106:107] op_sel_hi:[0,1,1]
	v_pk_mul_f32 v[108:109], v[56:57], v[6:7] op_sel_hi:[0,1]
	v_pk_fma_f32 v[114:115], s[50:51], v[20:21], v[114:115]
	v_exp_f32_e32 v108, v108
	v_exp_f32_e32 v109, v109
	v_pk_mul_f32 v[110:111], v[56:57], v[8:9] op_sel_hi:[0,1]
	v_pk_mul_f32 v[108:109], v[22:23], v[108:109]
	v_exp_f32_e32 v110, v110
	v_pk_fma_f32 v[22:23], v[112:113], s[36:37], v[108:109] op_sel_hi:[0,1,1]
	v_exp_f32_e32 v111, v111
	v_pk_fma_f32 v[114:115], s[52:53], v[22:23], v[114:115]
	v_pk_mul_f32 v[110:111], v[24:25], v[110:111]
	v_pk_mul_f32 v[104:105], v[56:57], v[10:11] op_sel_hi:[0,1]
	v_pk_fma_f32 v[24:25], v[112:113], s[38:39], v[110:111] op_sel_hi:[0,1,1]
	v_exp_f32_e32 v104, v104
	v_pk_fma_f32 v[114:115], s[54:55], v[24:25], v[114:115]
	v_exp_f32_e32 v105, v105
	v_pk_mul_f32 v[106:107], v[56:57], v[12:13] op_sel_hi:[0,1]
	v_pk_mul_f32 v[104:105], v[26:27], v[104:105]
	v_exp_f32_e32 v106, v106
	v_pk_fma_f32 v[26:27], v[112:113], s[40:41], v[104:105] op_sel_hi:[0,1,1]
	v_exp_f32_e32 v107, v107
	v_pk_fma_f32 v[114:115], s[56:57], v[26:27], v[114:115]
	v_pk_mul_f32 v[106:107], v[28:29], v[106:107]
	v_pk_mul_f32 v[108:109], v[56:57], v[14:15] op_sel_hi:[0,1]
	v_pk_fma_f32 v[28:29], v[112:113], s[42:43], v[106:107] op_sel_hi:[0,1,1]
	v_exp_f32_e32 v108, v108
	v_pk_fma_f32 v[114:115], s[58:59], v[28:29], v[114:115]
	v_exp_f32_e32 v109, v109
	v_pk_mul_f32 v[110:111], v[56:57], v[16:17] op_sel_hi:[0,1]
	v_pk_mul_f32 v[108:109], v[30:31], v[108:109]
	v_exp_f32_e32 v110, v110
	v_pk_fma_f32 v[30:31], v[112:113], s[44:45], v[108:109] op_sel_hi:[0,1,1]
	v_exp_f32_e32 v111, v111
	v_pk_fma_f32 v[114:115], s[60:61], v[30:31], v[114:115]
	v_pk_mul_f32 v[110:111], v[32:33], v[110:111]
	v_cvt_f32_f16_e32 v117, v65
	v_pk_fma_f32 v[32:33], v[112:113], s[46:47], v[110:111] op_sel_hi:[0,1,1]
	s_nop 0
	v_pk_fma_f32 v[114:115], s[62:63], v[32:33], v[114:115]
	s_nop 0
	v_add_f32_e32 v116, v114, v115
	v_fmac_f32_e32 v116, v98, v113
	v_mul_f32_e32 v116, v116, v117
	v_fma_mixlo_f16 v116, v116, s30, 0
	global_store_short v99, v116, s[26:27]
	s_add_u32 s26, s26, 0x1000
	s_addc_u32 s27, s27, 0
	s_waitcnt lgkmcnt(0)
	s_load_dwordx16 s[32:47], s[24:25], 0x800
	s_load_dwordx16 s[48:63], s[24:25], 0x840
	v_cvt_f32_f16_sdwa v113, v61 dst_sel:DWORD dst_unused:UNUSED_PAD src0_sel:WORD_1
	v_pk_mul_f32 v[104:105], v[56:57], v[2:3] op_sel:[1,0]
	v_mul_f32_e32 v112, v57, v113
	v_exp_f32_e32 v104, v104
	v_exp_f32_e32 v105, v105
	v_pk_mul_f32 v[106:107], v[56:57], v[4:5] op_sel:[1,0]
	v_pk_mul_f32 v[104:105], v[18:19], v[104:105]
	v_exp_f32_e32 v106, v106
	v_pk_fma_f32 v[18:19], v[112:113], s[64:65], v[104:105] op_sel_hi:[0,1,1]
	v_exp_f32_e32 v107, v107
	v_pk_fma_f32 v[114:115], s[80:81], v[18:19], 0 op_sel_hi:[1,1,0]
	v_pk_mul_f32 v[106:107], v[20:21], v[106:107]
	v_pk_mul_f32 v[108:109], v[56:57], v[6:7] op_sel:[1,0]
	v_pk_fma_f32 v[20:21], v[112:113], s[66:67], v[106:107] op_sel_hi:[0,1,1]
	v_exp_f32_e32 v108, v108
	v_pk_fma_f32 v[114:115], s[82:83], v[20:21], v[114:115]
	v_exp_f32_e32 v109, v109
	v_pk_mul_f32 v[110:111], v[56:57], v[8:9] op_sel:[1,0]
	v_pk_mul_f32 v[108:109], v[22:23], v[108:109]
	v_exp_f32_e32 v110, v110
	v_pk_fma_f32 v[22:23], v[112:113], s[68:69], v[108:109] op_sel_hi:[0,1,1]
	v_exp_f32_e32 v111, v111
	v_pk_fma_f32 v[114:115], s[84:85], v[22:23], v[114:115]
	v_pk_mul_f32 v[110:111], v[24:25], v[110:111]
	v_pk_mul_f32 v[104:105], v[56:57], v[10:11] op_sel:[1,0]
	v_pk_fma_f32 v[24:25], v[112:113], s[70:71], v[110:111] op_sel_hi:[0,1,1]
	v_exp_f32_e32 v104, v104
	v_pk_fma_f32 v[114:115], s[86:87], v[24:25], v[114:115]
	v_exp_f32_e32 v105, v105
	v_pk_mul_f32 v[106:107], v[56:57], v[12:13] op_sel:[1,0]
	v_pk_mul_f32 v[104:105], v[26:27], v[104:105]
	v_exp_f32_e32 v106, v106
	v_pk_fma_f32 v[26:27], v[112:113], s[72:73], v[104:105] op_sel_hi:[0,1,1]
	v_exp_f32_e32 v107, v107
	v_pk_fma_f32 v[114:115], s[88:89], v[26:27], v[114:115]
	v_pk_mul_f32 v[106:107], v[28:29], v[106:107]
	v_pk_mul_f32 v[108:109], v[56:57], v[14:15] op_sel:[1,0]
	v_pk_fma_f32 v[28:29], v[112:113], s[74:75], v[106:107] op_sel_hi:[0,1,1]
	v_exp_f32_e32 v108, v108
	v_pk_fma_f32 v[114:115], s[90:91], v[28:29], v[114:115]
	v_exp_f32_e32 v109, v109
	v_pk_mul_f32 v[110:111], v[56:57], v[16:17] op_sel:[1,0]
	v_pk_mul_f32 v[108:109], v[30:31], v[108:109]
	v_exp_f32_e32 v110, v110
	v_pk_fma_f32 v[30:31], v[112:113], s[76:77], v[108:109] op_sel_hi:[0,1,1]
	v_exp_f32_e32 v111, v111
	v_pk_fma_f32 v[114:115], s[92:93], v[30:31], v[114:115]
	v_pk_mul_f32 v[110:111], v[32:33], v[110:111]
	v_cvt_f32_f16_sdwa v117, v65 dst_sel:DWORD dst_unused:UNUSED_PAD src0_sel:WORD_1
	v_pk_fma_f32 v[32:33], v[112:113], s[78:79], v[110:111] op_sel_hi:[0,1,1]
	s_nop 0
	v_pk_fma_f32 v[114:115], s[94:95], v[32:33], v[114:115]
	s_nop 0
	v_add_f32_e32 v116, v114, v115
	v_fmac_f32_e32 v116, v98, v113
	v_mul_f32_e32 v116, v116, v117
	v_fma_mixlo_f16 v116, v116, s30, 0
	global_store_short v99, v116, s[26:27]
	s_add_u32 s26, s26, 0x1000
	s_addc_u32 s27, s27, 0
	s_waitcnt vmcnt(21)
	s_waitcnt lgkmcnt(0)
	s_load_dwordx16 s[64:79], s[24:25], 0x880
	s_load_dwordx16 s[80:95], s[24:25], 0x8c0
	v_cvt_f32_f16_e32 v113, v74
	v_mul_f32_e32 v112, v66, v113
	v_pk_mul_f32 v[104:105], v[66:67], v[2:3] op_sel_hi:[0,1]
	v_pk_mul_f32 v[106:107], v[66:67], v[4:5] op_sel_hi:[0,1]
	v_exp_f32_e32 v104, v104
	v_exp_f32_e32 v105, v105
	v_exp_f32_e32 v106, v106
	v_pk_mul_f32 v[104:105], v[18:19], v[104:105]
	v_exp_f32_e32 v107, v107
	v_pk_fma_f32 v[18:19], v[112:113], s[32:33], v[104:105] op_sel_hi:[0,1,1]
	v_pk_mul_f32 v[106:107], v[20:21], v[106:107]
	v_pk_fma_f32 v[114:115], s[48:49], v[18:19], 0 op_sel_hi:[1,1,0]
	v_pk_fma_f32 v[20:21], v[112:113], s[34:35], v[106:107] op_sel_hi:[0,1,1]
	v_pk_mul_f32 v[108:109], v[66:67], v[6:7] op_sel_hi:[0,1]
	v_pk_fma_f32 v[114:115], s[50:51], v[20:21], v[114:115]
	v_exp_f32_e32 v108, v108
	v_exp_f32_e32 v109, v109
	v_pk_mul_f32 v[110:111], v[66:67], v[8:9] op_sel_hi:[0,1]
	v_pk_mul_f32 v[108:109], v[22:23], v[108:109]
	v_exp_f32_e32 v110, v110
	v_pk_fma_f32 v[22:23], v[112:113], s[36:37], v[108:109] op_sel_hi:[0,1,1]
	v_exp_f32_e32 v111, v111
	v_pk_fma_f32 v[114:115], s[52:53], v[22:23], v[114:115]
	v_pk_mul_f32 v[110:111], v[24:25], v[110:111]
	v_pk_mul_f32 v[104:105], v[66:67], v[10:11] op_sel_hi:[0,1]
	v_pk_fma_f32 v[24:25], v[112:113], s[38:39], v[110:111] op_sel_hi:[0,1,1]
	v_exp_f32_e32 v104, v104
	v_pk_fma_f32 v[114:115], s[54:55], v[24:25], v[114:115]
	v_exp_f32_e32 v105, v105
	v_pk_mul_f32 v[106:107], v[66:67], v[12:13] op_sel_hi:[0,1]
	v_pk_mul_f32 v[104:105], v[26:27], v[104:105]
	v_exp_f32_e32 v106, v106
	v_pk_fma_f32 v[26:27], v[112:113], s[40:41], v[104:105] op_sel_hi:[0,1,1]
	v_exp_f32_e32 v107, v107
	v_pk_fma_f32 v[114:115], s[56:57], v[26:27], v[114:115]
	v_pk_mul_f32 v[106:107], v[28:29], v[106:107]
	v_pk_mul_f32 v[108:109], v[66:67], v[14:15] op_sel_hi:[0,1]
	v_pk_fma_f32 v[28:29], v[112:113], s[42:43], v[106:107] op_sel_hi:[0,1,1]
	v_exp_f32_e32 v108, v108
	v_pk_fma_f32 v[114:115], s[58:59], v[28:29], v[114:115]
	v_exp_f32_e32 v109, v109
	v_pk_mul_f32 v[110:111], v[66:67], v[16:17] op_sel_hi:[0,1]
	v_pk_mul_f32 v[108:109], v[30:31], v[108:109]
	v_exp_f32_e32 v110, v110
	v_pk_fma_f32 v[30:31], v[112:113], s[44:45], v[108:109] op_sel_hi:[0,1,1]
	v_exp_f32_e32 v111, v111
	v_pk_fma_f32 v[114:115], s[60:61], v[30:31], v[114:115]
	v_pk_mul_f32 v[110:111], v[32:33], v[110:111]
	v_cvt_f32_f16_e32 v117, v78
	v_pk_fma_f32 v[32:33], v[112:113], s[46:47], v[110:111] op_sel_hi:[0,1,1]
	s_nop 0
	v_pk_fma_f32 v[114:115], s[62:63], v[32:33], v[114:115]
	s_nop 0
	v_add_f32_e32 v116, v114, v115
	v_fmac_f32_e32 v116, v98, v113
	v_mul_f32_e32 v116, v116, v117
	v_fma_mixlo_f16 v116, v116, s30, 0
	global_store_short v99, v116, s[26:27]
	s_add_u32 s26, s26, 0x1000
	s_addc_u32 s27, s27, 0
	s_waitcnt lgkmcnt(0)
	s_load_dwordx16 s[32:47], s[24:25], 0x900
	s_load_dwordx16 s[48:63], s[24:25], 0x940
	v_cvt_f32_f16_sdwa v113, v74 dst_sel:DWORD dst_unused:UNUSED_PAD src0_sel:WORD_1
	v_pk_mul_f32 v[104:105], v[66:67], v[2:3] op_sel:[1,0]
	v_mul_f32_e32 v112, v67, v113
	v_exp_f32_e32 v104, v104
	v_exp_f32_e32 v105, v105
	v_pk_mul_f32 v[106:107], v[66:67], v[4:5] op_sel:[1,0]
	v_pk_mul_f32 v[104:105], v[18:19], v[104:105]
	v_exp_f32_e32 v106, v106
	v_pk_fma_f32 v[18:19], v[112:113], s[64:65], v[104:105] op_sel_hi:[0,1,1]
	v_exp_f32_e32 v107, v107
	v_pk_fma_f32 v[114:115], s[80:81], v[18:19], 0 op_sel_hi:[1,1,0]
	v_pk_mul_f32 v[106:107], v[20:21], v[106:107]
	v_pk_mul_f32 v[108:109], v[66:67], v[6:7] op_sel:[1,0]
	v_pk_fma_f32 v[20:21], v[112:113], s[66:67], v[106:107] op_sel_hi:[0,1,1]
	v_exp_f32_e32 v108, v108
	v_pk_fma_f32 v[114:115], s[82:83], v[20:21], v[114:115]
	v_exp_f32_e32 v109, v109
	v_pk_mul_f32 v[110:111], v[66:67], v[8:9] op_sel:[1,0]
	v_pk_mul_f32 v[108:109], v[22:23], v[108:109]
	v_exp_f32_e32 v110, v110
	v_pk_fma_f32 v[22:23], v[112:113], s[68:69], v[108:109] op_sel_hi:[0,1,1]
	v_exp_f32_e32 v111, v111
	v_pk_fma_f32 v[114:115], s[84:85], v[22:23], v[114:115]
	v_pk_mul_f32 v[110:111], v[24:25], v[110:111]
	v_pk_mul_f32 v[104:105], v[66:67], v[10:11] op_sel:[1,0]
	v_pk_fma_f32 v[24:25], v[112:113], s[70:71], v[110:111] op_sel_hi:[0,1,1]
	v_exp_f32_e32 v104, v104
	v_pk_fma_f32 v[114:115], s[86:87], v[24:25], v[114:115]
	v_exp_f32_e32 v105, v105
	v_pk_mul_f32 v[106:107], v[66:67], v[12:13] op_sel:[1,0]
	v_pk_mul_f32 v[104:105], v[26:27], v[104:105]
	v_exp_f32_e32 v106, v106
	v_pk_fma_f32 v[26:27], v[112:113], s[72:73], v[104:105] op_sel_hi:[0,1,1]
	v_exp_f32_e32 v107, v107
	v_pk_fma_f32 v[114:115], s[88:89], v[26:27], v[114:115]
	v_pk_mul_f32 v[106:107], v[28:29], v[106:107]
	v_pk_mul_f32 v[108:109], v[66:67], v[14:15] op_sel:[1,0]
	v_pk_fma_f32 v[28:29], v[112:113], s[74:75], v[106:107] op_sel_hi:[0,1,1]
	v_exp_f32_e32 v108, v108
	v_pk_fma_f32 v[114:115], s[90:91], v[28:29], v[114:115]
	v_exp_f32_e32 v109, v109
	v_pk_mul_f32 v[110:111], v[66:67], v[16:17] op_sel:[1,0]
	v_pk_mul_f32 v[108:109], v[30:31], v[108:109]
	v_exp_f32_e32 v110, v110
	v_pk_fma_f32 v[30:31], v[112:113], s[76:77], v[108:109] op_sel_hi:[0,1,1]
	v_exp_f32_e32 v111, v111
	v_pk_fma_f32 v[114:115], s[92:93], v[30:31], v[114:115]
	v_pk_mul_f32 v[110:111], v[32:33], v[110:111]
	v_cvt_f32_f16_sdwa v117, v78 dst_sel:DWORD dst_unused:UNUSED_PAD src0_sel:WORD_1
	v_pk_fma_f32 v[32:33], v[112:113], s[78:79], v[110:111] op_sel_hi:[0,1,1]
	s_nop 0
	v_pk_fma_f32 v[114:115], s[94:95], v[32:33], v[114:115]
	s_nop 0
	v_add_f32_e32 v116, v114, v115
	v_fmac_f32_e32 v116, v98, v113
	v_mul_f32_e32 v116, v116, v117
	v_fma_mixlo_f16 v116, v116, s30, 0
	global_store_short v99, v116, s[26:27]
	s_add_u32 s26, s26, 0x1000
	s_addc_u32 s27, s27, 0
	s_waitcnt lgkmcnt(0)
	s_load_dwordx16 s[64:79], s[24:25], 0x980
	s_load_dwordx16 s[80:95], s[24:25], 0x9c0
	v_cvt_f32_f16_e32 v113, v75
	v_mul_f32_e32 v112, v68, v113
	v_pk_mul_f32 v[104:105], v[68:69], v[2:3] op_sel_hi:[0,1]
	v_pk_mul_f32 v[106:107], v[68:69], v[4:5] op_sel_hi:[0,1]
	v_exp_f32_e32 v104, v104
	v_exp_f32_e32 v105, v105
	v_exp_f32_e32 v106, v106
	v_pk_mul_f32 v[104:105], v[18:19], v[104:105]
	v_exp_f32_e32 v107, v107
	v_pk_fma_f32 v[18:19], v[112:113], s[32:33], v[104:105] op_sel_hi:[0,1,1]
	v_pk_mul_f32 v[106:107], v[20:21], v[106:107]
	v_pk_fma_f32 v[114:115], s[48:49], v[18:19], 0 op_sel_hi:[1,1,0]
	v_pk_fma_f32 v[20:21], v[112:113], s[34:35], v[106:107] op_sel_hi:[0,1,1]
	v_pk_mul_f32 v[108:109], v[68:69], v[6:7] op_sel_hi:[0,1]
	v_pk_fma_f32 v[114:115], s[50:51], v[20:21], v[114:115]
	v_exp_f32_e32 v108, v108
	v_exp_f32_e32 v109, v109
	v_pk_mul_f32 v[110:111], v[68:69], v[8:9] op_sel_hi:[0,1]
	v_pk_mul_f32 v[108:109], v[22:23], v[108:109]
	v_exp_f32_e32 v110, v110
	v_pk_fma_f32 v[22:23], v[112:113], s[36:37], v[108:109] op_sel_hi:[0,1,1]
	v_exp_f32_e32 v111, v111
	v_pk_fma_f32 v[114:115], s[52:53], v[22:23], v[114:115]
	v_pk_mul_f32 v[110:111], v[24:25], v[110:111]
	v_pk_mul_f32 v[104:105], v[68:69], v[10:11] op_sel_hi:[0,1]
	v_pk_fma_f32 v[24:25], v[112:113], s[38:39], v[110:111] op_sel_hi:[0,1,1]
	v_exp_f32_e32 v104, v104
	v_pk_fma_f32 v[114:115], s[54:55], v[24:25], v[114:115]
	v_exp_f32_e32 v105, v105
	v_pk_mul_f32 v[106:107], v[68:69], v[12:13] op_sel_hi:[0,1]
	v_pk_mul_f32 v[104:105], v[26:27], v[104:105]
	v_exp_f32_e32 v106, v106
	v_pk_fma_f32 v[26:27], v[112:113], s[40:41], v[104:105] op_sel_hi:[0,1,1]
	v_exp_f32_e32 v107, v107
	v_pk_fma_f32 v[114:115], s[56:57], v[26:27], v[114:115]
	v_pk_mul_f32 v[106:107], v[28:29], v[106:107]
	v_pk_mul_f32 v[108:109], v[68:69], v[14:15] op_sel_hi:[0,1]
	v_pk_fma_f32 v[28:29], v[112:113], s[42:43], v[106:107] op_sel_hi:[0,1,1]
	v_exp_f32_e32 v108, v108
	v_pk_fma_f32 v[114:115], s[58:59], v[28:29], v[114:115]
	v_exp_f32_e32 v109, v109
	v_pk_mul_f32 v[110:111], v[68:69], v[16:17] op_sel_hi:[0,1]
	v_pk_mul_f32 v[108:109], v[30:31], v[108:109]
	v_exp_f32_e32 v110, v110
	v_pk_fma_f32 v[30:31], v[112:113], s[44:45], v[108:109] op_sel_hi:[0,1,1]
	v_exp_f32_e32 v111, v111
	v_pk_fma_f32 v[114:115], s[60:61], v[30:31], v[114:115]
	v_pk_mul_f32 v[110:111], v[32:33], v[110:111]
	v_cvt_f32_f16_e32 v117, v79
	v_pk_fma_f32 v[32:33], v[112:113], s[46:47], v[110:111] op_sel_hi:[0,1,1]
	s_nop 0
	v_pk_fma_f32 v[114:115], s[62:63], v[32:33], v[114:115]
	s_nop 0
	v_add_f32_e32 v116, v114, v115
	v_fmac_f32_e32 v116, v98, v113
	v_mul_f32_e32 v116, v116, v117
	v_fma_mixlo_f16 v116, v116, s30, 0
	global_store_short v99, v116, s[26:27]
	s_add_u32 s26, s26, 0x1000
	s_addc_u32 s27, s27, 0
	s_waitcnt lgkmcnt(0)
	s_load_dwordx16 s[32:47], s[24:25], 0xa00
	s_load_dwordx16 s[48:63], s[24:25], 0xa40
	v_cvt_f32_f16_sdwa v113, v75 dst_sel:DWORD dst_unused:UNUSED_PAD src0_sel:WORD_1
	v_pk_mul_f32 v[104:105], v[68:69], v[2:3] op_sel:[1,0]
	v_mul_f32_e32 v112, v69, v113
	v_exp_f32_e32 v104, v104
	v_exp_f32_e32 v105, v105
	v_pk_mul_f32 v[106:107], v[68:69], v[4:5] op_sel:[1,0]
	v_pk_mul_f32 v[104:105], v[18:19], v[104:105]
	v_exp_f32_e32 v106, v106
	v_pk_fma_f32 v[18:19], v[112:113], s[64:65], v[104:105] op_sel_hi:[0,1,1]
	v_exp_f32_e32 v107, v107
	v_pk_fma_f32 v[114:115], s[80:81], v[18:19], 0 op_sel_hi:[1,1,0]
	v_pk_mul_f32 v[106:107], v[20:21], v[106:107]
	v_pk_mul_f32 v[108:109], v[68:69], v[6:7] op_sel:[1,0]
	v_pk_fma_f32 v[20:21], v[112:113], s[66:67], v[106:107] op_sel_hi:[0,1,1]
	v_exp_f32_e32 v108, v108
	v_pk_fma_f32 v[114:115], s[82:83], v[20:21], v[114:115]
	v_exp_f32_e32 v109, v109
	v_pk_mul_f32 v[110:111], v[68:69], v[8:9] op_sel:[1,0]
	v_pk_mul_f32 v[108:109], v[22:23], v[108:109]
	v_exp_f32_e32 v110, v110
	v_pk_fma_f32 v[22:23], v[112:113], s[68:69], v[108:109] op_sel_hi:[0,1,1]
	v_exp_f32_e32 v111, v111
	v_pk_fma_f32 v[114:115], s[84:85], v[22:23], v[114:115]
	v_pk_mul_f32 v[110:111], v[24:25], v[110:111]
	v_pk_mul_f32 v[104:105], v[68:69], v[10:11] op_sel:[1,0]
	v_pk_fma_f32 v[24:25], v[112:113], s[70:71], v[110:111] op_sel_hi:[0,1,1]
	v_exp_f32_e32 v104, v104
	v_pk_fma_f32 v[114:115], s[86:87], v[24:25], v[114:115]
	v_exp_f32_e32 v105, v105
	v_pk_mul_f32 v[106:107], v[68:69], v[12:13] op_sel:[1,0]
	v_pk_mul_f32 v[104:105], v[26:27], v[104:105]
	v_exp_f32_e32 v106, v106
	v_pk_fma_f32 v[26:27], v[112:113], s[72:73], v[104:105] op_sel_hi:[0,1,1]
	v_exp_f32_e32 v107, v107
	v_pk_fma_f32 v[114:115], s[88:89], v[26:27], v[114:115]
	v_pk_mul_f32 v[106:107], v[28:29], v[106:107]
	v_pk_mul_f32 v[108:109], v[68:69], v[14:15] op_sel:[1,0]
	v_pk_fma_f32 v[28:29], v[112:113], s[74:75], v[106:107] op_sel_hi:[0,1,1]
	v_exp_f32_e32 v108, v108
	v_pk_fma_f32 v[114:115], s[90:91], v[28:29], v[114:115]
	v_exp_f32_e32 v109, v109
	v_pk_mul_f32 v[110:111], v[68:69], v[16:17] op_sel:[1,0]
	v_pk_mul_f32 v[108:109], v[30:31], v[108:109]
	v_exp_f32_e32 v110, v110
	v_pk_fma_f32 v[30:31], v[112:113], s[76:77], v[108:109] op_sel_hi:[0,1,1]
	v_exp_f32_e32 v111, v111
	v_pk_fma_f32 v[114:115], s[92:93], v[30:31], v[114:115]
	v_pk_mul_f32 v[110:111], v[32:33], v[110:111]
	v_cvt_f32_f16_sdwa v117, v79 dst_sel:DWORD dst_unused:UNUSED_PAD src0_sel:WORD_1
	v_pk_fma_f32 v[32:33], v[112:113], s[78:79], v[110:111] op_sel_hi:[0,1,1]
	s_nop 0
	v_pk_fma_f32 v[114:115], s[94:95], v[32:33], v[114:115]
	s_nop 0
	v_add_f32_e32 v116, v114, v115
	v_fmac_f32_e32 v116, v98, v113
	v_mul_f32_e32 v116, v116, v117
	v_fma_mixlo_f16 v116, v116, s30, 0
	global_store_short v99, v116, s[26:27]
	s_add_u32 s26, s26, 0x1000
	s_addc_u32 s27, s27, 0
	s_waitcnt lgkmcnt(0)
	s_load_dwordx16 s[64:79], s[24:25], 0xa80
	s_load_dwordx16 s[80:95], s[24:25], 0xac0
	v_cvt_f32_f16_e32 v113, v76
	v_mul_f32_e32 v112, v70, v113
	v_pk_mul_f32 v[104:105], v[70:71], v[2:3] op_sel_hi:[0,1]
	v_pk_mul_f32 v[106:107], v[70:71], v[4:5] op_sel_hi:[0,1]
	v_exp_f32_e32 v104, v104
	v_exp_f32_e32 v105, v105
	v_exp_f32_e32 v106, v106
	v_pk_mul_f32 v[104:105], v[18:19], v[104:105]
	v_exp_f32_e32 v107, v107
	v_pk_fma_f32 v[18:19], v[112:113], s[32:33], v[104:105] op_sel_hi:[0,1,1]
	v_pk_mul_f32 v[106:107], v[20:21], v[106:107]
	v_pk_fma_f32 v[114:115], s[48:49], v[18:19], 0 op_sel_hi:[1,1,0]
	v_pk_fma_f32 v[20:21], v[112:113], s[34:35], v[106:107] op_sel_hi:[0,1,1]
	v_pk_mul_f32 v[108:109], v[70:71], v[6:7] op_sel_hi:[0,1]
	v_pk_fma_f32 v[114:115], s[50:51], v[20:21], v[114:115]
	v_exp_f32_e32 v108, v108
	v_exp_f32_e32 v109, v109
	v_pk_mul_f32 v[110:111], v[70:71], v[8:9] op_sel_hi:[0,1]
	v_pk_mul_f32 v[108:109], v[22:23], v[108:109]
	v_exp_f32_e32 v110, v110
	v_pk_fma_f32 v[22:23], v[112:113], s[36:37], v[108:109] op_sel_hi:[0,1,1]
	v_exp_f32_e32 v111, v111
	v_pk_fma_f32 v[114:115], s[52:53], v[22:23], v[114:115]
	v_pk_mul_f32 v[110:111], v[24:25], v[110:111]
	v_pk_mul_f32 v[104:105], v[70:71], v[10:11] op_sel_hi:[0,1]
	v_pk_fma_f32 v[24:25], v[112:113], s[38:39], v[110:111] op_sel_hi:[0,1,1]
	v_exp_f32_e32 v104, v104
	v_pk_fma_f32 v[114:115], s[54:55], v[24:25], v[114:115]
	v_exp_f32_e32 v105, v105
	v_pk_mul_f32 v[106:107], v[70:71], v[12:13] op_sel_hi:[0,1]
	v_pk_mul_f32 v[104:105], v[26:27], v[104:105]
	v_exp_f32_e32 v106, v106
	v_pk_fma_f32 v[26:27], v[112:113], s[40:41], v[104:105] op_sel_hi:[0,1,1]
	v_exp_f32_e32 v107, v107
	v_pk_fma_f32 v[114:115], s[56:57], v[26:27], v[114:115]
	v_pk_mul_f32 v[106:107], v[28:29], v[106:107]
	v_pk_mul_f32 v[108:109], v[70:71], v[14:15] op_sel_hi:[0,1]
	v_pk_fma_f32 v[28:29], v[112:113], s[42:43], v[106:107] op_sel_hi:[0,1,1]
	v_exp_f32_e32 v108, v108
	v_pk_fma_f32 v[114:115], s[58:59], v[28:29], v[114:115]
	v_exp_f32_e32 v109, v109
	v_pk_mul_f32 v[110:111], v[70:71], v[16:17] op_sel_hi:[0,1]
	v_pk_mul_f32 v[108:109], v[30:31], v[108:109]
	v_exp_f32_e32 v110, v110
	v_pk_fma_f32 v[30:31], v[112:113], s[44:45], v[108:109] op_sel_hi:[0,1,1]
	v_exp_f32_e32 v111, v111
	v_pk_fma_f32 v[114:115], s[60:61], v[30:31], v[114:115]
	v_pk_mul_f32 v[110:111], v[32:33], v[110:111]
	v_cvt_f32_f16_e32 v117, v80
	v_pk_fma_f32 v[32:33], v[112:113], s[46:47], v[110:111] op_sel_hi:[0,1,1]
	s_nop 0
	v_pk_fma_f32 v[114:115], s[62:63], v[32:33], v[114:115]
	s_nop 0
	v_add_f32_e32 v116, v114, v115
	v_fmac_f32_e32 v116, v98, v113
	v_mul_f32_e32 v116, v116, v117
	v_fma_mixlo_f16 v116, v116, s30, 0
	global_store_short v99, v116, s[26:27]
	s_add_u32 s26, s26, 0x1000
	s_addc_u32 s27, s27, 0
	s_waitcnt lgkmcnt(0)
	s_load_dwordx16 s[32:47], s[24:25], 0xb00
	s_load_dwordx16 s[48:63], s[24:25], 0xb40
	v_cvt_f32_f16_sdwa v113, v76 dst_sel:DWORD dst_unused:UNUSED_PAD src0_sel:WORD_1
	v_pk_mul_f32 v[104:105], v[70:71], v[2:3] op_sel:[1,0]
	v_mul_f32_e32 v112, v71, v113
	v_exp_f32_e32 v104, v104
	v_exp_f32_e32 v105, v105
	v_pk_mul_f32 v[106:107], v[70:71], v[4:5] op_sel:[1,0]
	v_pk_mul_f32 v[104:105], v[18:19], v[104:105]
	v_exp_f32_e32 v106, v106
	v_pk_fma_f32 v[18:19], v[112:113], s[64:65], v[104:105] op_sel_hi:[0,1,1]
	v_exp_f32_e32 v107, v107
	v_pk_fma_f32 v[114:115], s[80:81], v[18:19], 0 op_sel_hi:[1,1,0]
	v_pk_mul_f32 v[106:107], v[20:21], v[106:107]
	v_pk_mul_f32 v[108:109], v[70:71], v[6:7] op_sel:[1,0]
	v_pk_fma_f32 v[20:21], v[112:113], s[66:67], v[106:107] op_sel_hi:[0,1,1]
	v_exp_f32_e32 v108, v108
	v_pk_fma_f32 v[114:115], s[82:83], v[20:21], v[114:115]
	v_exp_f32_e32 v109, v109
	v_pk_mul_f32 v[110:111], v[70:71], v[8:9] op_sel:[1,0]
	v_pk_mul_f32 v[108:109], v[22:23], v[108:109]
	v_exp_f32_e32 v110, v110
	v_pk_fma_f32 v[22:23], v[112:113], s[68:69], v[108:109] op_sel_hi:[0,1,1]
	v_exp_f32_e32 v111, v111
	v_pk_fma_f32 v[114:115], s[84:85], v[22:23], v[114:115]
	v_pk_mul_f32 v[110:111], v[24:25], v[110:111]
	v_pk_mul_f32 v[104:105], v[70:71], v[10:11] op_sel:[1,0]
	v_pk_fma_f32 v[24:25], v[112:113], s[70:71], v[110:111] op_sel_hi:[0,1,1]
	v_exp_f32_e32 v104, v104
	v_pk_fma_f32 v[114:115], s[86:87], v[24:25], v[114:115]
	v_exp_f32_e32 v105, v105
	v_pk_mul_f32 v[106:107], v[70:71], v[12:13] op_sel:[1,0]
	v_pk_mul_f32 v[104:105], v[26:27], v[104:105]
	v_exp_f32_e32 v106, v106
	v_pk_fma_f32 v[26:27], v[112:113], s[72:73], v[104:105] op_sel_hi:[0,1,1]
	v_exp_f32_e32 v107, v107
	v_pk_fma_f32 v[114:115], s[88:89], v[26:27], v[114:115]
	v_pk_mul_f32 v[106:107], v[28:29], v[106:107]
	v_pk_mul_f32 v[108:109], v[70:71], v[14:15] op_sel:[1,0]
	v_pk_fma_f32 v[28:29], v[112:113], s[74:75], v[106:107] op_sel_hi:[0,1,1]
	v_exp_f32_e32 v108, v108
	v_pk_fma_f32 v[114:115], s[90:91], v[28:29], v[114:115]
	v_exp_f32_e32 v109, v109
	v_pk_mul_f32 v[110:111], v[70:71], v[16:17] op_sel:[1,0]
	v_pk_mul_f32 v[108:109], v[30:31], v[108:109]
	v_exp_f32_e32 v110, v110
	v_pk_fma_f32 v[30:31], v[112:113], s[76:77], v[108:109] op_sel_hi:[0,1,1]
	v_exp_f32_e32 v111, v111
	v_pk_fma_f32 v[114:115], s[92:93], v[30:31], v[114:115]
	v_pk_mul_f32 v[110:111], v[32:33], v[110:111]
	v_cvt_f32_f16_sdwa v117, v80 dst_sel:DWORD dst_unused:UNUSED_PAD src0_sel:WORD_1
	v_pk_fma_f32 v[32:33], v[112:113], s[78:79], v[110:111] op_sel_hi:[0,1,1]
	s_nop 0
	v_pk_fma_f32 v[114:115], s[94:95], v[32:33], v[114:115]
	s_nop 0
	v_add_f32_e32 v116, v114, v115
	v_fmac_f32_e32 v116, v98, v113
	v_mul_f32_e32 v116, v116, v117
	v_fma_mixlo_f16 v116, v116, s30, 0
	global_store_short v99, v116, s[26:27]
	s_add_u32 s26, s26, 0x1000
	s_addc_u32 s27, s27, 0
	s_waitcnt lgkmcnt(0)
	s_load_dwordx16 s[64:79], s[24:25], 0xb80
	s_load_dwordx16 s[80:95], s[24:25], 0xbc0
	v_cvt_f32_f16_e32 v113, v77
	v_mul_f32_e32 v112, v72, v113
	v_pk_mul_f32 v[104:105], v[72:73], v[2:3] op_sel_hi:[0,1]
	v_pk_mul_f32 v[106:107], v[72:73], v[4:5] op_sel_hi:[0,1]
	v_exp_f32_e32 v104, v104
	v_exp_f32_e32 v105, v105
	v_exp_f32_e32 v106, v106
	v_pk_mul_f32 v[104:105], v[18:19], v[104:105]
	v_exp_f32_e32 v107, v107
	v_pk_fma_f32 v[18:19], v[112:113], s[32:33], v[104:105] op_sel_hi:[0,1,1]
	v_pk_mul_f32 v[106:107], v[20:21], v[106:107]
	v_pk_fma_f32 v[114:115], s[48:49], v[18:19], 0 op_sel_hi:[1,1,0]
	v_pk_fma_f32 v[20:21], v[112:113], s[34:35], v[106:107] op_sel_hi:[0,1,1]
	v_pk_mul_f32 v[108:109], v[72:73], v[6:7] op_sel_hi:[0,1]
	v_pk_fma_f32 v[114:115], s[50:51], v[20:21], v[114:115]
	v_exp_f32_e32 v108, v108
	v_exp_f32_e32 v109, v109
	v_pk_mul_f32 v[110:111], v[72:73], v[8:9] op_sel_hi:[0,1]
	v_pk_mul_f32 v[108:109], v[22:23], v[108:109]
	v_exp_f32_e32 v110, v110
	v_pk_fma_f32 v[22:23], v[112:113], s[36:37], v[108:109] op_sel_hi:[0,1,1]
	v_exp_f32_e32 v111, v111
	v_pk_fma_f32 v[114:115], s[52:53], v[22:23], v[114:115]
	v_pk_mul_f32 v[110:111], v[24:25], v[110:111]
	v_pk_mul_f32 v[104:105], v[72:73], v[10:11] op_sel_hi:[0,1]
	v_pk_fma_f32 v[24:25], v[112:113], s[38:39], v[110:111] op_sel_hi:[0,1,1]
	v_exp_f32_e32 v104, v104
	v_pk_fma_f32 v[114:115], s[54:55], v[24:25], v[114:115]
	v_exp_f32_e32 v105, v105
	v_pk_mul_f32 v[106:107], v[72:73], v[12:13] op_sel_hi:[0,1]
	v_pk_mul_f32 v[104:105], v[26:27], v[104:105]
	v_exp_f32_e32 v106, v106
	v_pk_fma_f32 v[26:27], v[112:113], s[40:41], v[104:105] op_sel_hi:[0,1,1]
	v_exp_f32_e32 v107, v107
	v_pk_fma_f32 v[114:115], s[56:57], v[26:27], v[114:115]
	v_pk_mul_f32 v[106:107], v[28:29], v[106:107]
	v_pk_mul_f32 v[108:109], v[72:73], v[14:15] op_sel_hi:[0,1]
	v_pk_fma_f32 v[28:29], v[112:113], s[42:43], v[106:107] op_sel_hi:[0,1,1]
	v_exp_f32_e32 v108, v108
	v_pk_fma_f32 v[114:115], s[58:59], v[28:29], v[114:115]
	v_exp_f32_e32 v109, v109
	v_pk_mul_f32 v[110:111], v[72:73], v[16:17] op_sel_hi:[0,1]
	v_pk_mul_f32 v[108:109], v[30:31], v[108:109]
	v_exp_f32_e32 v110, v110
	v_pk_fma_f32 v[30:31], v[112:113], s[44:45], v[108:109] op_sel_hi:[0,1,1]
	v_exp_f32_e32 v111, v111
	v_pk_fma_f32 v[114:115], s[60:61], v[30:31], v[114:115]
	v_pk_mul_f32 v[110:111], v[32:33], v[110:111]
	v_cvt_f32_f16_e32 v117, v81
	v_pk_fma_f32 v[32:33], v[112:113], s[46:47], v[110:111] op_sel_hi:[0,1,1]
	s_nop 0
	v_pk_fma_f32 v[114:115], s[62:63], v[32:33], v[114:115]
	s_nop 0
	v_add_f32_e32 v116, v114, v115
	v_fmac_f32_e32 v116, v98, v113
	v_mul_f32_e32 v116, v116, v117
	v_fma_mixlo_f16 v116, v116, s30, 0
	global_store_short v99, v116, s[26:27]
	s_add_u32 s26, s26, 0x1000
	s_addc_u32 s27, s27, 0
	s_waitcnt lgkmcnt(0)
	s_load_dwordx16 s[32:47], s[24:25], 0xc00
	s_load_dwordx16 s[48:63], s[24:25], 0xc40
	v_cvt_f32_f16_sdwa v113, v77 dst_sel:DWORD dst_unused:UNUSED_PAD src0_sel:WORD_1
	v_pk_mul_f32 v[104:105], v[72:73], v[2:3] op_sel:[1,0]
	v_mul_f32_e32 v112, v73, v113
	v_exp_f32_e32 v104, v104
	v_exp_f32_e32 v105, v105
	v_pk_mul_f32 v[106:107], v[72:73], v[4:5] op_sel:[1,0]
	v_pk_mul_f32 v[104:105], v[18:19], v[104:105]
	v_exp_f32_e32 v106, v106
	v_pk_fma_f32 v[18:19], v[112:113], s[64:65], v[104:105] op_sel_hi:[0,1,1]
	v_exp_f32_e32 v107, v107
	v_pk_fma_f32 v[114:115], s[80:81], v[18:19], 0 op_sel_hi:[1,1,0]
	v_pk_mul_f32 v[106:107], v[20:21], v[106:107]
	v_pk_mul_f32 v[108:109], v[72:73], v[6:7] op_sel:[1,0]
	v_pk_fma_f32 v[20:21], v[112:113], s[66:67], v[106:107] op_sel_hi:[0,1,1]
	v_exp_f32_e32 v108, v108
	v_pk_fma_f32 v[114:115], s[82:83], v[20:21], v[114:115]
	v_exp_f32_e32 v109, v109
	v_pk_mul_f32 v[110:111], v[72:73], v[8:9] op_sel:[1,0]
	v_pk_mul_f32 v[108:109], v[22:23], v[108:109]
	v_exp_f32_e32 v110, v110
	v_pk_fma_f32 v[22:23], v[112:113], s[68:69], v[108:109] op_sel_hi:[0,1,1]
	v_exp_f32_e32 v111, v111
	v_pk_fma_f32 v[114:115], s[84:85], v[22:23], v[114:115]
	v_pk_mul_f32 v[110:111], v[24:25], v[110:111]
	v_pk_mul_f32 v[104:105], v[72:73], v[10:11] op_sel:[1,0]
	v_pk_fma_f32 v[24:25], v[112:113], s[70:71], v[110:111] op_sel_hi:[0,1,1]
	v_exp_f32_e32 v104, v104
	v_pk_fma_f32 v[114:115], s[86:87], v[24:25], v[114:115]
	v_exp_f32_e32 v105, v105
	v_pk_mul_f32 v[106:107], v[72:73], v[12:13] op_sel:[1,0]
	v_pk_mul_f32 v[104:105], v[26:27], v[104:105]
	v_exp_f32_e32 v106, v106
	v_pk_fma_f32 v[26:27], v[112:113], s[72:73], v[104:105] op_sel_hi:[0,1,1]
	v_exp_f32_e32 v107, v107
	v_pk_fma_f32 v[114:115], s[88:89], v[26:27], v[114:115]
	v_pk_mul_f32 v[106:107], v[28:29], v[106:107]
	v_pk_mul_f32 v[108:109], v[72:73], v[14:15] op_sel:[1,0]
	v_pk_fma_f32 v[28:29], v[112:113], s[74:75], v[106:107] op_sel_hi:[0,1,1]
	v_exp_f32_e32 v108, v108
	v_pk_fma_f32 v[114:115], s[90:91], v[28:29], v[114:115]
	v_exp_f32_e32 v109, v109
	v_pk_mul_f32 v[110:111], v[72:73], v[16:17] op_sel:[1,0]
	v_pk_mul_f32 v[108:109], v[30:31], v[108:109]
	v_exp_f32_e32 v110, v110
	v_pk_fma_f32 v[30:31], v[112:113], s[76:77], v[108:109] op_sel_hi:[0,1,1]
	v_exp_f32_e32 v111, v111
	v_pk_fma_f32 v[114:115], s[92:93], v[30:31], v[114:115]
	v_pk_mul_f32 v[110:111], v[32:33], v[110:111]
	v_cvt_f32_f16_sdwa v117, v81 dst_sel:DWORD dst_unused:UNUSED_PAD src0_sel:WORD_1
	v_pk_fma_f32 v[32:33], v[112:113], s[78:79], v[110:111] op_sel_hi:[0,1,1]
	s_nop 0
	v_pk_fma_f32 v[114:115], s[94:95], v[32:33], v[114:115]
	s_nop 0
	v_add_f32_e32 v116, v114, v115
	v_fmac_f32_e32 v116, v98, v113
	v_mul_f32_e32 v116, v116, v117
	v_fma_mixlo_f16 v116, v116, s30, 0
	global_store_short v99, v116, s[26:27]
	s_add_u32 s26, s26, 0x1000
	s_addc_u32 s27, s27, 0
	s_waitcnt vmcnt(16)
	s_waitcnt lgkmcnt(0)
	s_load_dwordx16 s[64:79], s[24:25], 0xc80
	s_load_dwordx16 s[80:95], s[24:25], 0xcc0
	v_cvt_f32_f16_e32 v113, v90
	v_mul_f32_e32 v112, v82, v113
	v_pk_mul_f32 v[104:105], v[82:83], v[2:3] op_sel_hi:[0,1]
	v_pk_mul_f32 v[106:107], v[82:83], v[4:5] op_sel_hi:[0,1]
	v_exp_f32_e32 v104, v104
	v_exp_f32_e32 v105, v105
	v_exp_f32_e32 v106, v106
	v_pk_mul_f32 v[104:105], v[18:19], v[104:105]
	v_exp_f32_e32 v107, v107
	v_pk_fma_f32 v[18:19], v[112:113], s[32:33], v[104:105] op_sel_hi:[0,1,1]
	v_pk_mul_f32 v[106:107], v[20:21], v[106:107]
	v_pk_fma_f32 v[114:115], s[48:49], v[18:19], 0 op_sel_hi:[1,1,0]
	v_pk_fma_f32 v[20:21], v[112:113], s[34:35], v[106:107] op_sel_hi:[0,1,1]
	v_pk_mul_f32 v[108:109], v[82:83], v[6:7] op_sel_hi:[0,1]
	v_pk_fma_f32 v[114:115], s[50:51], v[20:21], v[114:115]
	v_exp_f32_e32 v108, v108
	v_exp_f32_e32 v109, v109
	v_pk_mul_f32 v[110:111], v[82:83], v[8:9] op_sel_hi:[0,1]
	v_pk_mul_f32 v[108:109], v[22:23], v[108:109]
	v_exp_f32_e32 v110, v110
	v_pk_fma_f32 v[22:23], v[112:113], s[36:37], v[108:109] op_sel_hi:[0,1,1]
	v_exp_f32_e32 v111, v111
	v_pk_fma_f32 v[114:115], s[52:53], v[22:23], v[114:115]
	v_pk_mul_f32 v[110:111], v[24:25], v[110:111]
	v_pk_mul_f32 v[104:105], v[82:83], v[10:11] op_sel_hi:[0,1]
	v_pk_fma_f32 v[24:25], v[112:113], s[38:39], v[110:111] op_sel_hi:[0,1,1]
	v_exp_f32_e32 v104, v104
	v_pk_fma_f32 v[114:115], s[54:55], v[24:25], v[114:115]
	v_exp_f32_e32 v105, v105
	v_pk_mul_f32 v[106:107], v[82:83], v[12:13] op_sel_hi:[0,1]
	v_pk_mul_f32 v[104:105], v[26:27], v[104:105]
	v_exp_f32_e32 v106, v106
	v_pk_fma_f32 v[26:27], v[112:113], s[40:41], v[104:105] op_sel_hi:[0,1,1]
	v_exp_f32_e32 v107, v107
	v_pk_fma_f32 v[114:115], s[56:57], v[26:27], v[114:115]
	v_pk_mul_f32 v[106:107], v[28:29], v[106:107]
	v_pk_mul_f32 v[108:109], v[82:83], v[14:15] op_sel_hi:[0,1]
	v_pk_fma_f32 v[28:29], v[112:113], s[42:43], v[106:107] op_sel_hi:[0,1,1]
	v_exp_f32_e32 v108, v108
	v_pk_fma_f32 v[114:115], s[58:59], v[28:29], v[114:115]
	v_exp_f32_e32 v109, v109
	v_pk_mul_f32 v[110:111], v[82:83], v[16:17] op_sel_hi:[0,1]
	v_pk_mul_f32 v[108:109], v[30:31], v[108:109]
	v_exp_f32_e32 v110, v110
	v_pk_fma_f32 v[30:31], v[112:113], s[44:45], v[108:109] op_sel_hi:[0,1,1]
	v_exp_f32_e32 v111, v111
	v_pk_fma_f32 v[114:115], s[60:61], v[30:31], v[114:115]
	v_pk_mul_f32 v[110:111], v[32:33], v[110:111]
	v_cvt_f32_f16_e32 v117, v94
	v_pk_fma_f32 v[32:33], v[112:113], s[46:47], v[110:111] op_sel_hi:[0,1,1]
	s_nop 0
	v_pk_fma_f32 v[114:115], s[62:63], v[32:33], v[114:115]
	s_nop 0
	v_add_f32_e32 v116, v114, v115
	v_fmac_f32_e32 v116, v98, v113
	v_mul_f32_e32 v116, v116, v117
	v_fma_mixlo_f16 v116, v116, s30, 0
	global_store_short v99, v116, s[26:27]
	s_add_u32 s26, s26, 0x1000
	s_addc_u32 s27, s27, 0
	s_waitcnt lgkmcnt(0)
	s_load_dwordx16 s[32:47], s[24:25], 0xd00
	s_load_dwordx16 s[48:63], s[24:25], 0xd40
	v_cvt_f32_f16_sdwa v113, v90 dst_sel:DWORD dst_unused:UNUSED_PAD src0_sel:WORD_1
	v_pk_mul_f32 v[104:105], v[82:83], v[2:3] op_sel:[1,0]
	v_mul_f32_e32 v112, v83, v113
	v_exp_f32_e32 v104, v104
	v_exp_f32_e32 v105, v105
	v_pk_mul_f32 v[106:107], v[82:83], v[4:5] op_sel:[1,0]
	v_pk_mul_f32 v[104:105], v[18:19], v[104:105]
	v_exp_f32_e32 v106, v106
	v_pk_fma_f32 v[18:19], v[112:113], s[64:65], v[104:105] op_sel_hi:[0,1,1]
	v_exp_f32_e32 v107, v107
	v_pk_fma_f32 v[114:115], s[80:81], v[18:19], 0 op_sel_hi:[1,1,0]
	v_pk_mul_f32 v[106:107], v[20:21], v[106:107]
	v_pk_mul_f32 v[108:109], v[82:83], v[6:7] op_sel:[1,0]
	v_pk_fma_f32 v[20:21], v[112:113], s[66:67], v[106:107] op_sel_hi:[0,1,1]
	v_exp_f32_e32 v108, v108
	v_pk_fma_f32 v[114:115], s[82:83], v[20:21], v[114:115]
	v_exp_f32_e32 v109, v109
	v_pk_mul_f32 v[110:111], v[82:83], v[8:9] op_sel:[1,0]
	v_pk_mul_f32 v[108:109], v[22:23], v[108:109]
	v_exp_f32_e32 v110, v110
	v_pk_fma_f32 v[22:23], v[112:113], s[68:69], v[108:109] op_sel_hi:[0,1,1]
	v_exp_f32_e32 v111, v111
	v_pk_fma_f32 v[114:115], s[84:85], v[22:23], v[114:115]
	v_pk_mul_f32 v[110:111], v[24:25], v[110:111]
	v_pk_mul_f32 v[104:105], v[82:83], v[10:11] op_sel:[1,0]
	v_pk_fma_f32 v[24:25], v[112:113], s[70:71], v[110:111] op_sel_hi:[0,1,1]
	v_exp_f32_e32 v104, v104
	v_pk_fma_f32 v[114:115], s[86:87], v[24:25], v[114:115]
	v_exp_f32_e32 v105, v105
	v_pk_mul_f32 v[106:107], v[82:83], v[12:13] op_sel:[1,0]
	v_pk_mul_f32 v[104:105], v[26:27], v[104:105]
	v_exp_f32_e32 v106, v106
	v_pk_fma_f32 v[26:27], v[112:113], s[72:73], v[104:105] op_sel_hi:[0,1,1]
	v_exp_f32_e32 v107, v107
	v_pk_fma_f32 v[114:115], s[88:89], v[26:27], v[114:115]
	v_pk_mul_f32 v[106:107], v[28:29], v[106:107]
	v_pk_mul_f32 v[108:109], v[82:83], v[14:15] op_sel:[1,0]
	v_pk_fma_f32 v[28:29], v[112:113], s[74:75], v[106:107] op_sel_hi:[0,1,1]
	v_exp_f32_e32 v108, v108
	v_pk_fma_f32 v[114:115], s[90:91], v[28:29], v[114:115]
	v_exp_f32_e32 v109, v109
	v_pk_mul_f32 v[110:111], v[82:83], v[16:17] op_sel:[1,0]
	v_pk_mul_f32 v[108:109], v[30:31], v[108:109]
	v_exp_f32_e32 v110, v110
	v_pk_fma_f32 v[30:31], v[112:113], s[76:77], v[108:109] op_sel_hi:[0,1,1]
	v_exp_f32_e32 v111, v111
	v_pk_fma_f32 v[114:115], s[92:93], v[30:31], v[114:115]
	v_pk_mul_f32 v[110:111], v[32:33], v[110:111]
	v_cvt_f32_f16_sdwa v117, v94 dst_sel:DWORD dst_unused:UNUSED_PAD src0_sel:WORD_1
	v_pk_fma_f32 v[32:33], v[112:113], s[78:79], v[110:111] op_sel_hi:[0,1,1]
	s_nop 0
	v_pk_fma_f32 v[114:115], s[94:95], v[32:33], v[114:115]
	s_nop 0
	v_add_f32_e32 v116, v114, v115
	v_fmac_f32_e32 v116, v98, v113
	v_mul_f32_e32 v116, v116, v117
	v_fma_mixlo_f16 v116, v116, s30, 0
	global_store_short v99, v116, s[26:27]
	s_add_u32 s26, s26, 0x1000
	s_addc_u32 s27, s27, 0
	s_waitcnt lgkmcnt(0)
	s_load_dwordx16 s[64:79], s[24:25], 0xd80
	s_load_dwordx16 s[80:95], s[24:25], 0xdc0
	v_cvt_f32_f16_e32 v113, v91
	v_mul_f32_e32 v112, v84, v113
	v_pk_mul_f32 v[104:105], v[84:85], v[2:3] op_sel_hi:[0,1]
	v_pk_mul_f32 v[106:107], v[84:85], v[4:5] op_sel_hi:[0,1]
	v_exp_f32_e32 v104, v104
	v_exp_f32_e32 v105, v105
	v_exp_f32_e32 v106, v106
	v_pk_mul_f32 v[104:105], v[18:19], v[104:105]
	v_exp_f32_e32 v107, v107
	v_pk_fma_f32 v[18:19], v[112:113], s[32:33], v[104:105] op_sel_hi:[0,1,1]
	v_pk_mul_f32 v[106:107], v[20:21], v[106:107]
	v_pk_fma_f32 v[114:115], s[48:49], v[18:19], 0 op_sel_hi:[1,1,0]
	v_pk_fma_f32 v[20:21], v[112:113], s[34:35], v[106:107] op_sel_hi:[0,1,1]
	v_pk_mul_f32 v[108:109], v[84:85], v[6:7] op_sel_hi:[0,1]
	v_pk_fma_f32 v[114:115], s[50:51], v[20:21], v[114:115]
	v_exp_f32_e32 v108, v108
	v_exp_f32_e32 v109, v109
	v_pk_mul_f32 v[110:111], v[84:85], v[8:9] op_sel_hi:[0,1]
	v_pk_mul_f32 v[108:109], v[22:23], v[108:109]
	v_exp_f32_e32 v110, v110
	v_pk_fma_f32 v[22:23], v[112:113], s[36:37], v[108:109] op_sel_hi:[0,1,1]
	v_exp_f32_e32 v111, v111
	v_pk_fma_f32 v[114:115], s[52:53], v[22:23], v[114:115]
	v_pk_mul_f32 v[110:111], v[24:25], v[110:111]
	v_pk_mul_f32 v[104:105], v[84:85], v[10:11] op_sel_hi:[0,1]
	v_pk_fma_f32 v[24:25], v[112:113], s[38:39], v[110:111] op_sel_hi:[0,1,1]
	v_exp_f32_e32 v104, v104
	v_pk_fma_f32 v[114:115], s[54:55], v[24:25], v[114:115]
	v_exp_f32_e32 v105, v105
	v_pk_mul_f32 v[106:107], v[84:85], v[12:13] op_sel_hi:[0,1]
	v_pk_mul_f32 v[104:105], v[26:27], v[104:105]
	v_exp_f32_e32 v106, v106
	v_pk_fma_f32 v[26:27], v[112:113], s[40:41], v[104:105] op_sel_hi:[0,1,1]
	v_exp_f32_e32 v107, v107
	v_pk_fma_f32 v[114:115], s[56:57], v[26:27], v[114:115]
	v_pk_mul_f32 v[106:107], v[28:29], v[106:107]
	v_pk_mul_f32 v[108:109], v[84:85], v[14:15] op_sel_hi:[0,1]
	v_pk_fma_f32 v[28:29], v[112:113], s[42:43], v[106:107] op_sel_hi:[0,1,1]
	v_exp_f32_e32 v108, v108
	v_pk_fma_f32 v[114:115], s[58:59], v[28:29], v[114:115]
	v_exp_f32_e32 v109, v109
	v_pk_mul_f32 v[110:111], v[84:85], v[16:17] op_sel_hi:[0,1]
	v_pk_mul_f32 v[108:109], v[30:31], v[108:109]
	v_exp_f32_e32 v110, v110
	v_pk_fma_f32 v[30:31], v[112:113], s[44:45], v[108:109] op_sel_hi:[0,1,1]
	v_exp_f32_e32 v111, v111
	v_pk_fma_f32 v[114:115], s[60:61], v[30:31], v[114:115]
	v_pk_mul_f32 v[110:111], v[32:33], v[110:111]
	v_cvt_f32_f16_e32 v117, v95
	v_pk_fma_f32 v[32:33], v[112:113], s[46:47], v[110:111] op_sel_hi:[0,1,1]
	s_nop 0
	v_pk_fma_f32 v[114:115], s[62:63], v[32:33], v[114:115]
	s_nop 0
	v_add_f32_e32 v116, v114, v115
	v_fmac_f32_e32 v116, v98, v113
	v_mul_f32_e32 v116, v116, v117
	v_fma_mixlo_f16 v116, v116, s30, 0
	global_store_short v99, v116, s[26:27]
	s_add_u32 s26, s26, 0x1000
	s_addc_u32 s27, s27, 0
	s_waitcnt lgkmcnt(0)
	s_load_dwordx16 s[32:47], s[24:25], 0xe00
	s_load_dwordx16 s[48:63], s[24:25], 0xe40
	v_cvt_f32_f16_sdwa v113, v91 dst_sel:DWORD dst_unused:UNUSED_PAD src0_sel:WORD_1
	v_pk_mul_f32 v[104:105], v[84:85], v[2:3] op_sel:[1,0]
	v_mul_f32_e32 v112, v85, v113
	v_exp_f32_e32 v104, v104
	v_exp_f32_e32 v105, v105
	v_pk_mul_f32 v[106:107], v[84:85], v[4:5] op_sel:[1,0]
	v_pk_mul_f32 v[104:105], v[18:19], v[104:105]
	v_exp_f32_e32 v106, v106
	v_pk_fma_f32 v[18:19], v[112:113], s[64:65], v[104:105] op_sel_hi:[0,1,1]
	v_exp_f32_e32 v107, v107
	v_pk_fma_f32 v[114:115], s[80:81], v[18:19], 0 op_sel_hi:[1,1,0]
	v_pk_mul_f32 v[106:107], v[20:21], v[106:107]
	v_pk_mul_f32 v[108:109], v[84:85], v[6:7] op_sel:[1,0]
	v_pk_fma_f32 v[20:21], v[112:113], s[66:67], v[106:107] op_sel_hi:[0,1,1]
	v_exp_f32_e32 v108, v108
	v_pk_fma_f32 v[114:115], s[82:83], v[20:21], v[114:115]
	v_exp_f32_e32 v109, v109
	v_pk_mul_f32 v[110:111], v[84:85], v[8:9] op_sel:[1,0]
	v_pk_mul_f32 v[108:109], v[22:23], v[108:109]
	v_exp_f32_e32 v110, v110
	v_pk_fma_f32 v[22:23], v[112:113], s[68:69], v[108:109] op_sel_hi:[0,1,1]
	v_exp_f32_e32 v111, v111
	v_pk_fma_f32 v[114:115], s[84:85], v[22:23], v[114:115]
	v_pk_mul_f32 v[110:111], v[24:25], v[110:111]
	v_pk_mul_f32 v[104:105], v[84:85], v[10:11] op_sel:[1,0]
	v_pk_fma_f32 v[24:25], v[112:113], s[70:71], v[110:111] op_sel_hi:[0,1,1]
	v_exp_f32_e32 v104, v104
	v_pk_fma_f32 v[114:115], s[86:87], v[24:25], v[114:115]
	v_exp_f32_e32 v105, v105
	v_pk_mul_f32 v[106:107], v[84:85], v[12:13] op_sel:[1,0]
	v_pk_mul_f32 v[104:105], v[26:27], v[104:105]
	v_exp_f32_e32 v106, v106
	v_pk_fma_f32 v[26:27], v[112:113], s[72:73], v[104:105] op_sel_hi:[0,1,1]
	v_exp_f32_e32 v107, v107
	v_pk_fma_f32 v[114:115], s[88:89], v[26:27], v[114:115]
	v_pk_mul_f32 v[106:107], v[28:29], v[106:107]
	v_pk_mul_f32 v[108:109], v[84:85], v[14:15] op_sel:[1,0]
	v_pk_fma_f32 v[28:29], v[112:113], s[74:75], v[106:107] op_sel_hi:[0,1,1]
	v_exp_f32_e32 v108, v108
	v_pk_fma_f32 v[114:115], s[90:91], v[28:29], v[114:115]
	v_exp_f32_e32 v109, v109
	v_pk_mul_f32 v[110:111], v[84:85], v[16:17] op_sel:[1,0]
	v_pk_mul_f32 v[108:109], v[30:31], v[108:109]
	v_exp_f32_e32 v110, v110
	v_pk_fma_f32 v[30:31], v[112:113], s[76:77], v[108:109] op_sel_hi:[0,1,1]
	v_exp_f32_e32 v111, v111
	v_pk_fma_f32 v[114:115], s[92:93], v[30:31], v[114:115]
	v_pk_mul_f32 v[110:111], v[32:33], v[110:111]
	v_cvt_f32_f16_sdwa v117, v95 dst_sel:DWORD dst_unused:UNUSED_PAD src0_sel:WORD_1
	v_pk_fma_f32 v[32:33], v[112:113], s[78:79], v[110:111] op_sel_hi:[0,1,1]
	s_nop 0
	v_pk_fma_f32 v[114:115], s[94:95], v[32:33], v[114:115]
	s_nop 0
	v_add_f32_e32 v116, v114, v115
	v_fmac_f32_e32 v116, v98, v113
	v_mul_f32_e32 v116, v116, v117
	v_fma_mixlo_f16 v116, v116, s30, 0
	global_store_short v99, v116, s[26:27]
	s_add_u32 s26, s26, 0x1000
	s_addc_u32 s27, s27, 0
	s_waitcnt lgkmcnt(0)
	s_load_dwordx16 s[64:79], s[24:25], 0xe80
	s_load_dwordx16 s[80:95], s[24:25], 0xec0
	v_cvt_f32_f16_e32 v113, v92
	v_mul_f32_e32 v112, v86, v113
	v_pk_mul_f32 v[104:105], v[86:87], v[2:3] op_sel_hi:[0,1]
	v_pk_mul_f32 v[106:107], v[86:87], v[4:5] op_sel_hi:[0,1]
	v_exp_f32_e32 v104, v104
	v_exp_f32_e32 v105, v105
	v_exp_f32_e32 v106, v106
	v_pk_mul_f32 v[104:105], v[18:19], v[104:105]
	v_exp_f32_e32 v107, v107
	v_pk_fma_f32 v[18:19], v[112:113], s[32:33], v[104:105] op_sel_hi:[0,1,1]
	v_pk_mul_f32 v[106:107], v[20:21], v[106:107]
	v_pk_fma_f32 v[114:115], s[48:49], v[18:19], 0 op_sel_hi:[1,1,0]
	v_pk_fma_f32 v[20:21], v[112:113], s[34:35], v[106:107] op_sel_hi:[0,1,1]
	v_pk_mul_f32 v[108:109], v[86:87], v[6:7] op_sel_hi:[0,1]
	v_pk_fma_f32 v[114:115], s[50:51], v[20:21], v[114:115]
	v_exp_f32_e32 v108, v108
	v_exp_f32_e32 v109, v109
	v_pk_mul_f32 v[110:111], v[86:87], v[8:9] op_sel_hi:[0,1]
	v_pk_mul_f32 v[108:109], v[22:23], v[108:109]
	v_exp_f32_e32 v110, v110
	v_pk_fma_f32 v[22:23], v[112:113], s[36:37], v[108:109] op_sel_hi:[0,1,1]
	v_exp_f32_e32 v111, v111
	v_pk_fma_f32 v[114:115], s[52:53], v[22:23], v[114:115]
	v_pk_mul_f32 v[110:111], v[24:25], v[110:111]
	v_pk_mul_f32 v[104:105], v[86:87], v[10:11] op_sel_hi:[0,1]
	v_pk_fma_f32 v[24:25], v[112:113], s[38:39], v[110:111] op_sel_hi:[0,1,1]
	v_exp_f32_e32 v104, v104
	v_pk_fma_f32 v[114:115], s[54:55], v[24:25], v[114:115]
	v_exp_f32_e32 v105, v105
	v_pk_mul_f32 v[106:107], v[86:87], v[12:13] op_sel_hi:[0,1]
	v_pk_mul_f32 v[104:105], v[26:27], v[104:105]
	v_exp_f32_e32 v106, v106
	v_pk_fma_f32 v[26:27], v[112:113], s[40:41], v[104:105] op_sel_hi:[0,1,1]
	v_exp_f32_e32 v107, v107
	v_pk_fma_f32 v[114:115], s[56:57], v[26:27], v[114:115]
	v_pk_mul_f32 v[106:107], v[28:29], v[106:107]
	v_pk_mul_f32 v[108:109], v[86:87], v[14:15] op_sel_hi:[0,1]
	v_pk_fma_f32 v[28:29], v[112:113], s[42:43], v[106:107] op_sel_hi:[0,1,1]
	v_exp_f32_e32 v108, v108
	v_pk_fma_f32 v[114:115], s[58:59], v[28:29], v[114:115]
	v_exp_f32_e32 v109, v109
	v_pk_mul_f32 v[110:111], v[86:87], v[16:17] op_sel_hi:[0,1]
	v_pk_mul_f32 v[108:109], v[30:31], v[108:109]
	v_exp_f32_e32 v110, v110
	v_pk_fma_f32 v[30:31], v[112:113], s[44:45], v[108:109] op_sel_hi:[0,1,1]
	v_exp_f32_e32 v111, v111
	v_pk_fma_f32 v[114:115], s[60:61], v[30:31], v[114:115]
	v_pk_mul_f32 v[110:111], v[32:33], v[110:111]
	v_cvt_f32_f16_e32 v117, v96
	v_pk_fma_f32 v[32:33], v[112:113], s[46:47], v[110:111] op_sel_hi:[0,1,1]
	s_nop 0
	v_pk_fma_f32 v[114:115], s[62:63], v[32:33], v[114:115]
	s_nop 0
	v_add_f32_e32 v116, v114, v115
	v_fmac_f32_e32 v116, v98, v113
	v_mul_f32_e32 v116, v116, v117
	v_fma_mixlo_f16 v116, v116, s30, 0
	global_store_short v99, v116, s[26:27]
	s_add_u32 s26, s26, 0x1000
	s_addc_u32 s27, s27, 0
	s_waitcnt lgkmcnt(0)
	s_load_dwordx16 s[32:47], s[24:25], 0xf00
	s_load_dwordx16 s[48:63], s[24:25], 0xf40
	v_cvt_f32_f16_sdwa v113, v92 dst_sel:DWORD dst_unused:UNUSED_PAD src0_sel:WORD_1
	v_pk_mul_f32 v[104:105], v[86:87], v[2:3] op_sel:[1,0]
	v_mul_f32_e32 v112, v87, v113
	v_exp_f32_e32 v104, v104
	v_exp_f32_e32 v105, v105
	v_pk_mul_f32 v[106:107], v[86:87], v[4:5] op_sel:[1,0]
	v_pk_mul_f32 v[104:105], v[18:19], v[104:105]
	v_exp_f32_e32 v106, v106
	v_pk_fma_f32 v[18:19], v[112:113], s[64:65], v[104:105] op_sel_hi:[0,1,1]
	v_exp_f32_e32 v107, v107
	v_pk_fma_f32 v[114:115], s[80:81], v[18:19], 0 op_sel_hi:[1,1,0]
	v_pk_mul_f32 v[106:107], v[20:21], v[106:107]
	v_pk_mul_f32 v[108:109], v[86:87], v[6:7] op_sel:[1,0]
	v_pk_fma_f32 v[20:21], v[112:113], s[66:67], v[106:107] op_sel_hi:[0,1,1]
	v_exp_f32_e32 v108, v108
	v_pk_fma_f32 v[114:115], s[82:83], v[20:21], v[114:115]
	v_exp_f32_e32 v109, v109
	v_pk_mul_f32 v[110:111], v[86:87], v[8:9] op_sel:[1,0]
	v_pk_mul_f32 v[108:109], v[22:23], v[108:109]
	v_exp_f32_e32 v110, v110
	v_pk_fma_f32 v[22:23], v[112:113], s[68:69], v[108:109] op_sel_hi:[0,1,1]
	v_exp_f32_e32 v111, v111
	v_pk_fma_f32 v[114:115], s[84:85], v[22:23], v[114:115]
	v_pk_mul_f32 v[110:111], v[24:25], v[110:111]
	v_pk_mul_f32 v[104:105], v[86:87], v[10:11] op_sel:[1,0]
	v_pk_fma_f32 v[24:25], v[112:113], s[70:71], v[110:111] op_sel_hi:[0,1,1]
	v_exp_f32_e32 v104, v104
	v_pk_fma_f32 v[114:115], s[86:87], v[24:25], v[114:115]
	v_exp_f32_e32 v105, v105
	v_pk_mul_f32 v[106:107], v[86:87], v[12:13] op_sel:[1,0]
	v_pk_mul_f32 v[104:105], v[26:27], v[104:105]
	v_exp_f32_e32 v106, v106
	v_pk_fma_f32 v[26:27], v[112:113], s[72:73], v[104:105] op_sel_hi:[0,1,1]
	v_exp_f32_e32 v107, v107
	v_pk_fma_f32 v[114:115], s[88:89], v[26:27], v[114:115]
	v_pk_mul_f32 v[106:107], v[28:29], v[106:107]
	v_pk_mul_f32 v[108:109], v[86:87], v[14:15] op_sel:[1,0]
	v_pk_fma_f32 v[28:29], v[112:113], s[74:75], v[106:107] op_sel_hi:[0,1,1]
	v_exp_f32_e32 v108, v108
	v_pk_fma_f32 v[114:115], s[90:91], v[28:29], v[114:115]
	v_exp_f32_e32 v109, v109
	v_pk_mul_f32 v[110:111], v[86:87], v[16:17] op_sel:[1,0]
	v_pk_mul_f32 v[108:109], v[30:31], v[108:109]
	v_exp_f32_e32 v110, v110
	v_pk_fma_f32 v[30:31], v[112:113], s[76:77], v[108:109] op_sel_hi:[0,1,1]
	v_exp_f32_e32 v111, v111
	v_pk_fma_f32 v[114:115], s[92:93], v[30:31], v[114:115]
	v_pk_mul_f32 v[110:111], v[32:33], v[110:111]
	v_cvt_f32_f16_sdwa v117, v96 dst_sel:DWORD dst_unused:UNUSED_PAD src0_sel:WORD_1
	v_pk_fma_f32 v[32:33], v[112:113], s[78:79], v[110:111] op_sel_hi:[0,1,1]
	s_nop 0
	v_pk_fma_f32 v[114:115], s[94:95], v[32:33], v[114:115]
	s_nop 0
	v_add_f32_e32 v116, v114, v115
	v_fmac_f32_e32 v116, v98, v113
	v_mul_f32_e32 v116, v116, v117
	v_fma_mixlo_f16 v116, v116, s30, 0
	global_store_short v99, v116, s[26:27]
	s_add_u32 s26, s26, 0x1000
	s_addc_u32 s27, s27, 0
	s_waitcnt lgkmcnt(0)
	s_load_dwordx16 s[64:79], s[24:25], 0xf80
	s_load_dwordx16 s[80:95], s[24:25], 0xfc0
	v_cvt_f32_f16_e32 v113, v93
	v_mul_f32_e32 v112, v88, v113
	v_pk_mul_f32 v[104:105], v[88:89], v[2:3] op_sel_hi:[0,1]
	v_pk_mul_f32 v[106:107], v[88:89], v[4:5] op_sel_hi:[0,1]
	v_exp_f32_e32 v104, v104
	v_exp_f32_e32 v105, v105
	v_exp_f32_e32 v106, v106
	v_pk_mul_f32 v[104:105], v[18:19], v[104:105]
	v_exp_f32_e32 v107, v107
	v_pk_fma_f32 v[18:19], v[112:113], s[32:33], v[104:105] op_sel_hi:[0,1,1]
	v_pk_mul_f32 v[106:107], v[20:21], v[106:107]
	v_pk_fma_f32 v[114:115], s[48:49], v[18:19], 0 op_sel_hi:[1,1,0]
	v_pk_fma_f32 v[20:21], v[112:113], s[34:35], v[106:107] op_sel_hi:[0,1,1]
	v_pk_mul_f32 v[108:109], v[88:89], v[6:7] op_sel_hi:[0,1]
	v_pk_fma_f32 v[114:115], s[50:51], v[20:21], v[114:115]
	v_exp_f32_e32 v108, v108
	v_exp_f32_e32 v109, v109
	v_pk_mul_f32 v[110:111], v[88:89], v[8:9] op_sel_hi:[0,1]
	v_pk_mul_f32 v[108:109], v[22:23], v[108:109]
	v_exp_f32_e32 v110, v110
	v_pk_fma_f32 v[22:23], v[112:113], s[36:37], v[108:109] op_sel_hi:[0,1,1]
	v_exp_f32_e32 v111, v111
	v_pk_fma_f32 v[114:115], s[52:53], v[22:23], v[114:115]
	v_pk_mul_f32 v[110:111], v[24:25], v[110:111]
	v_pk_mul_f32 v[104:105], v[88:89], v[10:11] op_sel_hi:[0,1]
	v_pk_fma_f32 v[24:25], v[112:113], s[38:39], v[110:111] op_sel_hi:[0,1,1]
	v_exp_f32_e32 v104, v104
	v_pk_fma_f32 v[114:115], s[54:55], v[24:25], v[114:115]
	v_exp_f32_e32 v105, v105
	v_pk_mul_f32 v[106:107], v[88:89], v[12:13] op_sel_hi:[0,1]
	v_pk_mul_f32 v[104:105], v[26:27], v[104:105]
	v_exp_f32_e32 v106, v106
	v_pk_fma_f32 v[26:27], v[112:113], s[40:41], v[104:105] op_sel_hi:[0,1,1]
	v_exp_f32_e32 v107, v107
	v_pk_fma_f32 v[114:115], s[56:57], v[26:27], v[114:115]
	v_pk_mul_f32 v[106:107], v[28:29], v[106:107]
	v_pk_mul_f32 v[108:109], v[88:89], v[14:15] op_sel_hi:[0,1]
	v_pk_fma_f32 v[28:29], v[112:113], s[42:43], v[106:107] op_sel_hi:[0,1,1]
	v_exp_f32_e32 v108, v108
	v_pk_fma_f32 v[114:115], s[58:59], v[28:29], v[114:115]
	v_exp_f32_e32 v109, v109
	v_pk_mul_f32 v[110:111], v[88:89], v[16:17] op_sel_hi:[0,1]
	v_pk_mul_f32 v[108:109], v[30:31], v[108:109]
	v_exp_f32_e32 v110, v110
	v_pk_fma_f32 v[30:31], v[112:113], s[44:45], v[108:109] op_sel_hi:[0,1,1]
	v_exp_f32_e32 v111, v111
	v_pk_fma_f32 v[114:115], s[60:61], v[30:31], v[114:115]
	v_pk_mul_f32 v[110:111], v[32:33], v[110:111]
	v_cvt_f32_f16_e32 v117, v97
	v_pk_fma_f32 v[32:33], v[112:113], s[46:47], v[110:111] op_sel_hi:[0,1,1]
	s_nop 0
	v_pk_fma_f32 v[114:115], s[62:63], v[32:33], v[114:115]
	s_nop 0
	v_add_f32_e32 v116, v114, v115
	v_fmac_f32_e32 v116, v98, v113
	v_mul_f32_e32 v116, v116, v117
	v_fma_mixlo_f16 v116, v116, s30, 0
	global_store_short v99, v116, s[26:27]
	s_add_u32 s26, s26, 0x1000
	s_addc_u32 s27, s27, 0
	s_waitcnt lgkmcnt(0)
	v_cvt_f32_f16_sdwa v113, v93 dst_sel:DWORD dst_unused:UNUSED_PAD src0_sel:WORD_1
	v_pk_mul_f32 v[104:105], v[88:89], v[2:3] op_sel:[1,0]
	v_mul_f32_e32 v112, v89, v113
	v_exp_f32_e32 v104, v104
	v_exp_f32_e32 v105, v105
	v_pk_mul_f32 v[106:107], v[88:89], v[4:5] op_sel:[1,0]
	v_pk_mul_f32 v[104:105], v[18:19], v[104:105]
	v_exp_f32_e32 v106, v106
	v_pk_fma_f32 v[18:19], v[112:113], s[64:65], v[104:105] op_sel_hi:[0,1,1]
	v_exp_f32_e32 v107, v107
	v_pk_fma_f32 v[114:115], s[80:81], v[18:19], 0 op_sel_hi:[1,1,0]
	v_pk_mul_f32 v[106:107], v[20:21], v[106:107]
	v_pk_mul_f32 v[108:109], v[88:89], v[6:7] op_sel:[1,0]
	v_pk_fma_f32 v[20:21], v[112:113], s[66:67], v[106:107] op_sel_hi:[0,1,1]
	v_exp_f32_e32 v108, v108
	v_pk_fma_f32 v[114:115], s[82:83], v[20:21], v[114:115]
	v_exp_f32_e32 v109, v109
	v_pk_mul_f32 v[110:111], v[88:89], v[8:9] op_sel:[1,0]
	v_pk_mul_f32 v[108:109], v[22:23], v[108:109]
	v_exp_f32_e32 v110, v110
	v_pk_fma_f32 v[22:23], v[112:113], s[68:69], v[108:109] op_sel_hi:[0,1,1]
	v_exp_f32_e32 v111, v111
	v_pk_fma_f32 v[114:115], s[84:85], v[22:23], v[114:115]
	v_pk_mul_f32 v[110:111], v[24:25], v[110:111]
	v_pk_mul_f32 v[104:105], v[88:89], v[10:11] op_sel:[1,0]
	v_pk_fma_f32 v[24:25], v[112:113], s[70:71], v[110:111] op_sel_hi:[0,1,1]
	v_exp_f32_e32 v104, v104
	v_pk_fma_f32 v[114:115], s[86:87], v[24:25], v[114:115]
	v_exp_f32_e32 v105, v105
	v_pk_mul_f32 v[106:107], v[88:89], v[12:13] op_sel:[1,0]
	v_pk_mul_f32 v[104:105], v[26:27], v[104:105]
	v_exp_f32_e32 v106, v106
	v_pk_fma_f32 v[26:27], v[112:113], s[72:73], v[104:105] op_sel_hi:[0,1,1]
	v_exp_f32_e32 v107, v107
	v_pk_fma_f32 v[114:115], s[88:89], v[26:27], v[114:115]
	v_pk_mul_f32 v[106:107], v[28:29], v[106:107]
	v_pk_mul_f32 v[108:109], v[88:89], v[14:15] op_sel:[1,0]
	v_pk_fma_f32 v[28:29], v[112:113], s[74:75], v[106:107] op_sel_hi:[0,1,1]
	v_exp_f32_e32 v108, v108
	v_pk_fma_f32 v[114:115], s[90:91], v[28:29], v[114:115]
	v_exp_f32_e32 v109, v109
	v_pk_mul_f32 v[110:111], v[88:89], v[16:17] op_sel:[1,0]
	v_pk_mul_f32 v[108:109], v[30:31], v[108:109]
	v_exp_f32_e32 v110, v110
	v_pk_fma_f32 v[30:31], v[112:113], s[76:77], v[108:109] op_sel_hi:[0,1,1]
	v_exp_f32_e32 v111, v111
	v_pk_fma_f32 v[114:115], s[92:93], v[30:31], v[114:115]
	v_pk_mul_f32 v[110:111], v[32:33], v[110:111]
	v_cvt_f32_f16_sdwa v117, v97 dst_sel:DWORD dst_unused:UNUSED_PAD src0_sel:WORD_1
	v_pk_fma_f32 v[32:33], v[112:113], s[78:79], v[110:111] op_sel_hi:[0,1,1]
	s_nop 0
	v_pk_fma_f32 v[114:115], s[94:95], v[32:33], v[114:115]
	s_nop 0
	v_add_f32_e32 v116, v114, v115
	v_fmac_f32_e32 v116, v98, v113
	v_mul_f32_e32 v116, v116, v117
	v_fma_mixlo_f16 v116, v116, s30, 0
	global_store_short v99, v116, s[26:27]
	s_endpgm
	.p2alignl 8, 3212836864

amdhsa.kernels:
  - .agpr_count:     0
    .args:
      - .address_space:  global
        .offset:         0
        .size:           8
        .value_kind:     global_buffer
      - .address_space:  global
        .offset:         8
        .size:           8
        .value_kind:     global_buffer
      - .offset:         16
        .size:           8
        .value_kind:     by_value
      - .address_space:  global
        .offset:         24
        .size:           8
        .value_kind:     global_buffer
      - .address_space:  global
        .offset:         32
        .size:           8
        .value_kind:     global_buffer
      - .offset:         40
        .size:           8
        .value_kind:     by_value
      - .address_space:  global
        .offset:         48
        .size:           8
        .value_kind:     global_buffer
      - .address_space:  global
        .offset:         56
        .size:           8
        .value_kind:     global_buffer
      - .offset:         64
        .size:           8
        .value_kind:     by_value
      - .address_space:  global
        .offset:         72
        .size:           8
        .value_kind:     global_buffer
      - .address_space:  global
        .offset:         80
        .size:           8
        .value_kind:     global_buffer
      - .offset:         88
        .size:           8
        .value_kind:     by_value
      - .address_space:  global
        .offset:         96
        .size:           8
        .value_kind:     global_buffer
      - .address_space:  global
        .offset:         104
        .size:           8
        .value_kind:     global_buffer
      - .offset:         112
        .size:           8
        .value_kind:     by_value
      - .address_space:  global
        .offset:         120
        .size:           8
        .value_kind:     global_buffer
      - .actual_access:  read_only
        .address_space:  global
        .offset:         128
        .size:           8
        .value_kind:     global_buffer
      - .actual_access:  write_only
        .address_space:  global
        .offset:         136
        .size:           8
        .value_kind:     global_buffer
    .group_segment_fixed_size: 0
    .kernarg_segment_align: 8
    .kernarg_segment_size: 144
    .language:       OpenCL C
    .language_version:
      - 2
      - 0
    .max_flat_workgroup_size: 256
    .name:           _Z10cvt_kernelPKfPDF16_lS0_S1_lS0_S1_lS0_S1_lS0_S1_lPjS0_Pf
    .private_segment_fixed_size: 0
    .sgpr_count:     58
    .sgpr_spill_count: 0
    .symbol:         _Z10cvt_kernelPKfPDF16_lS0_S1_lS0_S1_lS0_S1_lS0_S1_lPjS0_Pf.kd
    .uniform_work_group_size: 1
    .uses_dynamic_stack: false
    .vgpr_count:     18
    .vgpr_spill_count: 0
    .wavefront_size: 64
  - .agpr_count:     0
    .args:
      - .actual_access:  read_only
        .address_space:  global
        .offset:         0
        .size:           8
        .value_kind:     global_buffer
      - .actual_access:  read_only
        .address_space:  global
        .offset:         8
        .size:           8
        .value_kind:     global_buffer
      - .actual_access:  read_only
        .address_space:  global
        .offset:         16
        .size:           8
        .value_kind:     global_buffer
      - .actual_access:  read_only
        .address_space:  global
        .offset:         24
        .size:           8
        .value_kind:     global_buffer
      - .actual_access:  write_only
        .address_space:  global
        .offset:         32
        .size:           8
        .value_kind:     global_buffer
      - .actual_access:  write_only
        .address_space:  global
        .offset:         40
        .size:           8
        .value_kind:     global_buffer
      - .actual_access:  write_only
        .address_space:  global
        .offset:         48
        .size:           8
        .value_kind:     global_buffer
    .group_segment_fixed_size: 65792
    .kernarg_segment_align: 8
    .kernarg_segment_size: 56
    .language:       OpenCL C
    .language_version:
      - 2
      - 0
    .max_flat_workgroup_size: 1024
    .name:           _Z17conv_xproj_kernelPKDF16_PKfS2_S0_PDF16_S3_Pf
    .private_segment_fixed_size: 0
    .sgpr_count:     22
    .sgpr_spill_count: 0
    .symbol:         _Z17conv_xproj_kernelPKDF16_PKfS2_S0_PDF16_S3_Pf.kd
    .uniform_work_group_size: 1
    .uses_dynamic_stack: false
    .vgpr_count:     126
    .vgpr_spill_count: 0
    .wavefront_size: 64
  - .agpr_count:     0
    .args:
      - .actual_access:  read_only
        .address_space:  global
        .offset:         0
        .size:           8
        .value_kind:     global_buffer
      - .actual_access:  read_only
        .address_space:  global
        .offset:         8
        .size:           8
        .value_kind:     global_buffer
      - .actual_access:  read_only
        .address_space:  global
        .offset:         16
        .size:           8
        .value_kind:     global_buffer
      - .actual_access:  read_only
        .address_space:  global
        .offset:         24
        .size:           8
        .value_kind:     global_buffer
      - .actual_access:  read_only
        .address_space:  global
        .offset:         32
        .size:           8
        .value_kind:     global_buffer
      - .actual_access:  read_only
        .address_space:  global
        .offset:         40
        .size:           8
        .value_kind:     global_buffer
      - .actual_access:  write_only
        .address_space:  global
        .offset:         48
        .size:           8
        .value_kind:     global_buffer
      - .actual_access:  write_only
        .address_space:  global
        .offset:         56
        .size:           8
        .value_kind:     global_buffer
      - .actual_access:  write_only
        .address_space:  global
        .offset:         64
        .size:           8
        .value_kind:     global_buffer
      - .actual_access:  read_only
        .address_space:  global
        .offset:         72
        .size:           8
        .value_kind:     global_buffer
      - .actual_access:  write_only
        .address_space:  global
        .offset:         80
        .size:           8
        .value_kind:     global_buffer
    .group_segment_fixed_size: 4096
    .kernarg_segment_align: 8
    .kernarg_segment_size: 88
    .language:       OpenCL C
    .language_version:
      - 2
      - 0
    .max_flat_workgroup_size: 256
    .name:           _Z10scan_pass1PKDF16_S0_PKfS0_S2_S2_PDF16_PfS4_S2_S3_
    .private_segment_fixed_size: 0
    .sgpr_count:     94
    .sgpr_spill_count: 0
    .symbol:         _Z10scan_pass1PKDF16_S0_PKfS0_S2_S2_PDF16_PfS4_S2_S3_.kd
    .uniform_work_group_size: 1
    .uses_dynamic_stack: false
    .vgpr_count:     128
    .vgpr_spill_count: 0
    .wavefront_size: 64
  - .agpr_count:     0
    .args:
      - .actual_access:  read_only
        .address_space:  global
        .offset:         0
        .size:           8
        .value_kind:     global_buffer
      - .actual_access:  read_only
        .address_space:  global
        .offset:         8
        .size:           8
        .value_kind:     global_buffer
      - .actual_access:  read_only
        .address_space:  global
        .offset:         16
        .size:           8
        .value_kind:     global_buffer
      - .actual_access:  read_only
        .address_space:  global
        .offset:         24
        .size:           8
        .value_kind:     global_buffer
      - .actual_access:  read_only
        .address_space:  global
        .offset:         32
        .size:           8
        .value_kind:     global_buffer
      - .actual_access:  read_only
        .address_space:  global
        .offset:         40
        .size:           8
        .value_kind:     global_buffer
      - .actual_access:  write_only
        .address_space:  global
        .offset:         48
        .size:           8
        .value_kind:     global_buffer
      - .actual_access:  read_only
        .address_space:  global
        .offset:         56
        .size:           8
        .value_kind:     global_buffer
    .group_segment_fixed_size: 4096
    .kernarg_segment_align: 8
    .kernarg_segment_size: 64
    .language:       OpenCL C
    .language_version:
      - 2
      - 0
    .max_flat_workgroup_size: 256
    .name:           _Z10scan_pass2PKDF16_PKfS2_S0_S2_S0_PDF16_S2_
    .private_segment_fixed_size: 0
    .sgpr_count:     104
    .sgpr_spill_count: 0
    .symbol:         _Z10scan_pass2PKDF16_PKfS2_S0_S2_S0_PDF16_S2_.kd
    .uniform_work_group_size: 1
    .uses_dynamic_stack: false
    .vgpr_count:     118
    .vgpr_spill_count: 0
    .wavefront_size: 64
  - .agpr_count:     0
    .args:
      - .actual_access:  read_only
        .address_space:  global
        .offset:         0
        .size:           8
        .value_kind:     global_buffer
      - .actual_access:  read_only
        .address_space:  global
        .offset:         8
        .size:           8
        .value_kind:     global_buffer
      - .actual_access:  read_only
        .address_space:  global
        .offset:         16
        .size:           8
        .value_kind:     global_buffer
      - .actual_access:  write_only
        .address_space:  global
        .offset:         24
        .size:           8
        .value_kind:     global_buffer
    .group_segment_fixed_size: 8192
    .kernarg_segment_align: 8
    .kernarg_segment_size: 32
    .language:       OpenCL C
    .language_version:
      - 2
      - 0
    .max_flat_workgroup_size: 512
    .name:           _Z12scan_combinePKfPKDF16_S0_PDF16_
    .private_segment_fixed_size: 0
    .sgpr_count:     20
    .sgpr_spill_count: 0
    .symbol:         _Z12scan_combinePKfPKDF16_S0_PDF16_.kd
    .uniform_work_group_size: 1
    .uses_dynamic_stack: false
    .vgpr_count:     66
    .vgpr_spill_count: 0
    .wavefront_size: 64
  - .agpr_count:     0
    .args:
      - .address_space:  global
        .offset:         0
        .size:           8
        .value_kind:     global_buffer
      - .address_space:  global
        .offset:         8
        .size:           8
        .value_kind:     global_buffer
      - .actual_access:  write_only
        .address_space:  global
        .offset:         16
        .size:           8
        .value_kind:     global_buffer
      - .actual_access:  read_only
        .address_space:  global
        .offset:         24
        .size:           8
        .value_kind:     global_buffer
      - .offset:         32
        .size:           4
        .value_kind:     by_value
      - .actual_access:  read_only
        .address_space:  global
        .offset:         40
        .size:           8
        .value_kind:     global_buffer
    .group_segment_fixed_size: 0
    .kernarg_segment_align: 8
    .kernarg_segment_size: 48
    .language:       OpenCL C
    .language_version:
      - 2
      - 0
    .max_flat_workgroup_size: 512
    .name:           _Z11gemm_8phaseILi0ELi16ELi16ELi1024ELi1024ELi4096ELi1EEvPKDF16_S1_PvS2_fPj
    .private_segment_fixed_size: 0
    .sgpr_count:     38
    .sgpr_spill_count: 0
    .symbol:         _Z11gemm_8phaseILi0ELi16ELi16ELi1024ELi1024ELi4096ELi1EEvPKDF16_S1_PvS2_fPj.kd
    .uniform_work_group_size: 1
    .uses_dynamic_stack: false
    .vgpr_count:     236
    .vgpr_spill_count: 0
    .wavefront_size: 64
  - .agpr_count:     0
    .args:
      - .address_space:  global
        .offset:         0
        .size:           8
        .value_kind:     global_buffer
      - .address_space:  global
        .offset:         8
        .size:           8
        .value_kind:     global_buffer
      - .actual_access:  write_only
        .address_space:  global
        .offset:         16
        .size:           8
        .value_kind:     global_buffer
      - .address_space:  global
        .offset:         24
        .size:           8
        .value_kind:     global_buffer
      - .offset:         32
        .size:           4
        .value_kind:     by_value
      - .address_space:  global
        .offset:         40
        .size:           8
        .value_kind:     global_buffer
    .group_segment_fixed_size: 0
    .kernarg_segment_align: 8
    .kernarg_segment_size: 48
    .language:       OpenCL C
    .language_version:
      - 2
      - 0
    .max_flat_workgroup_size: 512
    .name:           _Z11gemm_8phaseILi1ELi16ELi4ELi512ELi2048ELi1024ELi4EEvPKDF16_S1_PvS2_fPj
    .private_segment_fixed_size: 0
    .sgpr_count:     41
    .sgpr_spill_count: 0
    .symbol:         _Z11gemm_8phaseILi1ELi16ELi4ELi512ELi2048ELi1024ELi4EEvPKDF16_S1_PvS2_fPj.kd
    .uniform_work_group_size: 1
    .uses_dynamic_stack: false
    .vgpr_count:     236
    .vgpr_spill_count: 0
    .wavefront_size: 64
  - .agpr_count:     0
    .args:
      - .address_space:  global
        .offset:         0
        .size:           8
        .value_kind:     global_buffer
      - .address_space:  global
        .offset:         8
        .size:           8
        .value_kind:     global_buffer
      - .actual_access:  write_only
        .address_space:  global
        .offset:         16
        .size:           8
        .value_kind:     global_buffer
      - .address_space:  global
        .offset:         24
        .size:           8
        .value_kind:     global_buffer
      - .offset:         32
        .size:           4
        .value_kind:     by_value
      - .address_space:  global
        .offset:         40
        .size:           8
        .value_kind:     global_buffer
    .group_segment_fixed_size: 0
    .kernarg_segment_align: 8
    .kernarg_segment_size: 48
    .language:       OpenCL C
    .language_version:
      - 2
      - 0
    .max_flat_workgroup_size: 512
    .name:           _Z11gemm_8phaseILi2ELi16ELi4ELi512ELi2048ELi1024ELi4EEvPKDF16_S1_PvS2_fPj
    .private_segment_fixed_size: 0
    .sgpr_count:     41
    .sgpr_spill_count: 0
    .symbol:         _Z11gemm_8phaseILi2ELi16ELi4ELi512ELi2048ELi1024ELi4EEvPKDF16_S1_PvS2_fPj.kd
    .uniform_work_group_size: 1
    .uses_dynamic_stack: false
    .vgpr_count:     236
    .vgpr_spill_count: 0
    .wavefront_size: 64
